# MoE gate/up set-up token lists loaded straight into LDS by LDS-DMA (one wait instead of a round trip per round); proj gate-tile epilogue loads its two bias vectors once instead of per row block
# speedup vs baseline: 1.0067x; 1.0067x over previous
.LBB0_229:
	s_lshl_b32 s52, s46, 2
	s_add_u32 s10, s12, 0x11400000
	s_addc_u32 s11, s13, 0
	s_add_u32 s12, s12, 0x400000
	s_addc_u32 s13, s13, 0
	s_lshl_b64 s[20:21], s[52:53], 2
	s_add_u32 s14, s0, s20
	s_addc_u32 s15, s1, s21
	s_add_u32 s2, s2, s20
	s_mov_b64 s[0:1], 0x80
	s_addc_u32 s3, s3, s21
	v_lshl_add_u64 v[10:11], v[10:11], 0, s[0:1]
	s_add_i32 m0, s37, 0x18000
	s_and_b32 s43, s18, 3
	s_waitcnt vmcnt(2)
	s_barrier
	global_load_lds_dwordx4 v[10:11], off
	v_lshl_add_u64 v[8:9], v[8:9], 0, s[0:1]
	s_add_i32 m0, s37, 0x1a000
	s_add_i32 s45, s37, 0x8000
	s_lshl_b32 s44, s16, 6
	s_lshl_b32 s18, s16, 13
	s_lshl_b32 s16, s43, 5
	s_lshl_b32 s19, s43, 12
	global_load_lds_dwordx4 v[8:9], off
	v_lshl_add_u64 v[4:5], v[4:5], 0, s[0:1]
	s_mov_b32 m0, s45
	s_add_i32 s46, s37, 0xa000
	global_load_lds_dwordx4 v[4:5], off
	v_lshl_add_u64 v[4:5], v[6:7], 0, s[0:1]
	s_add_u32 s0, s4, 0x20080
	s_mov_b32 m0, s46
	s_addc_u32 s1, s5, 0
	global_load_lds_dwordx4 v[4:5], off
	v_lshl_add_u64 v[4:5], s[0:1], 0, v[176:177]
	s_add_i32 m0, s37, 0x1c000
	v_and_b32_e32 v3, 15, v12
	global_load_lds_dwordx4 v[4:5], off
	v_lshl_add_u64 v[4:5], s[0:1], 0, v[172:173]
	s_add_i32 m0, s37, 0x1e000
	v_lshlrev_b32_e32 v7, 2, v12
	global_load_lds_dwordx4 v[4:5], off
	v_lshlrev_b32_e32 v4, 1, v12
	v_and_b32_e32 v4, 32, v4
	v_lshlrev_b32_e32 v5, 5, v12
	v_lshlrev_b32_e32 v6, 6, v3
	v_and_b32_e32 v7, 32, v7
	v_and_b32_e32 v5, 0x400, v5
	v_bitop3_b32 v4, v6, v7, v4 bitop3:0x36
	v_or3_b32 v6, v4, s18, v5
	v_or3_b32 v192, v4, s19, v5
	v_and_b32_e32 v249, 16, v0
	v_xor_b32_e32 v192, v192, v249
	v_add_u32_e32 v192, 0x10000, v192
	v_xor_b32_e32 v249, 16, v192
	v_lshlrev_b32_e32 v4, 13, v17
	v_and_b32_e32 v4, 0xffffc000, v4
	v_lshl_add_u32 v4, v16, 10, v4
	v_and_b32_e32 v5, 1, v17
	v_lshl_or_b32 v4, v5, 6, v4
	v_lshl_add_u32 v180, v18, 1, v4
	v_lshlrev_b32_e32 v4, 13, v13
	v_and_b32_e32 v4, 0xffffc000, v4
	v_readlane_b32 s0, v252, 48
	s_waitcnt vmcnt(6)
	v_lshl_add_u32 v4, v14, 10, v4
	v_and_b32_e32 v5, 1, v13
	v_readlane_b32 s1, v252, 49
	s_cmpk_lt_u32 s17, 0x100
	v_lshl_or_b32 v4, v5, 6, v4
	s_mov_b32 s33, s0
	v_readlane_b32 s0, v252, 44
	v_bfe_u32 v170, v12, 4, 2
	s_cselect_b64 s[18:19], -1, 0
	s_mov_b32 s17, s53
	v_mov_b32_e32 v181, v2
	v_lshl_add_u32 v182, v15, 1, v4
	v_mov_b32_e32 v183, v2
	s_mov_b32 s47, 0
	v_add_u32_e32 v193, 0, v6
	v_and_b32_e32 v250, 16, v0
	v_xor_b32_e32 v193, v193, v250
	v_xor_b32_e32 v250, 16, v193
	s_mov_b32 s28, s0
	s_barrier
	v_readlane_b32 s1, v252, 45
	s_branch .LBB0_232

.LBB0_235:
	s_add_u32 s4, s0, 0xfffe0080
	s_addc_u32 s5, s1, -1
	s_add_i32 s52, 0, 0x10000
	s_cmp_eq_u32 s51, 4
	s_cselect_b32 s7, s21, s5
	s_cselect_b32 s6, s29, s4
	s_cselect_b32 s5, s23, s50
	s_cselect_b32 s4, s48, s49
	s_add_i32 s53, 0, 0x14000
	ds_read_b128 v[20:23], v192
	ds_read_b128 v[24:27], v249
	ds_read_b128 v[28:31], v192 offset:2048
	ds_read_b128 v[32:35], v249 offset:2048
	ds_read_b128 v[4:7], v192 offset:16384
	ds_read_b128 v[8:11], v249 offset:16384
	ds_read_b128 v[12:15], v192 offset:18432
	ds_read_b128 v[16:19], v249 offset:18432
	v_lshl_add_u64 v[234:235], s[0:1], 0, v[180:181]
	s_add_i32 m0, s37, 0xc000
	ds_read_b128 v[184:187], v193
	ds_read_b128 v[188:191], v250
	ds_read_b128 v[194:197], v193 offset:2048
	ds_read_b128 v[198:201], v250 offset:2048
	ds_read_b128 v[202:205], v193 offset:4096
	ds_read_b128 v[206:209], v250 offset:4096
	ds_read_b128 v[226:229], v193 offset:6144
	ds_read_b128 v[230:233], v250 offset:6144
	global_load_lds_dwordx4 v[234:235], off
	v_lshl_add_u64 v[234:235], s[0:1], 0, v[182:183]
	s_add_i32 m0, s37, 0xe000
	s_nop 0
	global_load_lds_dwordx4 v[234:235], off
	s_waitcnt vmcnt(8)
	s_waitcnt lgkmcnt(0)
	s_barrier
	s_setprio 1
	s_waitcnt lgkmcnt(0)
	v_mfma_scale_f32_16x16x128_f8f6f4 v[96:99], v[20:27], v[184:191], v[96:99], v1, v1 op_sel_hi:[0,0,0]
	v_mfma_scale_f32_16x16x128_f8f6f4 v[92:95], v[28:35], v[184:191], v[92:95], v1, v1 op_sel_hi:[0,0,0]
	v_mfma_scale_f32_16x16x128_f8f6f4 v[88:91], v[20:27], v[194:201], v[88:91], v1, v1 op_sel_hi:[0,0,0]
	v_mfma_scale_f32_16x16x128_f8f6f4 v[84:87], v[28:35], v[194:201], v[84:87], v1, v1 op_sel_hi:[0,0,0]
	v_mfma_scale_f32_16x16x128_f8f6f4 v[80:83], v[20:27], v[202:209], v[80:83], v1, v1 op_sel_hi:[0,0,0]
	v_mfma_scale_f32_16x16x128_f8f6f4 v[76:79], v[28:35], v[202:209], v[76:79], v1, v1 op_sel_hi:[0,0,0]
	v_mfma_scale_f32_16x16x128_f8f6f4 v[72:75], v[20:27], v[226:233], v[72:75], v1, v1 op_sel_hi:[0,0,0]
	v_mfma_scale_f32_16x16x128_f8f6f4 v[68:71], v[28:35], v[226:233], v[68:71], v1, v1 op_sel_hi:[0,0,0]
	s_setprio 0
	s_setprio 1
	v_mfma_scale_f32_16x16x128_f8f6f4 v[160:163], v[4:11], v[184:191], v[160:163], v1, v1 op_sel_hi:[0,0,0]
	v_mfma_scale_f32_16x16x128_f8f6f4 v[156:159], v[12:19], v[184:191], v[156:159], v1, v1 op_sel_hi:[0,0,0]
	v_mfma_scale_f32_16x16x128_f8f6f4 v[152:155], v[4:11], v[194:201], v[152:155], v1, v1 op_sel_hi:[0,0,0]
	v_mfma_scale_f32_16x16x128_f8f6f4 v[148:151], v[12:19], v[194:201], v[148:151], v1, v1 op_sel_hi:[0,0,0]
	v_mfma_scale_f32_16x16x128_f8f6f4 v[144:147], v[4:11], v[202:209], v[144:147], v1, v1 op_sel_hi:[0,0,0]
	v_mfma_scale_f32_16x16x128_f8f6f4 v[140:143], v[12:19], v[202:209], v[140:143], v1, v1 op_sel_hi:[0,0,0]
	v_mfma_scale_f32_16x16x128_f8f6f4 v[136:139], v[4:11], v[226:233], v[136:139], v1, v1 op_sel_hi:[0,0,0]
	v_mfma_scale_f32_16x16x128_f8f6f4 v[132:135], v[12:19], v[226:233], v[132:135], v1, v1 op_sel_hi:[0,0,0]
	s_setprio 0
	s_barrier
	s_add_i32 s52, s52, s36
	v_lshl_add_u64 v[184:185], s[4:5], 0, v[176:177]
	s_mov_b32 m0, s52
	ds_read_b128 v[194:197], v193 offset:16384
	ds_read_b128 v[198:201], v250 offset:16384
	ds_read_b128 v[202:205], v193 offset:18432
	ds_read_b128 v[206:209], v250 offset:18432
	ds_read_b128 v[226:229], v193 offset:20480
	ds_read_b128 v[230:233], v250 offset:20480
	ds_read_b128 v[234:237], v193 offset:22528
	ds_read_b128 v[238:241], v250 offset:22528
	global_load_lds_dwordx4 v[184:185], off
	s_add_i32 m0, s52, 0x2000
	s_add_u32 s54, s4, 0x20000
	v_lshl_add_u64 v[186:187], s[4:5], 0, v[172:173]
	s_addc_u32 s55, s5, 0
	s_add_i32 s52, s53, s36
	global_load_lds_dwordx4 v[186:187], off
	v_lshl_add_u64 v[188:189], s[54:55], 0, v[176:177]
	s_mov_b32 m0, s52
	v_lshl_add_u64 v[190:191], s[6:7], 0, v[174:175]
	global_load_lds_dwordx4 v[188:189], off
	v_lshl_add_u64 v[188:189], s[54:55], 0, v[172:173]
	s_add_i32 m0, s52, 0x2000
	s_nop 0
	global_load_lds_dwordx4 v[188:189], off
	v_lshl_add_u64 v[188:189], s[6:7], 0, v[178:179]
	s_mov_b32 m0, s37
	s_nop 0
	global_load_lds_dwordx4 v[188:189], off
	s_mov_b32 m0, s38
	s_nop 0
	global_load_lds_dwordx4 v[190:191], off
	s_waitcnt vmcnt(8)
	s_waitcnt lgkmcnt(0)
	s_barrier
	s_setprio 1
	s_waitcnt lgkmcnt(0)
	v_mfma_scale_f32_16x16x128_f8f6f4 v[64:67], v[20:27], v[194:201], v[64:67], v1, v1 op_sel_hi:[0,0,0]
	v_mfma_scale_f32_16x16x128_f8f6f4 v[60:63], v[28:35], v[194:201], v[60:63], v1, v1 op_sel_hi:[0,0,0]
	v_mfma_scale_f32_16x16x128_f8f6f4 v[56:59], v[20:27], v[202:209], v[56:59], v1, v1 op_sel_hi:[0,0,0]
	v_mfma_scale_f32_16x16x128_f8f6f4 v[52:55], v[28:35], v[202:209], v[52:55], v1, v1 op_sel_hi:[0,0,0]
	v_mfma_scale_f32_16x16x128_f8f6f4 v[48:51], v[20:27], v[226:233], v[48:51], v1, v1 op_sel_hi:[0,0,0]
	v_mfma_scale_f32_16x16x128_f8f6f4 v[44:47], v[28:35], v[226:233], v[44:47], v1, v1 op_sel_hi:[0,0,0]
	v_mfma_scale_f32_16x16x128_f8f6f4 v[40:43], v[20:27], v[234:241], v[40:43], v1, v1 op_sel_hi:[0,0,0]
	v_mfma_scale_f32_16x16x128_f8f6f4 v[36:39], v[28:35], v[234:241], v[36:39], v1, v1 op_sel_hi:[0,0,0]
	s_setprio 0
	s_setprio 1
	v_mfma_scale_f32_16x16x128_f8f6f4 v[128:131], v[4:11], v[194:201], v[128:131], v1, v1 op_sel_hi:[0,0,0]
	v_mfma_scale_f32_16x16x128_f8f6f4 v[124:127], v[12:19], v[194:201], v[124:127], v1, v1 op_sel_hi:[0,0,0]
	v_mfma_scale_f32_16x16x128_f8f6f4 v[120:123], v[4:11], v[202:209], v[120:123], v1, v1 op_sel_hi:[0,0,0]
	v_mfma_scale_f32_16x16x128_f8f6f4 v[116:119], v[12:19], v[202:209], v[116:119], v1, v1 op_sel_hi:[0,0,0]
	v_mfma_scale_f32_16x16x128_f8f6f4 v[112:115], v[4:11], v[226:233], v[112:115], v1, v1 op_sel_hi:[0,0,0]
	v_mfma_scale_f32_16x16x128_f8f6f4 v[108:111], v[12:19], v[226:233], v[108:111], v1, v1 op_sel_hi:[0,0,0]
	v_mfma_scale_f32_16x16x128_f8f6f4 v[104:107], v[4:11], v[234:241], v[104:107], v1, v1 op_sel_hi:[0,0,0]
	v_mfma_scale_f32_16x16x128_f8f6f4 v[100:103], v[12:19], v[234:241], v[100:103], v1, v1 op_sel_hi:[0,0,0]
	s_setprio 0
	s_barrier
	s_add_i32 s52, 0, 0x18000
	s_add_i32 s53, 0, 0x1c000
	ds_read_b128 v[4:7], v192 offset:32768
	ds_read_b128 v[8:11], v249 offset:32768
	ds_read_b128 v[12:15], v192 offset:34816
	ds_read_b128 v[16:19], v249 offset:34816
	ds_read_b128 v[20:23], v192 offset:49152
	ds_read_b128 v[24:27], v249 offset:49152
	ds_read_b128 v[28:31], v192 offset:51200
	ds_read_b128 v[32:35], v249 offset:51200
	s_add_u32 s6, s6, 0x20000
	s_addc_u32 s7, s7, 0
	s_mov_b32 m0, s39
	v_lshl_add_u64 v[242:243], s[6:7], 0, v[178:179]
	ds_read_b128 v[194:197], v193 offset:32768
	ds_read_b128 v[198:201], v250 offset:32768
	ds_read_b128 v[202:205], v193 offset:34816
	ds_read_b128 v[206:209], v250 offset:34816
	ds_read_b128 v[226:229], v193 offset:36864
	ds_read_b128 v[230:233], v250 offset:36864
	ds_read_b128 v[234:237], v193 offset:38912
	ds_read_b128 v[238:241], v250 offset:38912
	global_load_lds_dwordx4 v[242:243], off
	v_lshl_add_u64 v[242:243], s[6:7], 0, v[174:175]
	s_mov_b32 m0, s42
	s_nop 0
	global_load_lds_dwordx4 v[242:243], off
	s_waitcnt vmcnt(8)
	s_waitcnt lgkmcnt(0)
	s_barrier
	s_setprio 1
	s_waitcnt lgkmcnt(0)
	v_mfma_scale_f32_16x16x128_f8f6f4 v[96:99], v[4:11], v[194:201], v[96:99], v1, v1 op_sel_hi:[0,0,0]
	v_mfma_scale_f32_16x16x128_f8f6f4 v[92:95], v[12:19], v[194:201], v[92:95], v1, v1 op_sel_hi:[0,0,0]
	v_mfma_scale_f32_16x16x128_f8f6f4 v[88:91], v[4:11], v[202:209], v[88:91], v1, v1 op_sel_hi:[0,0,0]
	v_mfma_scale_f32_16x16x128_f8f6f4 v[84:87], v[12:19], v[202:209], v[84:87], v1, v1 op_sel_hi:[0,0,0]
	v_mfma_scale_f32_16x16x128_f8f6f4 v[80:83], v[4:11], v[226:233], v[80:83], v1, v1 op_sel_hi:[0,0,0]
	v_mfma_scale_f32_16x16x128_f8f6f4 v[76:79], v[12:19], v[226:233], v[76:79], v1, v1 op_sel_hi:[0,0,0]
	v_mfma_scale_f32_16x16x128_f8f6f4 v[72:75], v[4:11], v[234:241], v[72:75], v1, v1 op_sel_hi:[0,0,0]
	v_mfma_scale_f32_16x16x128_f8f6f4 v[68:71], v[12:19], v[234:241], v[68:71], v1, v1 op_sel_hi:[0,0,0]
	s_setprio 0
	s_setprio 1
	v_mfma_scale_f32_16x16x128_f8f6f4 v[160:163], v[20:27], v[194:201], v[160:163], v1, v1 op_sel_hi:[0,0,0]
	v_mfma_scale_f32_16x16x128_f8f6f4 v[156:159], v[28:35], v[194:201], v[156:159], v1, v1 op_sel_hi:[0,0,0]
	v_mfma_scale_f32_16x16x128_f8f6f4 v[152:155], v[20:27], v[202:209], v[152:155], v1, v1 op_sel_hi:[0,0,0]
	v_mfma_scale_f32_16x16x128_f8f6f4 v[148:151], v[28:35], v[202:209], v[148:151], v1, v1 op_sel_hi:[0,0,0]
	v_mfma_scale_f32_16x16x128_f8f6f4 v[144:147], v[20:27], v[226:233], v[144:147], v1, v1 op_sel_hi:[0,0,0]
	v_mfma_scale_f32_16x16x128_f8f6f4 v[140:143], v[28:35], v[226:233], v[140:143], v1, v1 op_sel_hi:[0,0,0]
	v_mfma_scale_f32_16x16x128_f8f6f4 v[136:139], v[20:27], v[234:241], v[136:139], v1, v1 op_sel_hi:[0,0,0]
	v_mfma_scale_f32_16x16x128_f8f6f4 v[132:135], v[28:35], v[234:241], v[132:135], v1, v1 op_sel_hi:[0,0,0]
	s_setprio 0
	s_barrier
	s_add_i32 s6, s52, s36
	v_lshl_add_u64 v[184:185], v[184:185], 0, s[56:57]
	s_mov_b32 m0, s6
	ds_read_b128 v[194:197], v193 offset:49152
	ds_read_b128 v[198:201], v250 offset:49152
	ds_read_b128 v[202:205], v193 offset:51200
	ds_read_b128 v[206:209], v250 offset:51200
	ds_read_b128 v[226:229], v193 offset:53248
	ds_read_b128 v[230:233], v250 offset:53248
	ds_read_b128 v[234:237], v193 offset:55296
	ds_read_b128 v[238:241], v250 offset:55296
	global_load_lds_dwordx4 v[184:185], off
	s_add_i32 m0, s6, 0x2000
	s_add_u32 s4, s4, 0x20080
	v_lshl_add_u64 v[184:185], v[186:187], 0, s[56:57]
	s_addc_u32 s5, s5, 0
	s_add_i32 s6, s53, s36
	global_load_lds_dwordx4 v[184:185], off
	v_lshl_add_u64 v[184:185], s[4:5], 0, v[176:177]
	s_mov_b32 m0, s6
	s_nop 0
	global_load_lds_dwordx4 v[184:185], off
	v_lshl_add_u64 v[184:185], s[4:5], 0, v[172:173]
	s_add_i32 m0, s6, 0x2000
	s_nop 0
	global_load_lds_dwordx4 v[184:185], off
	v_lshl_add_u64 v[184:185], v[188:189], 0, s[56:57]
	s_mov_b32 m0, s45
	s_nop 0
	global_load_lds_dwordx4 v[184:185], off
	v_lshl_add_u64 v[184:185], v[190:191], 0, s[56:57]
	s_mov_b32 m0, s46
	s_nop 0
	global_load_lds_dwordx4 v[184:185], off
	s_waitcnt vmcnt(8)
	s_waitcnt lgkmcnt(0)
	s_barrier
	s_setprio 1
	s_waitcnt lgkmcnt(0)
	v_mfma_scale_f32_16x16x128_f8f6f4 v[64:67], v[4:11], v[194:201], v[64:67], v1, v1 op_sel_hi:[0,0,0]
	v_mfma_scale_f32_16x16x128_f8f6f4 v[60:63], v[12:19], v[194:201], v[60:63], v1, v1 op_sel_hi:[0,0,0]
	v_mfma_scale_f32_16x16x128_f8f6f4 v[56:59], v[4:11], v[202:209], v[56:59], v1, v1 op_sel_hi:[0,0,0]
	v_mfma_scale_f32_16x16x128_f8f6f4 v[52:55], v[12:19], v[202:209], v[52:55], v1, v1 op_sel_hi:[0,0,0]
	v_mfma_scale_f32_16x16x128_f8f6f4 v[48:51], v[4:11], v[226:233], v[48:51], v1, v1 op_sel_hi:[0,0,0]
	v_mfma_scale_f32_16x16x128_f8f6f4 v[44:47], v[12:19], v[226:233], v[44:47], v1, v1 op_sel_hi:[0,0,0]
	v_mfma_scale_f32_16x16x128_f8f6f4 v[40:43], v[4:11], v[234:241], v[40:43], v1, v1 op_sel_hi:[0,0,0]
	v_mfma_scale_f32_16x16x128_f8f6f4 v[36:39], v[12:19], v[234:241], v[36:39], v1, v1 op_sel_hi:[0,0,0]
	s_setprio 0
	s_setprio 1
	v_mfma_scale_f32_16x16x128_f8f6f4 v[128:131], v[20:27], v[194:201], v[128:131], v1, v1 op_sel_hi:[0,0,0]
	v_mfma_scale_f32_16x16x128_f8f6f4 v[124:127], v[28:35], v[194:201], v[124:127], v1, v1 op_sel_hi:[0,0,0]
	v_mfma_scale_f32_16x16x128_f8f6f4 v[120:123], v[20:27], v[202:209], v[120:123], v1, v1 op_sel_hi:[0,0,0]
	v_mfma_scale_f32_16x16x128_f8f6f4 v[116:119], v[28:35], v[202:209], v[116:119], v1, v1 op_sel_hi:[0,0,0]
	v_mfma_scale_f32_16x16x128_f8f6f4 v[112:115], v[20:27], v[226:233], v[112:115], v1, v1 op_sel_hi:[0,0,0]
	v_mfma_scale_f32_16x16x128_f8f6f4 v[108:111], v[28:35], v[226:233], v[108:111], v1, v1 op_sel_hi:[0,0,0]
	v_mfma_scale_f32_16x16x128_f8f6f4 v[104:107], v[20:27], v[234:241], v[104:107], v1, v1 op_sel_hi:[0,0,0]
	v_mfma_scale_f32_16x16x128_f8f6f4 v[100:103], v[28:35], v[234:241], v[100:103], v1, v1 op_sel_hi:[0,0,0]
	s_setprio 0
	s_barrier
	s_add_i32 s51, s51, 2
	s_add_u32 s0, s0, 0x100
	s_addc_u32 s1, s1, 0
	s_add_u32 s49, s49, 0x100
	s_addc_u32 s50, s50, 0
	s_cmp_gt_u32 s51, 5
	s_cbranch_scc0 .LBB0_235
	s_and_b64 vcc, exec, s[18:19]
	s_cbranch_vccz .LBB0_238
	s_barrier

.LBB0_337:
	s_and_b64 vcc, exec, s[0:1]
	s_cbranch_vccz .LBB0_336
	v_or_b32_e32 v4, s43, v10
	v_cmp_eq_u32_e32 vcc, 0, v4
	s_and_saveexec_b64 s[4:5], vcc
	s_cbranch_execz .LBB0_340
	global_load_dwordx4 v[164:167], v2, s[2:3]
	global_load_dwordx4 v[244:247], v2, s[14:15]
	s_mov_b32 s6, 0xbfb8aa3b
	s_mov_b32 s7, 0x3f2aaaab
	s_mov_b32 s0, 0x3ecc95a3
	s_mov_b32 s48, 0x3e9b6dac
	s_mov_b32 s50, 0x3f2aaada
	s_mov_b32 s52, 0x3f317218
	s_mov_b32 s54, 0xb102e308
	s_mov_b32 s21, 0x7f800000
	s_mov_b32 s23, 0x33800000
	s_mov_b32 s28, 0x3c800000
	s_waitcnt vmcnt(0)
	v_mov_b32_e32 v4, v164
	v_mov_b32_e32 v5, v165
	v_mov_b32_e32 v6, v166
	v_mov_b32_e32 v7, v167
	v_fmamk_f32 v8, v92, 0x3c800000, v4
	v_min_f32_e32 v4, 0, v8
	v_mul_f32_e64 v8, |v8|, s6
	v_exp_f32_e32 v15, v8
	v_fmamk_f32 v13, v93, 0x3c800000, v5
	v_min_f32_e32 v5, 0, v13
	v_mul_f32_e64 v13, |v13|, s6
	v_exp_f32_e32 v104, v13
	v_add_f32_e32 v10, 1.0, v15
	v_add_f32_e32 v8, -1.0, v10
	v_sub_f32_e32 v9, v8, v10
	v_add_f32_e32 v9, 1.0, v9
	v_sub_f32_e32 v8, v15, v8
	v_add_f32_e32 v13, 1.0, v104
	v_add_f32_e32 v11, v8, v9
	v_frexp_mant_f32_e32 v8, v10
	v_add_f32_e32 v17, -1.0, v13
	v_cmp_gt_f32_e32 vcc, s7, v8
	v_cvt_f64_f32_e32 v[8:9], v10
	v_sub_f32_e32 v18, v17, v13
	v_frexp_exp_i32_f64_e32 v8, v[8:9]
	v_add_f32_e32 v18, 1.0, v18
	v_sub_f32_e32 v17, v104, v17
	v_subbrev_co_u32_e32 v24, vcc, 0, v8, vcc
	v_add_f32_e32 v17, v17, v18
	v_frexp_mant_f32_e32 v18, v13
	v_cmp_gt_f32_e32 vcc, s7, v18
	v_cvt_f64_f32_e32 v[18:19], v13
	v_frexp_exp_i32_f64_e32 v18, v[18:19]
	v_subbrev_co_u32_e32 v25, vcc, 0, v18, vcc
	v_sub_u32_e32 v8, 0, v24
	v_sub_u32_e32 v18, 0, v25
	v_ldexp_f32 v12, v10, v8
	v_ldexp_f32 v13, v13, v18
	v_ldexp_f32 v17, v17, v18
	v_pk_add_f32 v[18:19], v[12:13], 1.0 op_sel_hi:[1,0]
	v_ldexp_f32 v16, v11, v8
	v_pk_add_f32 v[20:21], v[18:19], -1.0 op_sel_hi:[1,0]
	v_pk_add_f32 v[28:29], v[12:13], -1.0 op_sel_hi:[1,0]
	v_pk_add_f32 v[20:21], v[12:13], v[20:21] neg_lo:[0,1] neg_hi:[0,1]
	v_pk_add_f32 v[30:31], v[28:29], 1.0 op_sel_hi:[1,0]
	v_pk_add_f32 v[20:21], v[16:17], v[20:21]
	v_pk_add_f32 v[12:13], v[12:13], v[30:31] neg_lo:[0,1] neg_hi:[0,1]
	v_pk_add_f32 v[22:23], v[18:19], v[20:21]
	v_pk_add_f32 v[12:13], v[16:17], v[12:13]
	v_rcp_f32_e32 v26, v22
	v_rcp_f32_e32 v27, v23
	v_pk_add_f32 v[16:17], v[28:29], v[12:13]
	v_pk_add_f32 v[18:19], v[22:23], v[18:19] neg_lo:[0,1] neg_hi:[0,1]
	v_pk_add_f32 v[28:29], v[16:17], v[28:29] neg_lo:[0,1] neg_hi:[0,1]
	v_pk_add_f32 v[18:19], v[20:21], v[18:19] neg_lo:[0,1] neg_hi:[0,1]
	v_pk_mul_f32 v[20:21], v[16:17], v[26:27]
	v_pk_add_f32 v[12:13], v[12:13], v[28:29] neg_lo:[0,1] neg_hi:[0,1]
	v_pk_mul_f32 v[28:29], v[22:23], v[20:21]
	v_cmp_neq_f32_e32 vcc, s21, v15
	v_pk_fma_f32 v[30:31], v[20:21], v[22:23], v[28:29] neg_lo:[0,0,1] neg_hi:[0,0,1]
	v_pk_fma_f32 v[30:31], v[20:21], v[18:19], v[30:31]
	v_fmamk_f32 v6, v94, 0x3c800000, v6
	v_pk_add_f32 v[32:33], v[28:29], v[30:31]
	v_fmac_f32_e32 v7, 0x3c800000, v95
	v_pk_add_f32 v[34:35], v[16:17], v[32:33] neg_lo:[0,1] neg_hi:[0,1]
	v_pk_add_f32 v[28:29], v[32:33], v[28:29] neg_lo:[0,1] neg_hi:[0,1]
	v_pk_add_f32 v[16:17], v[16:17], v[34:35] neg_lo:[0,1] neg_hi:[0,1]
	v_mov_b32_e32 v8, v244
	v_mov_b32_e32 v9, v245
	v_mov_b32_e32 v10, v246
	v_mov_b32_e32 v11, v247
	v_pk_fma_f32 v[8:9], v[96:97], s[28:29], v[8:9] op_sel_hi:[1,0,1]
	v_pk_add_f32 v[16:17], v[16:17], v[32:33] neg_lo:[0,1] neg_hi:[0,1]
	v_pk_fma_f32 v[10:11], v[98:99], s[28:29], v[10:11] op_sel_hi:[1,0,1]
	v_pk_add_f32 v[12:13], v[12:13], v[16:17]
	v_pk_add_f32 v[16:17], v[28:29], v[30:31] neg_lo:[0,1] neg_hi:[0,1]
	s_nop 0
	v_pk_add_f32 v[12:13], v[16:17], v[12:13]
	s_nop 0
	v_pk_add_f32 v[16:17], v[34:35], v[12:13]
	s_nop 0
	v_pk_mul_f32 v[28:29], v[26:27], v[16:17]
	s_nop 0
	v_pk_mul_f32 v[30:31], v[22:23], v[28:29]
	s_nop 0
	v_pk_fma_f32 v[22:23], v[28:29], v[22:23], v[30:31] neg_lo:[0,0,1] neg_hi:[0,0,1]
	s_nop 0
	v_pk_fma_f32 v[18:19], v[28:29], v[18:19], v[22:23]
	v_pk_add_f32 v[22:23], v[34:35], v[16:17] neg_lo:[0,1] neg_hi:[0,1]
	s_nop 0
	v_pk_add_f32 v[12:13], v[12:13], v[22:23]
	v_pk_add_f32 v[22:23], v[30:31], v[18:19]
	s_nop 0
	v_pk_add_f32 v[32:33], v[16:17], v[22:23] neg_lo:[0,1] neg_hi:[0,1]
	v_pk_add_f32 v[30:31], v[22:23], v[30:31] neg_lo:[0,1] neg_hi:[0,1]
	v_pk_add_f32 v[16:17], v[16:17], v[32:33] neg_lo:[0,1] neg_hi:[0,1]
	s_nop 0
	v_pk_add_f32 v[16:17], v[16:17], v[22:23] neg_lo:[0,1] neg_hi:[0,1]
	s_nop 0
	v_pk_add_f32 v[12:13], v[12:13], v[16:17]
	v_pk_add_f32 v[16:17], v[30:31], v[18:19] neg_lo:[0,1] neg_hi:[0,1]
	s_nop 0
	v_pk_add_f32 v[12:13], v[16:17], v[12:13]
	v_pk_add_f32 v[16:17], v[20:21], v[28:29]
	v_pk_add_f32 v[12:13], v[32:33], v[12:13]
	v_pk_add_f32 v[18:19], v[16:17], v[20:21] neg_lo:[0,1] neg_hi:[0,1]
	v_pk_mul_f32 v[12:13], v[26:27], v[12:13]
	v_pk_add_f32 v[18:19], v[28:29], v[18:19] neg_lo:[0,1] neg_hi:[0,1]
	s_nop 0
	v_pk_add_f32 v[12:13], v[18:19], v[12:13]
	s_nop 0
	v_pk_add_f32 v[20:21], v[16:17], v[12:13]
	s_nop 0
	v_pk_add_f32 v[16:17], v[20:21], v[16:17] neg_lo:[0,1] neg_hi:[0,1]
	v_pk_mul_f32 v[22:23], v[20:21], v[20:21]
	v_pk_add_f32 v[16:17], v[12:13], v[16:17] neg_lo:[0,1] neg_hi:[0,1]
	v_mov_b64_e32 v[12:13], s[0:1]
	v_pk_fma_f32 v[26:27], v[22:23], s[48:49], v[12:13] op_sel_hi:[1,0,0]
	v_ldexp_f32 v18, v20, 1
	v_pk_fma_f32 v[28:29], v[22:23], v[26:27], s[50:51] op_sel_hi:[1,1,0]
	v_ldexp_f32 v19, v21, 1
	v_pk_mul_f32 v[20:21], v[20:21], v[22:23]
	v_cvt_f32_i32_e32 v23, v25
	v_cvt_f32_i32_e32 v22, v24
	v_pk_mul_f32 v[28:29], v[20:21], v[28:29]
	v_ldexp_f32 v31, v17, 1
	v_pk_add_f32 v[20:21], v[18:19], v[28:29]
	v_pk_mul_f32 v[26:27], v[22:23], s[52:53] op_sel_hi:[1,0]
	v_pk_add_f32 v[18:19], v[20:21], v[18:19] neg_lo:[0,1] neg_hi:[0,1]
	v_pk_fma_f32 v[24:25], v[22:23], s[52:53], v[26:27] op_sel_hi:[1,0,1] neg_lo:[0,0,1] neg_hi:[0,0,1]
	v_pk_add_f32 v[28:29], v[28:29], v[18:19] neg_lo:[0,1] neg_hi:[0,1]
	v_pk_fma_f32 v[22:23], v[22:23], s[54:55], v[24:25] op_sel_hi:[1,0,1]
	v_ldexp_f32 v16, v16, 1
	v_mov_b32_e32 v18, v26
	v_mov_b32_e32 v19, v29
	v_mov_b32_e32 v30, v22
	v_mov_b32_e32 v17, v31
	v_pk_add_f32 v[18:19], v[18:19], v[30:31]
	v_pk_add_f32 v[30:31], v[16:17], v[28:29]
	v_pk_add_f32 v[24:25], v[26:27], v[22:23]
	v_mov_b32_e32 v17, v31
	v_mov_b32_e32 v29, v21
	v_pk_add_f32 v[32:33], v[20:21], v[30:31]
	v_pk_add_f32 v[28:29], v[16:17], v[28:29]
	v_pk_add_f32 v[16:17], v[24:25], v[32:33]
	v_mov_b32_e32 v100, v32
	v_mov_b32_e32 v101, v17
	v_mov_b32_e32 v102, v20
	v_mov_b32_e32 v103, v25
	v_pk_add_f32 v[100:101], v[100:101], v[102:103] neg_lo:[0,1] neg_hi:[0,1]
	v_mov_b32_e32 v34, v16
	v_mov_b32_e32 v35, v25
	v_mov_b32_e32 v92, v24
	v_mov_b32_e32 v93, v27
	v_mov_b32_e32 v102, v24
	v_mov_b32_e32 v103, v17
	v_mov_b32_e32 v27, v101
	v_pk_add_f32 v[34:35], v[34:35], v[92:93] neg_lo:[0,1] neg_hi:[0,1]
	v_mov_b32_e32 v92, v32
	v_mov_b32_e32 v93, v23
	v_pk_add_f32 v[26:27], v[102:103], v[26:27] neg_lo:[0,1] neg_hi:[0,1]
	v_pk_add_f32 v[92:93], v[92:93], v[34:35] neg_lo:[0,1] neg_hi:[0,1]
	v_mov_b32_e32 v102, v26
	v_mov_b32_e32 v103, v35
	v_mov_b32_e32 v106, v16
	v_mov_b32_e32 v107, v33
	v_mov_b32_e32 v35, v21
	v_pk_add_f32 v[102:103], v[22:23], v[102:103] neg_lo:[0,1] neg_hi:[0,1]
	v_pk_add_f32 v[34:35], v[106:107], v[34:35] neg_lo:[0,1] neg_hi:[0,1]
	v_mov_b32_e32 v23, v25
	v_pk_add_f32 v[18:19], v[18:19], v[34:35] neg_lo:[0,1] neg_hi:[0,1]
	v_pk_add_f32 v[22:23], v[22:23], v[26:27] neg_lo:[0,1] neg_hi:[0,1]
	v_pk_add_f32 v[24:25], v[28:29], v[100:101] neg_lo:[0,1] neg_hi:[0,1]
	v_pk_add_f32 v[28:29], v[92:93], v[18:19]
	v_pk_add_f32 v[26:27], v[24:25], v[22:23]
	v_mov_b32_e32 v23, v93
	v_mov_b32_e32 v25, v19
	v_pk_add_f32 v[18:19], v[22:23], v[24:25]
	v_pk_add_f32 v[20:21], v[32:33], v[20:21] neg_lo:[0,1] neg_hi:[0,1]
	v_pk_add_f32 v[18:19], v[18:19], v[102:103] neg_lo:[0,1] neg_hi:[0,1]
	v_mov_b32_e32 v24, v26
	v_mov_b32_e32 v25, v29
	v_pk_add_f32 v[20:21], v[30:31], v[20:21] neg_lo:[0,1] neg_hi:[0,1]
	v_pk_add_f32 v[24:25], v[24:25], v[18:19] neg_lo:[0,1] neg_hi:[0,1]
	v_pk_add_f32 v[18:19], v[20:21], v[18:19] neg_lo:[0,1] neg_hi:[0,1]
	v_pk_add_f32 v[22:23], v[22:23], v[24:25] neg_lo:[0,1] neg_hi:[0,1]
	v_pk_add_f32 v[20:21], v[28:29], v[26:27]
	v_pk_add_f32 v[18:19], v[18:19], v[22:23]
	v_pk_add_f32 v[22:23], v[16:17], v[20:21]
	v_cmp_lt_f32_e64 s[0:1], |v104|, s23
	v_pk_add_f32 v[16:17], v[22:23], v[16:17] neg_lo:[0,1] neg_hi:[0,1]
	s_nop 0
	v_pk_add_f32 v[16:17], v[20:21], v[16:17] neg_lo:[0,1] neg_hi:[0,1]
	s_nop 0
	v_pk_add_f32 v[16:17], v[18:19], v[16:17]
	s_nop 0
	v_pk_add_f32 v[16:17], v[22:23], v[16:17]
	s_nop 0
	v_cndmask_b32_e32 v16, v214, v16, vcc
	v_cmp_neq_f32_e32 vcc, s21, v104
	s_nop 1
	v_cndmask_b32_e32 v17, v214, v17, vcc
	v_cmp_ngt_f32_e32 vcc, -1.0, v104
	s_nop 1
	v_cndmask_b32_e32 v17, v215, v17, vcc
	v_cmp_ngt_f32_e32 vcc, -1.0, v15
	s_nop 1
	v_cndmask_b32_e32 v16, v215, v16, vcc
	v_cmp_neq_f32_e32 vcc, -1.0, v15
	s_nop 1
	v_cndmask_b32_e32 v16, v216, v16, vcc
	v_cmp_neq_f32_e32 vcc, -1.0, v104
	s_nop 1
	v_cndmask_b32_e32 v17, v216, v17, vcc
	v_cmp_lt_f32_e64 vcc, |v15|, s23
	v_cndmask_b32_e64 v17, v17, v104, s[0:1]
	s_nop 0
	v_cndmask_b32_e32 v16, v16, v15, vcc
	v_pk_add_f32 v[4:5], v[4:5], v[16:17] neg_lo:[0,1] neg_hi:[0,1]
	v_min_f32_e32 v16, 0, v6
	v_mul_f32_e64 v6, |v6|, s6
	v_exp_f32_e32 v15, v6
	s_nop 0
	v_add_f32_e32 v6, 1.0, v15
	v_add_f32_e32 v17, -1.0, v6
	v_sub_f32_e32 v18, v17, v6
	v_add_f32_e32 v18, 1.0, v18
	v_sub_f32_e32 v17, v15, v17
	v_add_f32_e32 v17, v17, v18
	v_frexp_mant_f32_e32 v18, v6
	v_cmp_gt_f32_e32 vcc, s7, v18
	v_cvt_f64_f32_e32 v[18:19], v6
	v_frexp_exp_i32_f64_e32 v18, v[18:19]
	v_subbrev_co_u32_e32 v92, vcc, 0, v18, vcc
	v_sub_u32_e32 v18, 0, v92
	v_ldexp_f32 v6, v6, v18
	v_ldexp_f32 v18, v17, v18
	v_min_f32_e32 v17, 0, v7
	v_mul_f32_e64 v7, |v7|, s6
	v_exp_f32_e32 v100, v7
	s_nop 0
	v_add_f32_e32 v7, 1.0, v100
	v_add_f32_e32 v19, -1.0, v7
	v_sub_f32_e32 v20, v19, v7
	v_add_f32_e32 v20, 1.0, v20
	v_sub_f32_e32 v19, v100, v19
	v_add_f32_e32 v19, v19, v20
	v_frexp_mant_f32_e32 v20, v7
	v_cmp_gt_f32_e32 vcc, s7, v20
	v_cvt_f64_f32_e32 v[20:21], v7
	v_frexp_exp_i32_f64_e32 v20, v[20:21]
	v_subbrev_co_u32_e32 v93, vcc, 0, v20, vcc
	v_sub_u32_e32 v20, 0, v93
	v_ldexp_f32 v7, v7, v20
	v_ldexp_f32 v19, v19, v20
	v_pk_add_f32 v[20:21], v[6:7], 1.0 op_sel_hi:[1,0]
	v_pk_add_f32 v[28:29], v[6:7], -1.0 op_sel_hi:[1,0]
	v_pk_add_f32 v[22:23], v[20:21], -1.0 op_sel_hi:[1,0]
	v_pk_add_f32 v[30:31], v[28:29], 1.0 op_sel_hi:[1,0]
	v_pk_add_f32 v[22:23], v[6:7], v[22:23] neg_lo:[0,1] neg_hi:[0,1]
	v_pk_add_f32 v[6:7], v[6:7], v[30:31] neg_lo:[0,1] neg_hi:[0,1]
	v_pk_add_f32 v[22:23], v[18:19], v[22:23]
	v_pk_add_f32 v[6:7], v[18:19], v[6:7]
	v_pk_add_f32 v[24:25], v[20:21], v[22:23]
	v_pk_add_f32 v[18:19], v[28:29], v[6:7]
	v_rcp_f32_e32 v26, v24
	v_rcp_f32_e32 v27, v25
	v_pk_add_f32 v[20:21], v[24:25], v[20:21] neg_lo:[0,1] neg_hi:[0,1]
	v_pk_add_f32 v[28:29], v[18:19], v[28:29] neg_lo:[0,1] neg_hi:[0,1]
	v_pk_add_f32 v[20:21], v[22:23], v[20:21] neg_lo:[0,1] neg_hi:[0,1]
	v_pk_mul_f32 v[22:23], v[18:19], v[26:27]
	v_pk_add_f32 v[6:7], v[6:7], v[28:29] neg_lo:[0,1] neg_hi:[0,1]
	v_pk_mul_f32 v[28:29], v[24:25], v[22:23]
	v_cmp_neq_f32_e32 vcc, s21, v15
	v_pk_fma_f32 v[30:31], v[22:23], v[24:25], v[28:29] neg_lo:[0,0,1] neg_hi:[0,0,1]
	v_cmp_lt_f32_e64 s[0:1], |v100|, s23
	v_pk_fma_f32 v[30:31], v[22:23], v[20:21], v[30:31]
	s_nop 0
	v_pk_add_f32 v[32:33], v[28:29], v[30:31]
	s_nop 0
	v_pk_add_f32 v[34:35], v[18:19], v[32:33] neg_lo:[0,1] neg_hi:[0,1]
	v_pk_add_f32 v[28:29], v[32:33], v[28:29] neg_lo:[0,1] neg_hi:[0,1]
	v_pk_add_f32 v[18:19], v[18:19], v[34:35] neg_lo:[0,1] neg_hi:[0,1]
	s_nop 0
	v_pk_add_f32 v[18:19], v[18:19], v[32:33] neg_lo:[0,1] neg_hi:[0,1]
	s_nop 0
	v_pk_add_f32 v[6:7], v[6:7], v[18:19]
	v_pk_add_f32 v[18:19], v[28:29], v[30:31] neg_lo:[0,1] neg_hi:[0,1]
	s_nop 0
	v_pk_add_f32 v[6:7], v[18:19], v[6:7]
	s_nop 0
	v_pk_add_f32 v[18:19], v[34:35], v[6:7]
	s_nop 0
	v_pk_mul_f32 v[28:29], v[26:27], v[18:19]
	s_nop 0
	v_pk_mul_f32 v[30:31], v[24:25], v[28:29]
	s_nop 0
	v_pk_fma_f32 v[24:25], v[28:29], v[24:25], v[30:31] neg_lo:[0,0,1] neg_hi:[0,0,1]
	s_nop 0
	v_pk_fma_f32 v[20:21], v[28:29], v[20:21], v[24:25]
	v_pk_add_f32 v[24:25], v[34:35], v[18:19] neg_lo:[0,1] neg_hi:[0,1]
	s_nop 0
	v_pk_add_f32 v[6:7], v[6:7], v[24:25]
	v_pk_add_f32 v[24:25], v[30:31], v[20:21]
	s_nop 0
	v_pk_add_f32 v[32:33], v[18:19], v[24:25] neg_lo:[0,1] neg_hi:[0,1]
	v_pk_add_f32 v[30:31], v[24:25], v[30:31] neg_lo:[0,1] neg_hi:[0,1]
	v_pk_add_f32 v[18:19], v[18:19], v[32:33] neg_lo:[0,1] neg_hi:[0,1]
	s_nop 0
	v_pk_add_f32 v[18:19], v[18:19], v[24:25] neg_lo:[0,1] neg_hi:[0,1]
	s_nop 0
	v_pk_add_f32 v[6:7], v[6:7], v[18:19]
	v_pk_add_f32 v[18:19], v[30:31], v[20:21] neg_lo:[0,1] neg_hi:[0,1]
	s_nop 0
	v_pk_add_f32 v[6:7], v[18:19], v[6:7]
	v_pk_add_f32 v[18:19], v[22:23], v[28:29]
	v_pk_add_f32 v[6:7], v[32:33], v[6:7]
	v_pk_add_f32 v[20:21], v[18:19], v[22:23] neg_lo:[0,1] neg_hi:[0,1]
	v_pk_mul_f32 v[6:7], v[26:27], v[6:7]
	v_pk_add_f32 v[20:21], v[28:29], v[20:21] neg_lo:[0,1] neg_hi:[0,1]
	s_nop 0
	v_pk_add_f32 v[6:7], v[20:21], v[6:7]
	s_nop 0
	v_pk_add_f32 v[20:21], v[18:19], v[6:7]
	s_nop 0
	v_pk_mul_f32 v[22:23], v[20:21], v[20:21]
	v_pk_add_f32 v[18:19], v[20:21], v[18:19] neg_lo:[0,1] neg_hi:[0,1]
	v_pk_fma_f32 v[24:25], v[22:23], s[48:49], v[12:13] op_sel_hi:[1,0,0]
	v_pk_add_f32 v[6:7], v[6:7], v[18:19] neg_lo:[0,1] neg_hi:[0,1]
	v_ldexp_f32 v18, v20, 1
	v_pk_fma_f32 v[24:25], v[22:23], v[24:25], s[50:51] op_sel_hi:[1,1,0]
	v_ldexp_f32 v19, v21, 1
	v_pk_mul_f32 v[20:21], v[20:21], v[22:23]
	v_cvt_f32_i32_e32 v23, v93
	v_cvt_f32_i32_e32 v22, v92
	v_pk_mul_f32 v[20:21], v[20:21], v[24:25]
	v_ldexp_f32 v27, v7, 1
	v_pk_add_f32 v[24:25], v[18:19], v[20:21]
	v_pk_mul_f32 v[28:29], v[22:23], s[52:53] op_sel_hi:[1,0]
	v_pk_add_f32 v[18:19], v[24:25], v[18:19] neg_lo:[0,1] neg_hi:[0,1]
	v_pk_fma_f32 v[30:31], v[22:23], s[52:53], v[28:29] op_sel_hi:[1,0,1] neg_lo:[0,0,1] neg_hi:[0,0,1]
	v_pk_add_f32 v[18:19], v[20:21], v[18:19] neg_lo:[0,1] neg_hi:[0,1]
	v_pk_fma_f32 v[22:23], v[22:23], s[54:55], v[30:31] op_sel_hi:[1,0,1]
	v_ldexp_f32 v6, v6, 1
	v_mov_b32_e32 v20, v28
	v_mov_b32_e32 v21, v19
	v_mov_b32_e32 v26, v22
	v_mov_b32_e32 v7, v27
	v_pk_add_f32 v[20:21], v[20:21], v[26:27]
	v_pk_add_f32 v[26:27], v[6:7], v[18:19]
	v_mov_b32_e32 v19, v25
	v_mov_b32_e32 v7, v27
	v_pk_add_f32 v[30:31], v[28:29], v[22:23]
	v_pk_add_f32 v[6:7], v[6:7], v[18:19]
	v_pk_add_f32 v[18:19], v[24:25], v[26:27]
	v_mov_b32_e32 v96, v24
	v_pk_add_f32 v[32:33], v[30:31], v[18:19]
	v_mov_b32_e32 v94, v18
	v_mov_b32_e32 v95, v33
	v_mov_b32_e32 v97, v31
	v_pk_add_f32 v[94:95], v[94:95], v[96:97] neg_lo:[0,1] neg_hi:[0,1]
	v_mov_b32_e32 v34, v32
	v_mov_b32_e32 v35, v31
	v_mov_b32_e32 v92, v30
	v_mov_b32_e32 v93, v29
	v_mov_b32_e32 v96, v30
	v_mov_b32_e32 v97, v33
	v_mov_b32_e32 v29, v95
	v_pk_add_f32 v[34:35], v[34:35], v[92:93] neg_lo:[0,1] neg_hi:[0,1]
	v_mov_b32_e32 v92, v18
	v_mov_b32_e32 v93, v23
	v_pk_add_f32 v[28:29], v[96:97], v[28:29] neg_lo:[0,1] neg_hi:[0,1]
	v_pk_add_f32 v[92:93], v[92:93], v[34:35] neg_lo:[0,1] neg_hi:[0,1]
	v_mov_b32_e32 v96, v28
	v_mov_b32_e32 v97, v35
	v_mov_b32_e32 v98, v32
	v_mov_b32_e32 v99, v19
	v_mov_b32_e32 v35, v25
	v_pk_add_f32 v[96:97], v[22:23], v[96:97] neg_lo:[0,1] neg_hi:[0,1]
	v_pk_add_f32 v[34:35], v[98:99], v[34:35] neg_lo:[0,1] neg_hi:[0,1]
	v_mov_b32_e32 v23, v31
	v_pk_add_f32 v[20:21], v[20:21], v[34:35] neg_lo:[0,1] neg_hi:[0,1]
	v_pk_add_f32 v[22:23], v[22:23], v[28:29] neg_lo:[0,1] neg_hi:[0,1]
	v_pk_add_f32 v[6:7], v[6:7], v[94:95] neg_lo:[0,1] neg_hi:[0,1]
	v_pk_add_f32 v[18:19], v[18:19], v[24:25] neg_lo:[0,1] neg_hi:[0,1]
	v_pk_add_f32 v[24:25], v[6:7], v[22:23]
	v_mov_b32_e32 v23, v93
	v_mov_b32_e32 v7, v21
	v_pk_add_f32 v[18:19], v[26:27], v[18:19] neg_lo:[0,1] neg_hi:[0,1]
	v_pk_add_f32 v[26:27], v[92:93], v[20:21]
	v_pk_add_f32 v[6:7], v[22:23], v[6:7]
	v_mov_b32_e32 v20, v24
	v_pk_add_f32 v[6:7], v[6:7], v[96:97] neg_lo:[0,1] neg_hi:[0,1]
	v_mov_b32_e32 v21, v27
	v_pk_add_f32 v[20:21], v[20:21], v[6:7] neg_lo:[0,1] neg_hi:[0,1]
	v_pk_add_f32 v[6:7], v[18:19], v[6:7] neg_lo:[0,1] neg_hi:[0,1]
	v_pk_add_f32 v[20:21], v[22:23], v[20:21] neg_lo:[0,1] neg_hi:[0,1]
	v_pk_add_f32 v[18:19], v[26:27], v[24:25]
	v_pk_add_f32 v[6:7], v[6:7], v[20:21]
	v_pk_add_f32 v[20:21], v[32:33], v[18:19]
	s_nop 0
	v_pk_add_f32 v[22:23], v[20:21], v[32:33] neg_lo:[0,1] neg_hi:[0,1]
	s_nop 0
	v_pk_add_f32 v[18:19], v[18:19], v[22:23] neg_lo:[0,1] neg_hi:[0,1]
	s_nop 0
	v_pk_add_f32 v[6:7], v[6:7], v[18:19]
	s_nop 0
	v_pk_add_f32 v[6:7], v[20:21], v[6:7]
	s_nop 0
	v_cndmask_b32_e32 v6, v214, v6, vcc
	v_cmp_neq_f32_e32 vcc, s21, v100
	s_nop 1
	v_cndmask_b32_e32 v7, v214, v7, vcc
	v_cmp_ngt_f32_e32 vcc, -1.0, v100
	s_nop 1
	v_cndmask_b32_e32 v7, v215, v7, vcc
	v_cmp_ngt_f32_e32 vcc, -1.0, v15
	s_nop 1
	v_cndmask_b32_e32 v6, v215, v6, vcc
	v_cmp_neq_f32_e32 vcc, -1.0, v15
	s_nop 1
	v_cndmask_b32_e32 v6, v216, v6, vcc
	v_cmp_neq_f32_e32 vcc, -1.0, v100
	s_nop 1
	v_cndmask_b32_e32 v7, v216, v7, vcc
	v_cmp_lt_f32_e64 vcc, |v15|, s23
	v_cndmask_b32_e64 v7, v7, v100, s[0:1]
	s_nop 0
	v_cndmask_b32_e32 v6, v6, v15, vcc
	v_ashrrev_i32_e32 v15, 31, v14
	v_lshlrev_b64 v[14:15], 5, v[14:15]
	v_lshl_add_u64 v[14:15], s[12:13], 0, v[14:15]
	v_pk_add_f32 v[6:7], v[16:17], v[6:7] neg_lo:[0,1] neg_hi:[0,1]
	global_store_dwordx4 v[14:15], v[8:11], off
	global_store_dwordx4 v[14:15], v[4:7], off offset:16
	s_nop 1
	v_mov_b32_e32 v4, v164
	v_mov_b32_e32 v5, v165
	v_mov_b32_e32 v6, v166
	v_mov_b32_e32 v7, v167
	v_fmamk_f32 v8, v84, 0x3c800000, v4
	v_min_f32_e32 v4, 0, v8
	v_mul_f32_e64 v8, |v8|, s6
	v_exp_f32_e32 v98, v8
	v_fmamk_f32 v17, v85, 0x3c800000, v5
	v_min_f32_e32 v5, 0, v17
	v_mul_f32_e64 v17, |v17|, s6
	v_exp_f32_e32 v99, v17
	v_add_f32_e32 v10, 1.0, v98
	v_add_f32_e32 v8, -1.0, v10
	v_sub_f32_e32 v9, v8, v10
	v_add_f32_e32 v9, 1.0, v9
	v_sub_f32_e32 v8, v98, v8
	v_add_f32_e32 v17, 1.0, v99
	v_add_f32_e32 v11, v8, v9
	v_frexp_mant_f32_e32 v8, v10
	v_add_f32_e32 v19, -1.0, v17
	v_cmp_gt_f32_e32 vcc, s7, v8
	v_cvt_f64_f32_e32 v[8:9], v10
	v_sub_f32_e32 v20, v19, v17
	v_frexp_exp_i32_f64_e32 v8, v[8:9]
	v_add_f32_e32 v20, 1.0, v20
	v_sub_f32_e32 v19, v99, v19
	v_subbrev_co_u32_e32 v84, vcc, 0, v8, vcc
	v_add_f32_e32 v19, v19, v20
	v_frexp_mant_f32_e32 v20, v17
	v_cmp_gt_f32_e32 vcc, s7, v20
	v_cvt_f64_f32_e32 v[20:21], v17
	v_frexp_exp_i32_f64_e32 v20, v[20:21]
	v_subbrev_co_u32_e32 v85, vcc, 0, v20, vcc
	v_sub_u32_e32 v8, 0, v84
	v_sub_u32_e32 v20, 0, v85
	v_ldexp_f32 v16, v10, v8
	v_ldexp_f32 v17, v17, v20
	v_ldexp_f32 v19, v19, v20
	v_pk_add_f32 v[20:21], v[16:17], 1.0 op_sel_hi:[1,0]
	v_ldexp_f32 v18, v11, v8
	v_pk_add_f32 v[22:23], v[20:21], -1.0 op_sel_hi:[1,0]
	v_pk_add_f32 v[28:29], v[16:17], -1.0 op_sel_hi:[1,0]
	v_pk_add_f32 v[22:23], v[16:17], v[22:23] neg_lo:[0,1] neg_hi:[0,1]
	v_pk_add_f32 v[30:31], v[28:29], 1.0 op_sel_hi:[1,0]
	v_pk_add_f32 v[22:23], v[18:19], v[22:23]
	v_pk_add_f32 v[16:17], v[16:17], v[30:31] neg_lo:[0,1] neg_hi:[0,1]
	v_pk_add_f32 v[24:25], v[20:21], v[22:23]
	v_pk_add_f32 v[16:17], v[18:19], v[16:17]
	v_rcp_f32_e32 v26, v24
	v_rcp_f32_e32 v27, v25
	v_pk_add_f32 v[18:19], v[28:29], v[16:17]
	v_pk_add_f32 v[20:21], v[24:25], v[20:21] neg_lo:[0,1] neg_hi:[0,1]
	v_pk_add_f32 v[28:29], v[18:19], v[28:29] neg_lo:[0,1] neg_hi:[0,1]
	v_pk_add_f32 v[20:21], v[22:23], v[20:21] neg_lo:[0,1] neg_hi:[0,1]
	v_pk_mul_f32 v[22:23], v[18:19], v[26:27]
	v_pk_add_f32 v[16:17], v[16:17], v[28:29] neg_lo:[0,1] neg_hi:[0,1]
	v_pk_mul_f32 v[28:29], v[24:25], v[22:23]
	v_cmp_neq_f32_e32 vcc, s21, v98
	v_pk_fma_f32 v[30:31], v[22:23], v[24:25], v[28:29] neg_lo:[0,0,1] neg_hi:[0,0,1]
	v_pk_fma_f32 v[30:31], v[22:23], v[20:21], v[30:31]
	v_cmp_lt_f32_e64 s[0:1], |v99|, s23
	v_pk_add_f32 v[32:33], v[28:29], v[30:31]
	v_fmamk_f32 v6, v86, 0x3c800000, v6
	v_pk_add_f32 v[34:35], v[18:19], v[32:33] neg_lo:[0,1] neg_hi:[0,1]
	v_pk_add_f32 v[28:29], v[32:33], v[28:29] neg_lo:[0,1] neg_hi:[0,1]
	v_pk_add_f32 v[18:19], v[18:19], v[34:35] neg_lo:[0,1] neg_hi:[0,1]
	v_fmac_f32_e32 v7, 0x3c800000, v87
	v_pk_add_f32 v[18:19], v[18:19], v[32:33] neg_lo:[0,1] neg_hi:[0,1]
	v_mov_b32_e32 v8, v244
	v_mov_b32_e32 v9, v245
	v_mov_b32_e32 v10, v246
	v_mov_b32_e32 v11, v247
	v_pk_fma_f32 v[8:9], v[88:89], s[28:29], v[8:9] op_sel_hi:[1,0,1]
	v_pk_add_f32 v[16:17], v[16:17], v[18:19]
	v_pk_add_f32 v[18:19], v[28:29], v[30:31] neg_lo:[0,1] neg_hi:[0,1]
	v_pk_fma_f32 v[10:11], v[90:91], s[28:29], v[10:11] op_sel_hi:[1,0,1]
	v_pk_add_f32 v[16:17], v[18:19], v[16:17]
	s_nop 0
	v_pk_add_f32 v[18:19], v[34:35], v[16:17]
	s_nop 0
	v_pk_mul_f32 v[28:29], v[26:27], v[18:19]
	s_nop 0
	v_pk_mul_f32 v[30:31], v[24:25], v[28:29]
	s_nop 0
	v_pk_fma_f32 v[24:25], v[28:29], v[24:25], v[30:31] neg_lo:[0,0,1] neg_hi:[0,0,1]
	s_nop 0
	v_pk_fma_f32 v[20:21], v[28:29], v[20:21], v[24:25]
	v_pk_add_f32 v[24:25], v[34:35], v[18:19] neg_lo:[0,1] neg_hi:[0,1]
	s_nop 0
	v_pk_add_f32 v[16:17], v[16:17], v[24:25]
	v_pk_add_f32 v[24:25], v[30:31], v[20:21]
	s_nop 0
	v_pk_add_f32 v[32:33], v[18:19], v[24:25] neg_lo:[0,1] neg_hi:[0,1]
	v_pk_add_f32 v[30:31], v[24:25], v[30:31] neg_lo:[0,1] neg_hi:[0,1]
	v_pk_add_f32 v[18:19], v[18:19], v[32:33] neg_lo:[0,1] neg_hi:[0,1]
	s_nop 0
	v_pk_add_f32 v[18:19], v[18:19], v[24:25] neg_lo:[0,1] neg_hi:[0,1]
	s_nop 0
	v_pk_add_f32 v[16:17], v[16:17], v[18:19]
	v_pk_add_f32 v[18:19], v[30:31], v[20:21] neg_lo:[0,1] neg_hi:[0,1]
	s_nop 0
	v_pk_add_f32 v[16:17], v[18:19], v[16:17]
	v_pk_add_f32 v[18:19], v[22:23], v[28:29]
	v_pk_add_f32 v[16:17], v[32:33], v[16:17]
	v_pk_add_f32 v[20:21], v[18:19], v[22:23] neg_lo:[0,1] neg_hi:[0,1]
	v_pk_mul_f32 v[16:17], v[26:27], v[16:17]
	v_pk_add_f32 v[20:21], v[28:29], v[20:21] neg_lo:[0,1] neg_hi:[0,1]
	s_nop 0
	v_pk_add_f32 v[16:17], v[20:21], v[16:17]
	s_nop 0
	v_pk_add_f32 v[20:21], v[18:19], v[16:17]
	s_nop 0
	v_pk_mul_f32 v[22:23], v[20:21], v[20:21]
	v_pk_add_f32 v[18:19], v[20:21], v[18:19] neg_lo:[0,1] neg_hi:[0,1]
	v_pk_fma_f32 v[24:25], v[22:23], s[48:49], v[12:13] op_sel_hi:[1,0,0]
	v_pk_add_f32 v[16:17], v[16:17], v[18:19] neg_lo:[0,1] neg_hi:[0,1]
	v_ldexp_f32 v18, v20, 1
	v_pk_fma_f32 v[24:25], v[22:23], v[24:25], s[50:51] op_sel_hi:[1,1,0]
	v_ldexp_f32 v19, v21, 1
	v_pk_mul_f32 v[20:21], v[20:21], v[22:23]
	v_cvt_f32_i32_e32 v23, v85
	v_cvt_f32_i32_e32 v22, v84
	v_pk_mul_f32 v[20:21], v[20:21], v[24:25]
	v_ldexp_f32 v27, v17, 1
	v_pk_add_f32 v[24:25], v[18:19], v[20:21]
	v_pk_mul_f32 v[28:29], v[22:23], s[52:53] op_sel_hi:[1,0]
	v_pk_add_f32 v[18:19], v[24:25], v[18:19] neg_lo:[0,1] neg_hi:[0,1]
	v_pk_fma_f32 v[30:31], v[22:23], s[52:53], v[28:29] op_sel_hi:[1,0,1] neg_lo:[0,0,1] neg_hi:[0,0,1]
	v_pk_add_f32 v[18:19], v[20:21], v[18:19] neg_lo:[0,1] neg_hi:[0,1]
	v_pk_fma_f32 v[22:23], v[22:23], s[54:55], v[30:31] op_sel_hi:[1,0,1]
	v_ldexp_f32 v16, v16, 1
	v_mov_b32_e32 v20, v28
	v_mov_b32_e32 v21, v19
	v_mov_b32_e32 v26, v22
	v_mov_b32_e32 v17, v27
	v_pk_add_f32 v[20:21], v[20:21], v[26:27]
	v_pk_add_f32 v[26:27], v[16:17], v[18:19]
	v_mov_b32_e32 v19, v25
	v_mov_b32_e32 v17, v27
	v_pk_add_f32 v[30:31], v[28:29], v[22:23]
	v_pk_add_f32 v[16:17], v[16:17], v[18:19]
	v_pk_add_f32 v[18:19], v[24:25], v[26:27]
	v_mov_b32_e32 v94, v24
	v_pk_add_f32 v[32:33], v[30:31], v[18:19]
	v_mov_b32_e32 v92, v18
	v_mov_b32_e32 v93, v33
	v_mov_b32_e32 v95, v31
	v_pk_add_f32 v[92:93], v[92:93], v[94:95] neg_lo:[0,1] neg_hi:[0,1]
	v_mov_b32_e32 v34, v32
	v_mov_b32_e32 v35, v31
	v_mov_b32_e32 v84, v30
	v_mov_b32_e32 v85, v29
	v_mov_b32_e32 v94, v30
	v_mov_b32_e32 v95, v33
	v_mov_b32_e32 v29, v93
	v_pk_add_f32 v[34:35], v[34:35], v[84:85] neg_lo:[0,1] neg_hi:[0,1]
	v_mov_b32_e32 v84, v18
	v_mov_b32_e32 v85, v23
	v_pk_add_f32 v[28:29], v[94:95], v[28:29] neg_lo:[0,1] neg_hi:[0,1]
	v_pk_add_f32 v[84:85], v[84:85], v[34:35] neg_lo:[0,1] neg_hi:[0,1]
	v_mov_b32_e32 v94, v28
	v_mov_b32_e32 v95, v35
	v_mov_b32_e32 v96, v32
	v_mov_b32_e32 v97, v19
	v_mov_b32_e32 v35, v25
	v_pk_add_f32 v[94:95], v[22:23], v[94:95] neg_lo:[0,1] neg_hi:[0,1]
	v_pk_add_f32 v[34:35], v[96:97], v[34:35] neg_lo:[0,1] neg_hi:[0,1]
	v_mov_b32_e32 v23, v31
	v_pk_add_f32 v[20:21], v[20:21], v[34:35] neg_lo:[0,1] neg_hi:[0,1]
	v_pk_add_f32 v[22:23], v[22:23], v[28:29] neg_lo:[0,1] neg_hi:[0,1]
	v_pk_add_f32 v[16:17], v[16:17], v[92:93] neg_lo:[0,1] neg_hi:[0,1]
	v_pk_add_f32 v[18:19], v[18:19], v[24:25] neg_lo:[0,1] neg_hi:[0,1]
	v_pk_add_f32 v[24:25], v[16:17], v[22:23]
	v_mov_b32_e32 v23, v85
	v_mov_b32_e32 v17, v21
	v_pk_add_f32 v[18:19], v[26:27], v[18:19] neg_lo:[0,1] neg_hi:[0,1]
	v_pk_add_f32 v[26:27], v[84:85], v[20:21]
	v_pk_add_f32 v[16:17], v[22:23], v[16:17]
	v_mov_b32_e32 v20, v24
	v_pk_add_f32 v[16:17], v[16:17], v[94:95] neg_lo:[0,1] neg_hi:[0,1]
	v_mov_b32_e32 v21, v27
	v_pk_add_f32 v[20:21], v[20:21], v[16:17] neg_lo:[0,1] neg_hi:[0,1]
	v_pk_add_f32 v[16:17], v[18:19], v[16:17] neg_lo:[0,1] neg_hi:[0,1]
	v_pk_add_f32 v[20:21], v[22:23], v[20:21] neg_lo:[0,1] neg_hi:[0,1]
	v_pk_add_f32 v[18:19], v[26:27], v[24:25]
	v_pk_add_f32 v[16:17], v[16:17], v[20:21]
	v_pk_add_f32 v[20:21], v[32:33], v[18:19]
	s_nop 0
	v_pk_add_f32 v[22:23], v[20:21], v[32:33] neg_lo:[0,1] neg_hi:[0,1]
	s_nop 0
	v_pk_add_f32 v[18:19], v[18:19], v[22:23] neg_lo:[0,1] neg_hi:[0,1]
	s_nop 0
	v_pk_add_f32 v[16:17], v[16:17], v[18:19]
	s_nop 0
	v_pk_add_f32 v[16:17], v[20:21], v[16:17]
	s_nop 0
	v_cndmask_b32_e32 v16, v214, v16, vcc
	v_cmp_neq_f32_e32 vcc, s21, v99
	s_nop 1
	v_cndmask_b32_e32 v17, v214, v17, vcc
	v_cmp_ngt_f32_e32 vcc, -1.0, v99
	s_nop 1
	v_cndmask_b32_e32 v17, v215, v17, vcc
	v_cmp_ngt_f32_e32 vcc, -1.0, v98
	s_nop 1
	v_cndmask_b32_e32 v16, v215, v16, vcc
	v_cmp_neq_f32_e32 vcc, -1.0, v98
	s_nop 1
	v_cndmask_b32_e32 v16, v216, v16, vcc
	v_cmp_neq_f32_e32 vcc, -1.0, v99
	s_nop 1
	v_cndmask_b32_e32 v17, v216, v17, vcc
	v_cmp_lt_f32_e64 vcc, |v98|, s23
	v_cndmask_b32_e64 v17, v17, v99, s[0:1]
	s_nop 0
	v_cndmask_b32_e32 v16, v16, v98, vcc
	v_pk_add_f32 v[4:5], v[4:5], v[16:17] neg_lo:[0,1] neg_hi:[0,1]
	v_min_f32_e32 v16, 0, v6
	v_mul_f32_e64 v6, |v6|, s6
	v_exp_f32_e32 v92, v6
	s_nop 0
	v_add_f32_e32 v6, 1.0, v92
	v_add_f32_e32 v17, -1.0, v6
	v_sub_f32_e32 v18, v17, v6
	v_add_f32_e32 v18, 1.0, v18
	v_sub_f32_e32 v17, v92, v17
	v_add_f32_e32 v17, v17, v18
	v_frexp_mant_f32_e32 v18, v6
	v_cmp_gt_f32_e32 vcc, s7, v18
	v_cvt_f64_f32_e32 v[18:19], v6
	v_frexp_exp_i32_f64_e32 v18, v[18:19]
	v_subbrev_co_u32_e32 v84, vcc, 0, v18, vcc
	v_sub_u32_e32 v18, 0, v84
	v_ldexp_f32 v6, v6, v18
	v_ldexp_f32 v18, v17, v18
	v_min_f32_e32 v17, 0, v7
	v_mul_f32_e64 v7, |v7|, s6
	v_exp_f32_e32 v93, v7
	s_nop 0
	v_add_f32_e32 v7, 1.0, v93
	v_add_f32_e32 v19, -1.0, v7
	v_sub_f32_e32 v20, v19, v7
	v_add_f32_e32 v20, 1.0, v20
	v_sub_f32_e32 v19, v93, v19
	v_add_f32_e32 v19, v19, v20
	v_frexp_mant_f32_e32 v20, v7
	v_cmp_gt_f32_e32 vcc, s7, v20
	v_cvt_f64_f32_e32 v[20:21], v7
	v_frexp_exp_i32_f64_e32 v20, v[20:21]
	v_subbrev_co_u32_e32 v85, vcc, 0, v20, vcc
	v_sub_u32_e32 v20, 0, v85
	v_ldexp_f32 v7, v7, v20
	v_ldexp_f32 v19, v19, v20
	v_pk_add_f32 v[20:21], v[6:7], 1.0 op_sel_hi:[1,0]
	v_pk_add_f32 v[28:29], v[6:7], -1.0 op_sel_hi:[1,0]
	v_pk_add_f32 v[22:23], v[20:21], -1.0 op_sel_hi:[1,0]
	v_pk_add_f32 v[30:31], v[28:29], 1.0 op_sel_hi:[1,0]
	v_pk_add_f32 v[22:23], v[6:7], v[22:23] neg_lo:[0,1] neg_hi:[0,1]
	v_pk_add_f32 v[6:7], v[6:7], v[30:31] neg_lo:[0,1] neg_hi:[0,1]
	v_pk_add_f32 v[22:23], v[18:19], v[22:23]
	v_pk_add_f32 v[6:7], v[18:19], v[6:7]
	v_pk_add_f32 v[24:25], v[20:21], v[22:23]
	v_pk_add_f32 v[18:19], v[28:29], v[6:7]
	v_rcp_f32_e32 v26, v24
	v_rcp_f32_e32 v27, v25
	v_pk_add_f32 v[20:21], v[24:25], v[20:21] neg_lo:[0,1] neg_hi:[0,1]
	v_pk_add_f32 v[28:29], v[18:19], v[28:29] neg_lo:[0,1] neg_hi:[0,1]
	v_pk_add_f32 v[20:21], v[22:23], v[20:21] neg_lo:[0,1] neg_hi:[0,1]
	v_pk_mul_f32 v[22:23], v[18:19], v[26:27]
	v_pk_add_f32 v[6:7], v[6:7], v[28:29] neg_lo:[0,1] neg_hi:[0,1]
	v_pk_mul_f32 v[28:29], v[24:25], v[22:23]
	v_cmp_neq_f32_e32 vcc, s21, v92
	v_pk_fma_f32 v[30:31], v[22:23], v[24:25], v[28:29] neg_lo:[0,0,1] neg_hi:[0,0,1]
	v_cmp_lt_f32_e64 s[0:1], |v93|, s23
	v_pk_fma_f32 v[30:31], v[22:23], v[20:21], v[30:31]
	s_nop 0
	v_pk_add_f32 v[32:33], v[28:29], v[30:31]
	s_nop 0
	v_pk_add_f32 v[34:35], v[18:19], v[32:33] neg_lo:[0,1] neg_hi:[0,1]
	v_pk_add_f32 v[28:29], v[32:33], v[28:29] neg_lo:[0,1] neg_hi:[0,1]
	v_pk_add_f32 v[18:19], v[18:19], v[34:35] neg_lo:[0,1] neg_hi:[0,1]
	s_nop 0
	v_pk_add_f32 v[18:19], v[18:19], v[32:33] neg_lo:[0,1] neg_hi:[0,1]
	s_nop 0
	v_pk_add_f32 v[6:7], v[6:7], v[18:19]
	v_pk_add_f32 v[18:19], v[28:29], v[30:31] neg_lo:[0,1] neg_hi:[0,1]
	s_nop 0
	v_pk_add_f32 v[6:7], v[18:19], v[6:7]
	s_nop 0
	v_pk_add_f32 v[18:19], v[34:35], v[6:7]
	s_nop 0
	v_pk_mul_f32 v[28:29], v[26:27], v[18:19]
	s_nop 0
	v_pk_mul_f32 v[30:31], v[24:25], v[28:29]
	s_nop 0
	v_pk_fma_f32 v[24:25], v[28:29], v[24:25], v[30:31] neg_lo:[0,0,1] neg_hi:[0,0,1]
	s_nop 0
	v_pk_fma_f32 v[20:21], v[28:29], v[20:21], v[24:25]
	v_pk_add_f32 v[24:25], v[34:35], v[18:19] neg_lo:[0,1] neg_hi:[0,1]
	s_nop 0
	v_pk_add_f32 v[6:7], v[6:7], v[24:25]
	v_pk_add_f32 v[24:25], v[30:31], v[20:21]
	s_nop 0
	v_pk_add_f32 v[32:33], v[18:19], v[24:25] neg_lo:[0,1] neg_hi:[0,1]
	v_pk_add_f32 v[30:31], v[24:25], v[30:31] neg_lo:[0,1] neg_hi:[0,1]
	v_pk_add_f32 v[18:19], v[18:19], v[32:33] neg_lo:[0,1] neg_hi:[0,1]
	s_nop 0
	v_pk_add_f32 v[18:19], v[18:19], v[24:25] neg_lo:[0,1] neg_hi:[0,1]
	s_nop 0
	v_pk_add_f32 v[6:7], v[6:7], v[18:19]
	v_pk_add_f32 v[18:19], v[30:31], v[20:21] neg_lo:[0,1] neg_hi:[0,1]
	s_nop 0
	v_pk_add_f32 v[6:7], v[18:19], v[6:7]
	v_pk_add_f32 v[18:19], v[22:23], v[28:29]
	v_pk_add_f32 v[6:7], v[32:33], v[6:7]
	v_pk_add_f32 v[20:21], v[18:19], v[22:23] neg_lo:[0,1] neg_hi:[0,1]
	v_pk_mul_f32 v[6:7], v[26:27], v[6:7]
	v_pk_add_f32 v[20:21], v[28:29], v[20:21] neg_lo:[0,1] neg_hi:[0,1]
	s_nop 0
	v_pk_add_f32 v[6:7], v[20:21], v[6:7]
	s_nop 0
	v_pk_add_f32 v[20:21], v[18:19], v[6:7]
	s_nop 0
	v_pk_mul_f32 v[22:23], v[20:21], v[20:21]
	v_pk_add_f32 v[18:19], v[20:21], v[18:19] neg_lo:[0,1] neg_hi:[0,1]
	v_pk_fma_f32 v[24:25], v[22:23], s[48:49], v[12:13] op_sel_hi:[1,0,0]
	v_pk_add_f32 v[6:7], v[6:7], v[18:19] neg_lo:[0,1] neg_hi:[0,1]
	v_ldexp_f32 v18, v20, 1
	v_pk_fma_f32 v[24:25], v[22:23], v[24:25], s[50:51] op_sel_hi:[1,1,0]
	v_ldexp_f32 v19, v21, 1
	v_pk_mul_f32 v[20:21], v[20:21], v[22:23]
	v_cvt_f32_i32_e32 v23, v85
	v_cvt_f32_i32_e32 v22, v84
	v_pk_mul_f32 v[20:21], v[20:21], v[24:25]
	v_ldexp_f32 v27, v7, 1
	v_pk_add_f32 v[24:25], v[18:19], v[20:21]
	v_pk_mul_f32 v[28:29], v[22:23], s[52:53] op_sel_hi:[1,0]
	v_pk_add_f32 v[18:19], v[24:25], v[18:19] neg_lo:[0,1] neg_hi:[0,1]
	v_pk_fma_f32 v[30:31], v[22:23], s[52:53], v[28:29] op_sel_hi:[1,0,1] neg_lo:[0,0,1] neg_hi:[0,0,1]
	v_pk_add_f32 v[18:19], v[20:21], v[18:19] neg_lo:[0,1] neg_hi:[0,1]
	v_pk_fma_f32 v[22:23], v[22:23], s[54:55], v[30:31] op_sel_hi:[1,0,1]
	v_ldexp_f32 v6, v6, 1
	v_mov_b32_e32 v20, v28
	v_mov_b32_e32 v21, v19
	v_mov_b32_e32 v26, v22
	v_mov_b32_e32 v7, v27
	v_pk_add_f32 v[20:21], v[20:21], v[26:27]
	v_pk_add_f32 v[26:27], v[6:7], v[18:19]
	v_mov_b32_e32 v19, v25
	v_mov_b32_e32 v7, v27
	v_pk_add_f32 v[30:31], v[28:29], v[22:23]
	v_pk_add_f32 v[6:7], v[6:7], v[18:19]
	v_pk_add_f32 v[18:19], v[24:25], v[26:27]
	v_mov_b32_e32 v88, v24
	v_pk_add_f32 v[32:33], v[30:31], v[18:19]
	v_mov_b32_e32 v86, v18
	v_mov_b32_e32 v87, v33
	v_mov_b32_e32 v89, v31
	v_pk_add_f32 v[86:87], v[86:87], v[88:89] neg_lo:[0,1] neg_hi:[0,1]
	v_mov_b32_e32 v34, v32
	v_mov_b32_e32 v35, v31
	v_mov_b32_e32 v84, v30
	v_mov_b32_e32 v85, v29
	v_mov_b32_e32 v88, v30
	v_mov_b32_e32 v89, v33
	v_mov_b32_e32 v29, v87
	v_pk_add_f32 v[34:35], v[34:35], v[84:85] neg_lo:[0,1] neg_hi:[0,1]
	v_mov_b32_e32 v84, v18
	v_mov_b32_e32 v85, v23
	v_pk_add_f32 v[28:29], v[88:89], v[28:29] neg_lo:[0,1] neg_hi:[0,1]
	v_pk_add_f32 v[84:85], v[84:85], v[34:35] neg_lo:[0,1] neg_hi:[0,1]
	v_mov_b32_e32 v88, v28
	v_mov_b32_e32 v89, v35
	v_mov_b32_e32 v90, v32
	v_mov_b32_e32 v91, v19
	v_mov_b32_e32 v35, v25
	v_pk_add_f32 v[88:89], v[22:23], v[88:89] neg_lo:[0,1] neg_hi:[0,1]
	v_pk_add_f32 v[34:35], v[90:91], v[34:35] neg_lo:[0,1] neg_hi:[0,1]
	v_mov_b32_e32 v23, v31
	v_pk_add_f32 v[20:21], v[20:21], v[34:35] neg_lo:[0,1] neg_hi:[0,1]
	v_pk_add_f32 v[22:23], v[22:23], v[28:29] neg_lo:[0,1] neg_hi:[0,1]
	v_pk_add_f32 v[6:7], v[6:7], v[86:87] neg_lo:[0,1] neg_hi:[0,1]
	v_pk_add_f32 v[18:19], v[18:19], v[24:25] neg_lo:[0,1] neg_hi:[0,1]
	v_pk_add_f32 v[24:25], v[6:7], v[22:23]
	v_mov_b32_e32 v23, v85
	v_mov_b32_e32 v7, v21
	v_pk_add_f32 v[18:19], v[26:27], v[18:19] neg_lo:[0,1] neg_hi:[0,1]
	v_pk_add_f32 v[26:27], v[84:85], v[20:21]
	v_pk_add_f32 v[6:7], v[22:23], v[6:7]
	v_mov_b32_e32 v20, v24
	v_pk_add_f32 v[6:7], v[6:7], v[88:89] neg_lo:[0,1] neg_hi:[0,1]
	v_mov_b32_e32 v21, v27
	v_pk_add_f32 v[20:21], v[20:21], v[6:7] neg_lo:[0,1] neg_hi:[0,1]
	v_pk_add_f32 v[6:7], v[18:19], v[6:7] neg_lo:[0,1] neg_hi:[0,1]
	v_pk_add_f32 v[20:21], v[22:23], v[20:21] neg_lo:[0,1] neg_hi:[0,1]
	v_pk_add_f32 v[18:19], v[26:27], v[24:25]
	v_pk_add_f32 v[6:7], v[6:7], v[20:21]
	v_pk_add_f32 v[20:21], v[32:33], v[18:19]
	s_nop 0
	v_pk_add_f32 v[22:23], v[20:21], v[32:33] neg_lo:[0,1] neg_hi:[0,1]
	s_nop 0
	v_pk_add_f32 v[18:19], v[18:19], v[22:23] neg_lo:[0,1] neg_hi:[0,1]
	s_nop 0
	v_pk_add_f32 v[6:7], v[6:7], v[18:19]
	s_nop 0
	v_pk_add_f32 v[6:7], v[20:21], v[6:7]
	s_nop 0
	v_cndmask_b32_e32 v6, v214, v6, vcc
	v_cmp_neq_f32_e32 vcc, s21, v93
	s_nop 1
	v_cndmask_b32_e32 v7, v214, v7, vcc
	v_cmp_ngt_f32_e32 vcc, -1.0, v93
	s_nop 1
	v_cndmask_b32_e32 v7, v215, v7, vcc
	v_cmp_ngt_f32_e32 vcc, -1.0, v92
	s_nop 1
	v_cndmask_b32_e32 v6, v215, v6, vcc
	v_cmp_neq_f32_e32 vcc, -1.0, v92
	s_nop 1
	v_cndmask_b32_e32 v6, v216, v6, vcc
	v_cmp_neq_f32_e32 vcc, -1.0, v93
	s_nop 1
	v_cndmask_b32_e32 v7, v216, v7, vcc
	v_cmp_lt_f32_e64 vcc, |v92|, s23
	v_cndmask_b32_e64 v7, v7, v93, s[0:1]
	s_nop 0
	v_cndmask_b32_e32 v6, v6, v92, vcc
	v_pk_add_f32 v[6:7], v[16:17], v[6:7] neg_lo:[0,1] neg_hi:[0,1]
	global_store_dwordx4 v[14:15], v[8:11], off offset:512
	global_store_dwordx4 v[14:15], v[4:7], off offset:528
	s_nop 1
	v_mov_b32_e32 v4, v164
	v_mov_b32_e32 v5, v165
	v_mov_b32_e32 v6, v166
	v_mov_b32_e32 v7, v167
	v_fmamk_f32 v8, v76, 0x3c800000, v4
	v_min_f32_e32 v4, 0, v8
	v_mul_f32_e64 v8, |v8|, s6
	v_exp_f32_e32 v90, v8
	v_fmamk_f32 v17, v77, 0x3c800000, v5
	v_min_f32_e32 v5, 0, v17
	v_mul_f32_e64 v17, |v17|, s6
	v_exp_f32_e32 v91, v17
	v_add_f32_e32 v10, 1.0, v90
	v_add_f32_e32 v8, -1.0, v10
	v_sub_f32_e32 v9, v8, v10
	v_add_f32_e32 v9, 1.0, v9
	v_sub_f32_e32 v8, v90, v8
	v_add_f32_e32 v17, 1.0, v91
	v_add_f32_e32 v11, v8, v9
	v_frexp_mant_f32_e32 v8, v10
	v_add_f32_e32 v19, -1.0, v17
	v_cmp_gt_f32_e32 vcc, s7, v8
	v_cvt_f64_f32_e32 v[8:9], v10
	v_sub_f32_e32 v20, v19, v17
	v_frexp_exp_i32_f64_e32 v8, v[8:9]
	v_add_f32_e32 v20, 1.0, v20
	v_sub_f32_e32 v19, v91, v19
	v_subbrev_co_u32_e32 v76, vcc, 0, v8, vcc
	v_add_f32_e32 v19, v19, v20
	v_frexp_mant_f32_e32 v20, v17
	v_cmp_gt_f32_e32 vcc, s7, v20
	v_cvt_f64_f32_e32 v[20:21], v17
	v_frexp_exp_i32_f64_e32 v20, v[20:21]
	v_subbrev_co_u32_e32 v77, vcc, 0, v20, vcc
	v_sub_u32_e32 v8, 0, v76
	v_sub_u32_e32 v20, 0, v77
	v_ldexp_f32 v16, v10, v8
	v_ldexp_f32 v17, v17, v20
	v_ldexp_f32 v19, v19, v20
	v_pk_add_f32 v[20:21], v[16:17], 1.0 op_sel_hi:[1,0]
	v_ldexp_f32 v18, v11, v8
	v_pk_add_f32 v[22:23], v[20:21], -1.0 op_sel_hi:[1,0]
	v_pk_add_f32 v[28:29], v[16:17], -1.0 op_sel_hi:[1,0]
	v_pk_add_f32 v[22:23], v[16:17], v[22:23] neg_lo:[0,1] neg_hi:[0,1]
	v_pk_add_f32 v[30:31], v[28:29], 1.0 op_sel_hi:[1,0]
	v_pk_add_f32 v[22:23], v[18:19], v[22:23]
	v_pk_add_f32 v[16:17], v[16:17], v[30:31] neg_lo:[0,1] neg_hi:[0,1]
	v_pk_add_f32 v[24:25], v[20:21], v[22:23]
	v_pk_add_f32 v[16:17], v[18:19], v[16:17]
	v_rcp_f32_e32 v26, v24
	v_rcp_f32_e32 v27, v25
	v_pk_add_f32 v[18:19], v[28:29], v[16:17]
	v_pk_add_f32 v[20:21], v[24:25], v[20:21] neg_lo:[0,1] neg_hi:[0,1]
	v_pk_add_f32 v[28:29], v[18:19], v[28:29] neg_lo:[0,1] neg_hi:[0,1]
	v_pk_add_f32 v[20:21], v[22:23], v[20:21] neg_lo:[0,1] neg_hi:[0,1]
	v_pk_mul_f32 v[22:23], v[18:19], v[26:27]
	v_pk_add_f32 v[16:17], v[16:17], v[28:29] neg_lo:[0,1] neg_hi:[0,1]
	v_pk_mul_f32 v[28:29], v[24:25], v[22:23]
	v_cmp_neq_f32_e32 vcc, s21, v90
	v_pk_fma_f32 v[30:31], v[22:23], v[24:25], v[28:29] neg_lo:[0,0,1] neg_hi:[0,0,1]
	v_pk_fma_f32 v[30:31], v[22:23], v[20:21], v[30:31]
	v_cmp_lt_f32_e64 s[0:1], |v91|, s23
	v_pk_add_f32 v[32:33], v[28:29], v[30:31]
	v_fmamk_f32 v6, v78, 0x3c800000, v6
	v_pk_add_f32 v[34:35], v[18:19], v[32:33] neg_lo:[0,1] neg_hi:[0,1]
	v_pk_add_f32 v[28:29], v[32:33], v[28:29] neg_lo:[0,1] neg_hi:[0,1]
	v_pk_add_f32 v[18:19], v[18:19], v[34:35] neg_lo:[0,1] neg_hi:[0,1]
	v_fmac_f32_e32 v7, 0x3c800000, v79
	v_pk_add_f32 v[18:19], v[18:19], v[32:33] neg_lo:[0,1] neg_hi:[0,1]
	v_mov_b32_e32 v8, v244
	v_mov_b32_e32 v9, v245
	v_mov_b32_e32 v10, v246
	v_mov_b32_e32 v11, v247
	v_pk_fma_f32 v[8:9], v[80:81], s[28:29], v[8:9] op_sel_hi:[1,0,1]
	v_pk_add_f32 v[16:17], v[16:17], v[18:19]
	v_pk_add_f32 v[18:19], v[28:29], v[30:31] neg_lo:[0,1] neg_hi:[0,1]
	v_pk_fma_f32 v[10:11], v[82:83], s[28:29], v[10:11] op_sel_hi:[1,0,1]
	v_pk_add_f32 v[16:17], v[18:19], v[16:17]
	s_nop 0
	v_pk_add_f32 v[18:19], v[34:35], v[16:17]
	s_nop 0
	v_pk_mul_f32 v[28:29], v[26:27], v[18:19]
	s_nop 0
	v_pk_mul_f32 v[30:31], v[24:25], v[28:29]
	s_nop 0
	v_pk_fma_f32 v[24:25], v[28:29], v[24:25], v[30:31] neg_lo:[0,0,1] neg_hi:[0,0,1]
	s_nop 0
	v_pk_fma_f32 v[20:21], v[28:29], v[20:21], v[24:25]
	v_pk_add_f32 v[24:25], v[34:35], v[18:19] neg_lo:[0,1] neg_hi:[0,1]
	s_nop 0
	v_pk_add_f32 v[16:17], v[16:17], v[24:25]
	v_pk_add_f32 v[24:25], v[30:31], v[20:21]
	s_nop 0
	v_pk_add_f32 v[32:33], v[18:19], v[24:25] neg_lo:[0,1] neg_hi:[0,1]
	v_pk_add_f32 v[30:31], v[24:25], v[30:31] neg_lo:[0,1] neg_hi:[0,1]
	v_pk_add_f32 v[18:19], v[18:19], v[32:33] neg_lo:[0,1] neg_hi:[0,1]
	s_nop 0
	v_pk_add_f32 v[18:19], v[18:19], v[24:25] neg_lo:[0,1] neg_hi:[0,1]
	s_nop 0
	v_pk_add_f32 v[16:17], v[16:17], v[18:19]
	v_pk_add_f32 v[18:19], v[30:31], v[20:21] neg_lo:[0,1] neg_hi:[0,1]
	s_nop 0
	v_pk_add_f32 v[16:17], v[18:19], v[16:17]
	v_pk_add_f32 v[18:19], v[22:23], v[28:29]
	v_pk_add_f32 v[16:17], v[32:33], v[16:17]
	v_pk_add_f32 v[20:21], v[18:19], v[22:23] neg_lo:[0,1] neg_hi:[0,1]
	v_pk_mul_f32 v[16:17], v[26:27], v[16:17]
	v_pk_add_f32 v[20:21], v[28:29], v[20:21] neg_lo:[0,1] neg_hi:[0,1]
	s_nop 0
	v_pk_add_f32 v[16:17], v[20:21], v[16:17]
	s_nop 0
	v_pk_add_f32 v[20:21], v[18:19], v[16:17]
	s_nop 0
	v_pk_mul_f32 v[22:23], v[20:21], v[20:21]
	v_pk_add_f32 v[18:19], v[20:21], v[18:19] neg_lo:[0,1] neg_hi:[0,1]
	v_pk_fma_f32 v[24:25], v[22:23], s[48:49], v[12:13] op_sel_hi:[1,0,0]
	v_pk_add_f32 v[16:17], v[16:17], v[18:19] neg_lo:[0,1] neg_hi:[0,1]
	v_ldexp_f32 v18, v20, 1
	v_pk_fma_f32 v[24:25], v[22:23], v[24:25], s[50:51] op_sel_hi:[1,1,0]
	v_ldexp_f32 v19, v21, 1
	v_pk_mul_f32 v[20:21], v[20:21], v[22:23]
	v_cvt_f32_i32_e32 v23, v77
	v_cvt_f32_i32_e32 v22, v76
	v_pk_mul_f32 v[20:21], v[20:21], v[24:25]
	v_ldexp_f32 v27, v17, 1
	v_pk_add_f32 v[24:25], v[18:19], v[20:21]
	v_pk_mul_f32 v[28:29], v[22:23], s[52:53] op_sel_hi:[1,0]
	v_pk_add_f32 v[18:19], v[24:25], v[18:19] neg_lo:[0,1] neg_hi:[0,1]
	v_pk_fma_f32 v[30:31], v[22:23], s[52:53], v[28:29] op_sel_hi:[1,0,1] neg_lo:[0,0,1] neg_hi:[0,0,1]
	v_pk_add_f32 v[18:19], v[20:21], v[18:19] neg_lo:[0,1] neg_hi:[0,1]
	v_pk_fma_f32 v[22:23], v[22:23], s[54:55], v[30:31] op_sel_hi:[1,0,1]
	v_ldexp_f32 v16, v16, 1
	v_mov_b32_e32 v20, v28
	v_mov_b32_e32 v21, v19
	v_mov_b32_e32 v26, v22
	v_mov_b32_e32 v17, v27
	v_pk_add_f32 v[20:21], v[20:21], v[26:27]
	v_pk_add_f32 v[26:27], v[16:17], v[18:19]
	v_mov_b32_e32 v19, v25
	v_mov_b32_e32 v17, v27
	v_pk_add_f32 v[30:31], v[28:29], v[22:23]
	v_pk_add_f32 v[16:17], v[16:17], v[18:19]
	v_pk_add_f32 v[18:19], v[24:25], v[26:27]
	v_mov_b32_e32 v86, v24
	v_pk_add_f32 v[32:33], v[30:31], v[18:19]
	v_mov_b32_e32 v84, v18
	v_mov_b32_e32 v85, v33
	v_mov_b32_e32 v87, v31
	v_pk_add_f32 v[84:85], v[84:85], v[86:87] neg_lo:[0,1] neg_hi:[0,1]
	v_mov_b32_e32 v34, v32
	v_mov_b32_e32 v35, v31
	v_mov_b32_e32 v76, v30
	v_mov_b32_e32 v77, v29
	v_mov_b32_e32 v86, v30
	v_mov_b32_e32 v87, v33
	v_mov_b32_e32 v29, v85
	v_pk_add_f32 v[34:35], v[34:35], v[76:77] neg_lo:[0,1] neg_hi:[0,1]
	v_mov_b32_e32 v76, v18
	v_mov_b32_e32 v77, v23
	v_pk_add_f32 v[28:29], v[86:87], v[28:29] neg_lo:[0,1] neg_hi:[0,1]
	v_pk_add_f32 v[76:77], v[76:77], v[34:35] neg_lo:[0,1] neg_hi:[0,1]
	v_mov_b32_e32 v86, v28
	v_mov_b32_e32 v87, v35
	v_mov_b32_e32 v88, v32
	v_mov_b32_e32 v89, v19
	v_mov_b32_e32 v35, v25
	v_pk_add_f32 v[86:87], v[22:23], v[86:87] neg_lo:[0,1] neg_hi:[0,1]
	v_pk_add_f32 v[34:35], v[88:89], v[34:35] neg_lo:[0,1] neg_hi:[0,1]
	v_mov_b32_e32 v23, v31
	v_pk_add_f32 v[20:21], v[20:21], v[34:35] neg_lo:[0,1] neg_hi:[0,1]
	v_pk_add_f32 v[22:23], v[22:23], v[28:29] neg_lo:[0,1] neg_hi:[0,1]
	v_pk_add_f32 v[16:17], v[16:17], v[84:85] neg_lo:[0,1] neg_hi:[0,1]
	v_pk_add_f32 v[18:19], v[18:19], v[24:25] neg_lo:[0,1] neg_hi:[0,1]
	v_pk_add_f32 v[24:25], v[16:17], v[22:23]
	v_mov_b32_e32 v23, v77
	v_mov_b32_e32 v17, v21
	v_pk_add_f32 v[18:19], v[26:27], v[18:19] neg_lo:[0,1] neg_hi:[0,1]
	v_pk_add_f32 v[26:27], v[76:77], v[20:21]
	v_pk_add_f32 v[16:17], v[22:23], v[16:17]
	v_mov_b32_e32 v20, v24
	v_pk_add_f32 v[16:17], v[16:17], v[86:87] neg_lo:[0,1] neg_hi:[0,1]
	v_mov_b32_e32 v21, v27
	v_pk_add_f32 v[20:21], v[20:21], v[16:17] neg_lo:[0,1] neg_hi:[0,1]
	v_pk_add_f32 v[16:17], v[18:19], v[16:17] neg_lo:[0,1] neg_hi:[0,1]
	v_pk_add_f32 v[20:21], v[22:23], v[20:21] neg_lo:[0,1] neg_hi:[0,1]
	v_pk_add_f32 v[18:19], v[26:27], v[24:25]
	v_pk_add_f32 v[16:17], v[16:17], v[20:21]
	v_pk_add_f32 v[20:21], v[32:33], v[18:19]
	s_nop 0
	v_pk_add_f32 v[22:23], v[20:21], v[32:33] neg_lo:[0,1] neg_hi:[0,1]
	s_nop 0
	v_pk_add_f32 v[18:19], v[18:19], v[22:23] neg_lo:[0,1] neg_hi:[0,1]
	s_nop 0
	v_pk_add_f32 v[16:17], v[16:17], v[18:19]
	s_nop 0
	v_pk_add_f32 v[16:17], v[20:21], v[16:17]
	s_nop 0
	v_cndmask_b32_e32 v16, v214, v16, vcc
	v_cmp_neq_f32_e32 vcc, s21, v91
	s_nop 1
	v_cndmask_b32_e32 v17, v214, v17, vcc
	v_cmp_ngt_f32_e32 vcc, -1.0, v91
	s_nop 1
	v_cndmask_b32_e32 v17, v215, v17, vcc
	v_cmp_ngt_f32_e32 vcc, -1.0, v90
	s_nop 1
	v_cndmask_b32_e32 v16, v215, v16, vcc
	v_cmp_neq_f32_e32 vcc, -1.0, v90
	s_nop 1
	v_cndmask_b32_e32 v16, v216, v16, vcc
	v_cmp_neq_f32_e32 vcc, -1.0, v91
	s_nop 1
	v_cndmask_b32_e32 v17, v216, v17, vcc
	v_cmp_lt_f32_e64 vcc, |v90|, s23
	v_cndmask_b32_e64 v17, v17, v91, s[0:1]
	s_nop 0
	v_cndmask_b32_e32 v16, v16, v90, vcc
	v_pk_add_f32 v[4:5], v[4:5], v[16:17] neg_lo:[0,1] neg_hi:[0,1]
	v_min_f32_e32 v16, 0, v6
	v_mul_f32_e64 v6, |v6|, s6
	v_exp_f32_e32 v84, v6
	s_nop 0
	v_add_f32_e32 v6, 1.0, v84
	v_add_f32_e32 v17, -1.0, v6
	v_sub_f32_e32 v18, v17, v6
	v_add_f32_e32 v18, 1.0, v18
	v_sub_f32_e32 v17, v84, v17
	v_add_f32_e32 v17, v17, v18
	v_frexp_mant_f32_e32 v18, v6
	v_cmp_gt_f32_e32 vcc, s7, v18
	v_cvt_f64_f32_e32 v[18:19], v6
	v_frexp_exp_i32_f64_e32 v18, v[18:19]
	v_subbrev_co_u32_e32 v76, vcc, 0, v18, vcc
	v_sub_u32_e32 v18, 0, v76
	v_ldexp_f32 v6, v6, v18
	v_ldexp_f32 v18, v17, v18
	v_min_f32_e32 v17, 0, v7
	v_mul_f32_e64 v7, |v7|, s6
	v_exp_f32_e32 v85, v7
	s_nop 0
	v_add_f32_e32 v7, 1.0, v85
	v_add_f32_e32 v19, -1.0, v7
	v_sub_f32_e32 v20, v19, v7
	v_add_f32_e32 v20, 1.0, v20
	v_sub_f32_e32 v19, v85, v19
	v_add_f32_e32 v19, v19, v20
	v_frexp_mant_f32_e32 v20, v7
	v_cmp_gt_f32_e32 vcc, s7, v20
	v_cvt_f64_f32_e32 v[20:21], v7
	v_frexp_exp_i32_f64_e32 v20, v[20:21]
	v_subbrev_co_u32_e32 v77, vcc, 0, v20, vcc
	v_sub_u32_e32 v20, 0, v77
	v_ldexp_f32 v7, v7, v20
	v_ldexp_f32 v19, v19, v20
	v_pk_add_f32 v[20:21], v[6:7], 1.0 op_sel_hi:[1,0]
	v_pk_add_f32 v[28:29], v[6:7], -1.0 op_sel_hi:[1,0]
	v_pk_add_f32 v[22:23], v[20:21], -1.0 op_sel_hi:[1,0]
	v_pk_add_f32 v[30:31], v[28:29], 1.0 op_sel_hi:[1,0]
	v_pk_add_f32 v[22:23], v[6:7], v[22:23] neg_lo:[0,1] neg_hi:[0,1]
	v_pk_add_f32 v[6:7], v[6:7], v[30:31] neg_lo:[0,1] neg_hi:[0,1]
	v_pk_add_f32 v[22:23], v[18:19], v[22:23]
	v_pk_add_f32 v[6:7], v[18:19], v[6:7]
	v_pk_add_f32 v[24:25], v[20:21], v[22:23]
	v_pk_add_f32 v[18:19], v[28:29], v[6:7]
	v_rcp_f32_e32 v26, v24
	v_rcp_f32_e32 v27, v25
	v_pk_add_f32 v[20:21], v[24:25], v[20:21] neg_lo:[0,1] neg_hi:[0,1]
	v_pk_add_f32 v[28:29], v[18:19], v[28:29] neg_lo:[0,1] neg_hi:[0,1]
	v_pk_add_f32 v[20:21], v[22:23], v[20:21] neg_lo:[0,1] neg_hi:[0,1]
	v_pk_mul_f32 v[22:23], v[18:19], v[26:27]
	v_pk_add_f32 v[6:7], v[6:7], v[28:29] neg_lo:[0,1] neg_hi:[0,1]
	v_pk_mul_f32 v[28:29], v[24:25], v[22:23]
	v_cmp_neq_f32_e32 vcc, s21, v84
	v_pk_fma_f32 v[30:31], v[22:23], v[24:25], v[28:29] neg_lo:[0,0,1] neg_hi:[0,0,1]
	v_cmp_lt_f32_e64 s[0:1], |v85|, s23
	v_pk_fma_f32 v[30:31], v[22:23], v[20:21], v[30:31]
	s_nop 0
	v_pk_add_f32 v[32:33], v[28:29], v[30:31]
	s_nop 0
	v_pk_add_f32 v[34:35], v[18:19], v[32:33] neg_lo:[0,1] neg_hi:[0,1]
	v_pk_add_f32 v[28:29], v[32:33], v[28:29] neg_lo:[0,1] neg_hi:[0,1]
	v_pk_add_f32 v[18:19], v[18:19], v[34:35] neg_lo:[0,1] neg_hi:[0,1]
	s_nop 0
	v_pk_add_f32 v[18:19], v[18:19], v[32:33] neg_lo:[0,1] neg_hi:[0,1]
	s_nop 0
	v_pk_add_f32 v[6:7], v[6:7], v[18:19]
	v_pk_add_f32 v[18:19], v[28:29], v[30:31] neg_lo:[0,1] neg_hi:[0,1]
	s_nop 0
	v_pk_add_f32 v[6:7], v[18:19], v[6:7]
	s_nop 0
	v_pk_add_f32 v[18:19], v[34:35], v[6:7]
	s_nop 0
	v_pk_mul_f32 v[28:29], v[26:27], v[18:19]
	s_nop 0
	v_pk_mul_f32 v[30:31], v[24:25], v[28:29]
	s_nop 0
	v_pk_fma_f32 v[24:25], v[28:29], v[24:25], v[30:31] neg_lo:[0,0,1] neg_hi:[0,0,1]
	s_nop 0
	v_pk_fma_f32 v[20:21], v[28:29], v[20:21], v[24:25]
	v_pk_add_f32 v[24:25], v[34:35], v[18:19] neg_lo:[0,1] neg_hi:[0,1]
	s_nop 0
	v_pk_add_f32 v[6:7], v[6:7], v[24:25]
	v_pk_add_f32 v[24:25], v[30:31], v[20:21]
	s_nop 0
	v_pk_add_f32 v[32:33], v[18:19], v[24:25] neg_lo:[0,1] neg_hi:[0,1]
	v_pk_add_f32 v[30:31], v[24:25], v[30:31] neg_lo:[0,1] neg_hi:[0,1]
	v_pk_add_f32 v[18:19], v[18:19], v[32:33] neg_lo:[0,1] neg_hi:[0,1]
	s_nop 0
	v_pk_add_f32 v[18:19], v[18:19], v[24:25] neg_lo:[0,1] neg_hi:[0,1]
	s_nop 0
	v_pk_add_f32 v[6:7], v[6:7], v[18:19]
	v_pk_add_f32 v[18:19], v[30:31], v[20:21] neg_lo:[0,1] neg_hi:[0,1]
	s_nop 0
	v_pk_add_f32 v[6:7], v[18:19], v[6:7]
	v_pk_add_f32 v[18:19], v[22:23], v[28:29]
	v_pk_add_f32 v[6:7], v[32:33], v[6:7]
	v_pk_add_f32 v[20:21], v[18:19], v[22:23] neg_lo:[0,1] neg_hi:[0,1]
	v_pk_mul_f32 v[6:7], v[26:27], v[6:7]
	v_pk_add_f32 v[20:21], v[28:29], v[20:21] neg_lo:[0,1] neg_hi:[0,1]
	s_nop 0
	v_pk_add_f32 v[6:7], v[20:21], v[6:7]
	s_nop 0
	v_pk_add_f32 v[20:21], v[18:19], v[6:7]
	s_nop 0
	v_pk_mul_f32 v[22:23], v[20:21], v[20:21]
	v_pk_add_f32 v[18:19], v[20:21], v[18:19] neg_lo:[0,1] neg_hi:[0,1]
	v_pk_fma_f32 v[24:25], v[22:23], s[48:49], v[12:13] op_sel_hi:[1,0,0]
	v_pk_add_f32 v[6:7], v[6:7], v[18:19] neg_lo:[0,1] neg_hi:[0,1]
	v_ldexp_f32 v18, v20, 1
	v_pk_fma_f32 v[24:25], v[22:23], v[24:25], s[50:51] op_sel_hi:[1,1,0]
	v_ldexp_f32 v19, v21, 1
	v_pk_mul_f32 v[20:21], v[20:21], v[22:23]
	v_cvt_f32_i32_e32 v23, v77
	v_cvt_f32_i32_e32 v22, v76
	v_pk_mul_f32 v[20:21], v[20:21], v[24:25]
	v_ldexp_f32 v27, v7, 1
	v_pk_add_f32 v[24:25], v[18:19], v[20:21]
	v_pk_mul_f32 v[28:29], v[22:23], s[52:53] op_sel_hi:[1,0]
	v_pk_add_f32 v[18:19], v[24:25], v[18:19] neg_lo:[0,1] neg_hi:[0,1]
	v_pk_fma_f32 v[30:31], v[22:23], s[52:53], v[28:29] op_sel_hi:[1,0,1] neg_lo:[0,0,1] neg_hi:[0,0,1]
	v_pk_add_f32 v[18:19], v[20:21], v[18:19] neg_lo:[0,1] neg_hi:[0,1]
	v_pk_fma_f32 v[22:23], v[22:23], s[54:55], v[30:31] op_sel_hi:[1,0,1]
	v_ldexp_f32 v6, v6, 1
	v_mov_b32_e32 v20, v28
	v_mov_b32_e32 v21, v19
	v_mov_b32_e32 v26, v22
	v_mov_b32_e32 v7, v27
	v_pk_add_f32 v[20:21], v[20:21], v[26:27]
	v_pk_add_f32 v[26:27], v[6:7], v[18:19]
	v_mov_b32_e32 v19, v25
	v_mov_b32_e32 v7, v27
	v_pk_add_f32 v[30:31], v[28:29], v[22:23]
	v_pk_add_f32 v[6:7], v[6:7], v[18:19]
	v_pk_add_f32 v[18:19], v[24:25], v[26:27]
	v_mov_b32_e32 v80, v24
	v_pk_add_f32 v[32:33], v[30:31], v[18:19]
	v_mov_b32_e32 v78, v18
	v_mov_b32_e32 v79, v33
	v_mov_b32_e32 v81, v31
	v_pk_add_f32 v[78:79], v[78:79], v[80:81] neg_lo:[0,1] neg_hi:[0,1]
	v_mov_b32_e32 v34, v32
	v_mov_b32_e32 v35, v31
	v_mov_b32_e32 v76, v30
	v_mov_b32_e32 v77, v29
	v_mov_b32_e32 v80, v30
	v_mov_b32_e32 v81, v33
	v_mov_b32_e32 v29, v79
	v_pk_add_f32 v[34:35], v[34:35], v[76:77] neg_lo:[0,1] neg_hi:[0,1]
	v_mov_b32_e32 v76, v18
	v_mov_b32_e32 v77, v23
	v_pk_add_f32 v[28:29], v[80:81], v[28:29] neg_lo:[0,1] neg_hi:[0,1]
	v_pk_add_f32 v[76:77], v[76:77], v[34:35] neg_lo:[0,1] neg_hi:[0,1]
	v_mov_b32_e32 v80, v28
	v_mov_b32_e32 v81, v35
	v_mov_b32_e32 v82, v32
	v_mov_b32_e32 v83, v19
	v_mov_b32_e32 v35, v25
	v_pk_add_f32 v[80:81], v[22:23], v[80:81] neg_lo:[0,1] neg_hi:[0,1]
	v_pk_add_f32 v[34:35], v[82:83], v[34:35] neg_lo:[0,1] neg_hi:[0,1]
	v_mov_b32_e32 v23, v31
	v_pk_add_f32 v[20:21], v[20:21], v[34:35] neg_lo:[0,1] neg_hi:[0,1]
	v_pk_add_f32 v[22:23], v[22:23], v[28:29] neg_lo:[0,1] neg_hi:[0,1]
	v_pk_add_f32 v[6:7], v[6:7], v[78:79] neg_lo:[0,1] neg_hi:[0,1]
	v_pk_add_f32 v[18:19], v[18:19], v[24:25] neg_lo:[0,1] neg_hi:[0,1]
	v_pk_add_f32 v[24:25], v[6:7], v[22:23]
	v_mov_b32_e32 v23, v77
	v_mov_b32_e32 v7, v21
	v_pk_add_f32 v[18:19], v[26:27], v[18:19] neg_lo:[0,1] neg_hi:[0,1]
	v_pk_add_f32 v[26:27], v[76:77], v[20:21]
	v_pk_add_f32 v[6:7], v[22:23], v[6:7]
	v_mov_b32_e32 v20, v24
	v_pk_add_f32 v[6:7], v[6:7], v[80:81] neg_lo:[0,1] neg_hi:[0,1]
	v_mov_b32_e32 v21, v27
	v_pk_add_f32 v[20:21], v[20:21], v[6:7] neg_lo:[0,1] neg_hi:[0,1]
	v_pk_add_f32 v[6:7], v[18:19], v[6:7] neg_lo:[0,1] neg_hi:[0,1]
	v_pk_add_f32 v[20:21], v[22:23], v[20:21] neg_lo:[0,1] neg_hi:[0,1]
	v_pk_add_f32 v[18:19], v[26:27], v[24:25]
	v_pk_add_f32 v[6:7], v[6:7], v[20:21]
	v_pk_add_f32 v[20:21], v[32:33], v[18:19]
	s_nop 0
	v_pk_add_f32 v[22:23], v[20:21], v[32:33] neg_lo:[0,1] neg_hi:[0,1]
	s_nop 0
	v_pk_add_f32 v[18:19], v[18:19], v[22:23] neg_lo:[0,1] neg_hi:[0,1]
	s_nop 0
	v_pk_add_f32 v[6:7], v[6:7], v[18:19]
	s_nop 0
	v_pk_add_f32 v[6:7], v[20:21], v[6:7]
	s_nop 0
	v_cndmask_b32_e32 v6, v214, v6, vcc
	v_cmp_neq_f32_e32 vcc, s21, v85
	s_nop 1
	v_cndmask_b32_e32 v7, v214, v7, vcc
	v_cmp_ngt_f32_e32 vcc, -1.0, v85
	s_nop 1
	v_cndmask_b32_e32 v7, v215, v7, vcc
	v_cmp_ngt_f32_e32 vcc, -1.0, v84
	s_nop 1
	v_cndmask_b32_e32 v6, v215, v6, vcc
	v_cmp_neq_f32_e32 vcc, -1.0, v84
	s_nop 1
	v_cndmask_b32_e32 v6, v216, v6, vcc
	v_cmp_neq_f32_e32 vcc, -1.0, v85
	s_nop 1
	v_cndmask_b32_e32 v7, v216, v7, vcc
	v_cmp_lt_f32_e64 vcc, |v84|, s23
	v_cndmask_b32_e64 v7, v7, v85, s[0:1]
	s_nop 0
	v_cndmask_b32_e32 v6, v6, v84, vcc
	v_pk_add_f32 v[6:7], v[16:17], v[6:7] neg_lo:[0,1] neg_hi:[0,1]
	global_store_dwordx4 v[14:15], v[8:11], off offset:1024
	global_store_dwordx4 v[14:15], v[4:7], off offset:1040
	s_nop 1
	v_mov_b32_e32 v4, v164
	v_mov_b32_e32 v5, v165
	v_mov_b32_e32 v6, v166
	v_mov_b32_e32 v7, v167
	v_fmamk_f32 v8, v68, 0x3c800000, v4
	v_min_f32_e32 v4, 0, v8
	v_mul_f32_e64 v8, |v8|, s6
	v_exp_f32_e32 v82, v8
	v_fmamk_f32 v17, v69, 0x3c800000, v5
	v_min_f32_e32 v5, 0, v17
	v_mul_f32_e64 v17, |v17|, s6
	v_exp_f32_e32 v83, v17
	v_add_f32_e32 v10, 1.0, v82
	v_add_f32_e32 v8, -1.0, v10
	v_sub_f32_e32 v9, v8, v10
	v_add_f32_e32 v9, 1.0, v9
	v_sub_f32_e32 v8, v82, v8
	v_add_f32_e32 v17, 1.0, v83
	v_add_f32_e32 v11, v8, v9
	v_frexp_mant_f32_e32 v8, v10
	v_add_f32_e32 v19, -1.0, v17
	v_cmp_gt_f32_e32 vcc, s7, v8
	v_cvt_f64_f32_e32 v[8:9], v10
	v_sub_f32_e32 v20, v19, v17
	v_frexp_exp_i32_f64_e32 v8, v[8:9]
	v_add_f32_e32 v20, 1.0, v20
	v_sub_f32_e32 v19, v83, v19
	v_subbrev_co_u32_e32 v68, vcc, 0, v8, vcc
	v_add_f32_e32 v19, v19, v20
	v_frexp_mant_f32_e32 v20, v17
	v_cmp_gt_f32_e32 vcc, s7, v20
	v_cvt_f64_f32_e32 v[20:21], v17
	v_frexp_exp_i32_f64_e32 v20, v[20:21]
	v_subbrev_co_u32_e32 v69, vcc, 0, v20, vcc
	v_sub_u32_e32 v8, 0, v68
	v_sub_u32_e32 v20, 0, v69
	v_ldexp_f32 v16, v10, v8
	v_ldexp_f32 v17, v17, v20
	v_ldexp_f32 v19, v19, v20
	v_pk_add_f32 v[20:21], v[16:17], 1.0 op_sel_hi:[1,0]
	v_ldexp_f32 v18, v11, v8
	v_pk_add_f32 v[22:23], v[20:21], -1.0 op_sel_hi:[1,0]
	v_pk_add_f32 v[28:29], v[16:17], -1.0 op_sel_hi:[1,0]
	v_pk_add_f32 v[22:23], v[16:17], v[22:23] neg_lo:[0,1] neg_hi:[0,1]
	v_pk_add_f32 v[30:31], v[28:29], 1.0 op_sel_hi:[1,0]
	v_pk_add_f32 v[22:23], v[18:19], v[22:23]
	v_pk_add_f32 v[16:17], v[16:17], v[30:31] neg_lo:[0,1] neg_hi:[0,1]
	v_pk_add_f32 v[24:25], v[20:21], v[22:23]
	v_pk_add_f32 v[16:17], v[18:19], v[16:17]
	v_rcp_f32_e32 v26, v24
	v_rcp_f32_e32 v27, v25
	v_pk_add_f32 v[18:19], v[28:29], v[16:17]
	v_pk_add_f32 v[20:21], v[24:25], v[20:21] neg_lo:[0,1] neg_hi:[0,1]
	v_pk_add_f32 v[28:29], v[18:19], v[28:29] neg_lo:[0,1] neg_hi:[0,1]
	v_pk_add_f32 v[20:21], v[22:23], v[20:21] neg_lo:[0,1] neg_hi:[0,1]
	v_pk_mul_f32 v[22:23], v[18:19], v[26:27]
	v_pk_add_f32 v[16:17], v[16:17], v[28:29] neg_lo:[0,1] neg_hi:[0,1]
	v_pk_mul_f32 v[28:29], v[24:25], v[22:23]
	v_cmp_neq_f32_e32 vcc, s21, v82
	v_pk_fma_f32 v[30:31], v[22:23], v[24:25], v[28:29] neg_lo:[0,0,1] neg_hi:[0,0,1]
	v_pk_fma_f32 v[30:31], v[22:23], v[20:21], v[30:31]
	v_cmp_lt_f32_e64 s[0:1], |v83|, s23
	v_pk_add_f32 v[32:33], v[28:29], v[30:31]
	v_fmamk_f32 v6, v70, 0x3c800000, v6
	v_pk_add_f32 v[34:35], v[18:19], v[32:33] neg_lo:[0,1] neg_hi:[0,1]
	v_pk_add_f32 v[28:29], v[32:33], v[28:29] neg_lo:[0,1] neg_hi:[0,1]
	v_pk_add_f32 v[18:19], v[18:19], v[34:35] neg_lo:[0,1] neg_hi:[0,1]
	v_fmac_f32_e32 v7, 0x3c800000, v71
	v_pk_add_f32 v[18:19], v[18:19], v[32:33] neg_lo:[0,1] neg_hi:[0,1]
	v_mov_b32_e32 v8, v244
	v_mov_b32_e32 v9, v245
	v_mov_b32_e32 v10, v246
	v_mov_b32_e32 v11, v247
	v_pk_fma_f32 v[8:9], v[72:73], s[28:29], v[8:9] op_sel_hi:[1,0,1]
	v_pk_add_f32 v[16:17], v[16:17], v[18:19]
	v_pk_add_f32 v[18:19], v[28:29], v[30:31] neg_lo:[0,1] neg_hi:[0,1]
	v_pk_fma_f32 v[10:11], v[74:75], s[28:29], v[10:11] op_sel_hi:[1,0,1]
	v_pk_add_f32 v[16:17], v[18:19], v[16:17]
	s_nop 0
	v_pk_add_f32 v[18:19], v[34:35], v[16:17]
	s_nop 0
	v_pk_mul_f32 v[28:29], v[26:27], v[18:19]
	s_nop 0
	v_pk_mul_f32 v[30:31], v[24:25], v[28:29]
	s_nop 0
	v_pk_fma_f32 v[24:25], v[28:29], v[24:25], v[30:31] neg_lo:[0,0,1] neg_hi:[0,0,1]
	s_nop 0
	v_pk_fma_f32 v[20:21], v[28:29], v[20:21], v[24:25]
	v_pk_add_f32 v[24:25], v[34:35], v[18:19] neg_lo:[0,1] neg_hi:[0,1]
	s_nop 0
	v_pk_add_f32 v[16:17], v[16:17], v[24:25]
	v_pk_add_f32 v[24:25], v[30:31], v[20:21]
	s_nop 0
	v_pk_add_f32 v[32:33], v[18:19], v[24:25] neg_lo:[0,1] neg_hi:[0,1]
	v_pk_add_f32 v[30:31], v[24:25], v[30:31] neg_lo:[0,1] neg_hi:[0,1]
	v_pk_add_f32 v[18:19], v[18:19], v[32:33] neg_lo:[0,1] neg_hi:[0,1]
	s_nop 0
	v_pk_add_f32 v[18:19], v[18:19], v[24:25] neg_lo:[0,1] neg_hi:[0,1]
	s_nop 0
	v_pk_add_f32 v[16:17], v[16:17], v[18:19]
	v_pk_add_f32 v[18:19], v[30:31], v[20:21] neg_lo:[0,1] neg_hi:[0,1]
	s_nop 0
	v_pk_add_f32 v[16:17], v[18:19], v[16:17]
	v_pk_add_f32 v[18:19], v[22:23], v[28:29]
	v_pk_add_f32 v[16:17], v[32:33], v[16:17]
	v_pk_add_f32 v[20:21], v[18:19], v[22:23] neg_lo:[0,1] neg_hi:[0,1]
	v_pk_mul_f32 v[16:17], v[26:27], v[16:17]
	v_pk_add_f32 v[20:21], v[28:29], v[20:21] neg_lo:[0,1] neg_hi:[0,1]
	s_nop 0
	v_pk_add_f32 v[16:17], v[20:21], v[16:17]
	s_nop 0
	v_pk_add_f32 v[20:21], v[18:19], v[16:17]
	s_nop 0
	v_pk_mul_f32 v[22:23], v[20:21], v[20:21]
	v_pk_add_f32 v[18:19], v[20:21], v[18:19] neg_lo:[0,1] neg_hi:[0,1]
	v_pk_fma_f32 v[24:25], v[22:23], s[48:49], v[12:13] op_sel_hi:[1,0,0]
	v_pk_add_f32 v[16:17], v[16:17], v[18:19] neg_lo:[0,1] neg_hi:[0,1]
	v_ldexp_f32 v18, v20, 1
	v_pk_fma_f32 v[24:25], v[22:23], v[24:25], s[50:51] op_sel_hi:[1,1,0]
	v_ldexp_f32 v19, v21, 1
	v_pk_mul_f32 v[20:21], v[20:21], v[22:23]
	v_cvt_f32_i32_e32 v23, v69
	v_cvt_f32_i32_e32 v22, v68
	v_pk_mul_f32 v[20:21], v[20:21], v[24:25]
	v_ldexp_f32 v27, v17, 1
	v_pk_add_f32 v[24:25], v[18:19], v[20:21]
	v_pk_mul_f32 v[28:29], v[22:23], s[52:53] op_sel_hi:[1,0]
	v_pk_add_f32 v[18:19], v[24:25], v[18:19] neg_lo:[0,1] neg_hi:[0,1]
	v_pk_fma_f32 v[30:31], v[22:23], s[52:53], v[28:29] op_sel_hi:[1,0,1] neg_lo:[0,0,1] neg_hi:[0,0,1]
	v_pk_add_f32 v[18:19], v[20:21], v[18:19] neg_lo:[0,1] neg_hi:[0,1]
	v_pk_fma_f32 v[22:23], v[22:23], s[54:55], v[30:31] op_sel_hi:[1,0,1]
	v_ldexp_f32 v16, v16, 1
	v_mov_b32_e32 v20, v28
	v_mov_b32_e32 v21, v19
	v_mov_b32_e32 v26, v22
	v_mov_b32_e32 v17, v27
	v_pk_add_f32 v[20:21], v[20:21], v[26:27]
	v_pk_add_f32 v[26:27], v[16:17], v[18:19]
	v_mov_b32_e32 v19, v25
	v_mov_b32_e32 v17, v27
	v_pk_add_f32 v[30:31], v[28:29], v[22:23]
	v_pk_add_f32 v[16:17], v[16:17], v[18:19]
	v_pk_add_f32 v[18:19], v[24:25], v[26:27]
	v_mov_b32_e32 v78, v24
	v_pk_add_f32 v[32:33], v[30:31], v[18:19]
	v_mov_b32_e32 v76, v18
	v_mov_b32_e32 v77, v33
	v_mov_b32_e32 v79, v31
	v_pk_add_f32 v[76:77], v[76:77], v[78:79] neg_lo:[0,1] neg_hi:[0,1]
	v_mov_b32_e32 v34, v32
	v_mov_b32_e32 v35, v31
	v_mov_b32_e32 v68, v30
	v_mov_b32_e32 v69, v29
	v_mov_b32_e32 v78, v30
	v_mov_b32_e32 v79, v33
	v_mov_b32_e32 v29, v77
	v_pk_add_f32 v[34:35], v[34:35], v[68:69] neg_lo:[0,1] neg_hi:[0,1]
	v_mov_b32_e32 v68, v18
	v_mov_b32_e32 v69, v23
	v_pk_add_f32 v[28:29], v[78:79], v[28:29] neg_lo:[0,1] neg_hi:[0,1]
	v_pk_add_f32 v[68:69], v[68:69], v[34:35] neg_lo:[0,1] neg_hi:[0,1]
	v_mov_b32_e32 v78, v28
	v_mov_b32_e32 v79, v35
	v_mov_b32_e32 v80, v32
	v_mov_b32_e32 v81, v19
	v_mov_b32_e32 v35, v25
	v_pk_add_f32 v[78:79], v[22:23], v[78:79] neg_lo:[0,1] neg_hi:[0,1]
	v_pk_add_f32 v[34:35], v[80:81], v[34:35] neg_lo:[0,1] neg_hi:[0,1]
	v_mov_b32_e32 v23, v31
	v_pk_add_f32 v[20:21], v[20:21], v[34:35] neg_lo:[0,1] neg_hi:[0,1]
	v_pk_add_f32 v[22:23], v[22:23], v[28:29] neg_lo:[0,1] neg_hi:[0,1]
	v_pk_add_f32 v[16:17], v[16:17], v[76:77] neg_lo:[0,1] neg_hi:[0,1]
	v_pk_add_f32 v[18:19], v[18:19], v[24:25] neg_lo:[0,1] neg_hi:[0,1]
	v_pk_add_f32 v[24:25], v[16:17], v[22:23]
	v_mov_b32_e32 v23, v69
	v_mov_b32_e32 v17, v21
	v_pk_add_f32 v[18:19], v[26:27], v[18:19] neg_lo:[0,1] neg_hi:[0,1]
	v_pk_add_f32 v[26:27], v[68:69], v[20:21]
	v_pk_add_f32 v[16:17], v[22:23], v[16:17]
	v_mov_b32_e32 v20, v24
	v_pk_add_f32 v[16:17], v[16:17], v[78:79] neg_lo:[0,1] neg_hi:[0,1]
	v_mov_b32_e32 v21, v27
	v_pk_add_f32 v[20:21], v[20:21], v[16:17] neg_lo:[0,1] neg_hi:[0,1]
	v_pk_add_f32 v[16:17], v[18:19], v[16:17] neg_lo:[0,1] neg_hi:[0,1]
	v_pk_add_f32 v[20:21], v[22:23], v[20:21] neg_lo:[0,1] neg_hi:[0,1]
	v_pk_add_f32 v[18:19], v[26:27], v[24:25]
	v_pk_add_f32 v[16:17], v[16:17], v[20:21]
	v_pk_add_f32 v[20:21], v[32:33], v[18:19]
	s_nop 0
	v_pk_add_f32 v[22:23], v[20:21], v[32:33] neg_lo:[0,1] neg_hi:[0,1]
	s_nop 0
	v_pk_add_f32 v[18:19], v[18:19], v[22:23] neg_lo:[0,1] neg_hi:[0,1]
	s_nop 0
	v_pk_add_f32 v[16:17], v[16:17], v[18:19]
	s_nop 0
	v_pk_add_f32 v[16:17], v[20:21], v[16:17]
	s_nop 0
	v_cndmask_b32_e32 v16, v214, v16, vcc
	v_cmp_neq_f32_e32 vcc, s21, v83
	s_nop 1
	v_cndmask_b32_e32 v17, v214, v17, vcc
	v_cmp_ngt_f32_e32 vcc, -1.0, v83
	s_nop 1
	v_cndmask_b32_e32 v17, v215, v17, vcc
	v_cmp_ngt_f32_e32 vcc, -1.0, v82
	s_nop 1
	v_cndmask_b32_e32 v16, v215, v16, vcc
	v_cmp_neq_f32_e32 vcc, -1.0, v82
	s_nop 1
	v_cndmask_b32_e32 v16, v216, v16, vcc
	v_cmp_neq_f32_e32 vcc, -1.0, v83
	s_nop 1
	v_cndmask_b32_e32 v17, v216, v17, vcc
	v_cmp_lt_f32_e64 vcc, |v82|, s23
	v_cndmask_b32_e64 v17, v17, v83, s[0:1]
	s_nop 0
	v_cndmask_b32_e32 v16, v16, v82, vcc
	v_pk_add_f32 v[4:5], v[4:5], v[16:17] neg_lo:[0,1] neg_hi:[0,1]
	v_min_f32_e32 v16, 0, v6
	v_mul_f32_e64 v6, |v6|, s6
	v_exp_f32_e32 v76, v6
	s_nop 0
	v_add_f32_e32 v6, 1.0, v76
	v_add_f32_e32 v17, -1.0, v6
	v_sub_f32_e32 v18, v17, v6
	v_add_f32_e32 v18, 1.0, v18
	v_sub_f32_e32 v17, v76, v17
	v_add_f32_e32 v17, v17, v18
	v_frexp_mant_f32_e32 v18, v6
	v_cmp_gt_f32_e32 vcc, s7, v18
	v_cvt_f64_f32_e32 v[18:19], v6
	v_frexp_exp_i32_f64_e32 v18, v[18:19]
	v_subbrev_co_u32_e32 v68, vcc, 0, v18, vcc
	v_sub_u32_e32 v18, 0, v68
	v_ldexp_f32 v6, v6, v18
	v_ldexp_f32 v18, v17, v18
	v_min_f32_e32 v17, 0, v7
	v_mul_f32_e64 v7, |v7|, s6
	v_exp_f32_e32 v77, v7
	s_nop 0
	v_add_f32_e32 v7, 1.0, v77
	v_add_f32_e32 v19, -1.0, v7
	v_sub_f32_e32 v20, v19, v7
	v_add_f32_e32 v20, 1.0, v20
	v_sub_f32_e32 v19, v77, v19
	v_add_f32_e32 v19, v19, v20
	v_frexp_mant_f32_e32 v20, v7
	v_cmp_gt_f32_e32 vcc, s7, v20
	v_cvt_f64_f32_e32 v[20:21], v7
	v_frexp_exp_i32_f64_e32 v20, v[20:21]
	v_subbrev_co_u32_e32 v69, vcc, 0, v20, vcc
	v_sub_u32_e32 v20, 0, v69
	v_ldexp_f32 v7, v7, v20
	v_ldexp_f32 v19, v19, v20
	v_pk_add_f32 v[20:21], v[6:7], 1.0 op_sel_hi:[1,0]
	v_pk_add_f32 v[28:29], v[6:7], -1.0 op_sel_hi:[1,0]
	v_pk_add_f32 v[22:23], v[20:21], -1.0 op_sel_hi:[1,0]
	v_pk_add_f32 v[30:31], v[28:29], 1.0 op_sel_hi:[1,0]
	v_pk_add_f32 v[22:23], v[6:7], v[22:23] neg_lo:[0,1] neg_hi:[0,1]
	v_pk_add_f32 v[6:7], v[6:7], v[30:31] neg_lo:[0,1] neg_hi:[0,1]
	v_pk_add_f32 v[22:23], v[18:19], v[22:23]
	v_pk_add_f32 v[6:7], v[18:19], v[6:7]
	v_pk_add_f32 v[24:25], v[20:21], v[22:23]
	v_pk_add_f32 v[18:19], v[28:29], v[6:7]
	v_rcp_f32_e32 v26, v24
	v_rcp_f32_e32 v27, v25
	v_pk_add_f32 v[20:21], v[24:25], v[20:21] neg_lo:[0,1] neg_hi:[0,1]
	v_pk_add_f32 v[28:29], v[18:19], v[28:29] neg_lo:[0,1] neg_hi:[0,1]
	v_pk_add_f32 v[20:21], v[22:23], v[20:21] neg_lo:[0,1] neg_hi:[0,1]
	v_pk_mul_f32 v[22:23], v[18:19], v[26:27]
	v_pk_add_f32 v[6:7], v[6:7], v[28:29] neg_lo:[0,1] neg_hi:[0,1]
	v_pk_mul_f32 v[28:29], v[24:25], v[22:23]
	v_cmp_neq_f32_e32 vcc, s21, v76
	v_pk_fma_f32 v[30:31], v[22:23], v[24:25], v[28:29] neg_lo:[0,0,1] neg_hi:[0,0,1]
	v_cmp_lt_f32_e64 s[0:1], |v77|, s23
	v_pk_fma_f32 v[30:31], v[22:23], v[20:21], v[30:31]
	s_nop 0
	v_pk_add_f32 v[32:33], v[28:29], v[30:31]
	s_nop 0
	v_pk_add_f32 v[34:35], v[18:19], v[32:33] neg_lo:[0,1] neg_hi:[0,1]
	v_pk_add_f32 v[28:29], v[32:33], v[28:29] neg_lo:[0,1] neg_hi:[0,1]
	v_pk_add_f32 v[18:19], v[18:19], v[34:35] neg_lo:[0,1] neg_hi:[0,1]
	s_nop 0
	v_pk_add_f32 v[18:19], v[18:19], v[32:33] neg_lo:[0,1] neg_hi:[0,1]
	s_nop 0
	v_pk_add_f32 v[6:7], v[6:7], v[18:19]
	v_pk_add_f32 v[18:19], v[28:29], v[30:31] neg_lo:[0,1] neg_hi:[0,1]
	s_nop 0
	v_pk_add_f32 v[6:7], v[18:19], v[6:7]
	s_nop 0
	v_pk_add_f32 v[18:19], v[34:35], v[6:7]
	s_nop 0
	v_pk_mul_f32 v[28:29], v[26:27], v[18:19]
	s_nop 0
	v_pk_mul_f32 v[30:31], v[24:25], v[28:29]
	s_nop 0
	v_pk_fma_f32 v[24:25], v[28:29], v[24:25], v[30:31] neg_lo:[0,0,1] neg_hi:[0,0,1]
	s_nop 0
	v_pk_fma_f32 v[20:21], v[28:29], v[20:21], v[24:25]
	v_pk_add_f32 v[24:25], v[34:35], v[18:19] neg_lo:[0,1] neg_hi:[0,1]
	s_nop 0
	v_pk_add_f32 v[6:7], v[6:7], v[24:25]
	v_pk_add_f32 v[24:25], v[30:31], v[20:21]
	s_nop 0
	v_pk_add_f32 v[32:33], v[18:19], v[24:25] neg_lo:[0,1] neg_hi:[0,1]
	v_pk_add_f32 v[30:31], v[24:25], v[30:31] neg_lo:[0,1] neg_hi:[0,1]
	v_pk_add_f32 v[18:19], v[18:19], v[32:33] neg_lo:[0,1] neg_hi:[0,1]
	s_nop 0
	v_pk_add_f32 v[18:19], v[18:19], v[24:25] neg_lo:[0,1] neg_hi:[0,1]
	s_nop 0
	v_pk_add_f32 v[6:7], v[6:7], v[18:19]
	v_pk_add_f32 v[18:19], v[30:31], v[20:21] neg_lo:[0,1] neg_hi:[0,1]
	s_nop 0
	v_pk_add_f32 v[6:7], v[18:19], v[6:7]
	v_pk_add_f32 v[18:19], v[22:23], v[28:29]
	v_pk_add_f32 v[6:7], v[32:33], v[6:7]
	v_pk_add_f32 v[20:21], v[18:19], v[22:23] neg_lo:[0,1] neg_hi:[0,1]
	v_pk_mul_f32 v[6:7], v[26:27], v[6:7]
	v_pk_add_f32 v[20:21], v[28:29], v[20:21] neg_lo:[0,1] neg_hi:[0,1]
	s_nop 0
	v_pk_add_f32 v[6:7], v[20:21], v[6:7]
	s_nop 0
	v_pk_add_f32 v[20:21], v[18:19], v[6:7]
	s_nop 0
	v_pk_mul_f32 v[22:23], v[20:21], v[20:21]
	v_pk_add_f32 v[18:19], v[20:21], v[18:19] neg_lo:[0,1] neg_hi:[0,1]
	v_pk_fma_f32 v[24:25], v[22:23], s[48:49], v[12:13] op_sel_hi:[1,0,0]
	v_pk_add_f32 v[6:7], v[6:7], v[18:19] neg_lo:[0,1] neg_hi:[0,1]
	v_ldexp_f32 v18, v20, 1
	v_pk_fma_f32 v[24:25], v[22:23], v[24:25], s[50:51] op_sel_hi:[1,1,0]
	v_ldexp_f32 v19, v21, 1
	v_pk_mul_f32 v[20:21], v[20:21], v[22:23]
	v_cvt_f32_i32_e32 v23, v69
	v_cvt_f32_i32_e32 v22, v68
	v_pk_mul_f32 v[20:21], v[20:21], v[24:25]
	v_ldexp_f32 v27, v7, 1
	v_pk_add_f32 v[24:25], v[18:19], v[20:21]
	v_pk_mul_f32 v[28:29], v[22:23], s[52:53] op_sel_hi:[1,0]
	v_pk_add_f32 v[18:19], v[24:25], v[18:19] neg_lo:[0,1] neg_hi:[0,1]
	v_pk_fma_f32 v[30:31], v[22:23], s[52:53], v[28:29] op_sel_hi:[1,0,1] neg_lo:[0,0,1] neg_hi:[0,0,1]
	v_pk_add_f32 v[18:19], v[20:21], v[18:19] neg_lo:[0,1] neg_hi:[0,1]
	v_pk_fma_f32 v[22:23], v[22:23], s[54:55], v[30:31] op_sel_hi:[1,0,1]
	v_ldexp_f32 v6, v6, 1
	v_mov_b32_e32 v20, v28
	v_mov_b32_e32 v21, v19
	v_mov_b32_e32 v26, v22
	v_mov_b32_e32 v7, v27
	v_pk_add_f32 v[20:21], v[20:21], v[26:27]
	v_pk_add_f32 v[26:27], v[6:7], v[18:19]
	v_mov_b32_e32 v19, v25
	v_mov_b32_e32 v7, v27
	v_pk_add_f32 v[30:31], v[28:29], v[22:23]
	v_pk_add_f32 v[6:7], v[6:7], v[18:19]
	v_pk_add_f32 v[18:19], v[24:25], v[26:27]
	v_mov_b32_e32 v72, v24
	v_pk_add_f32 v[32:33], v[30:31], v[18:19]
	v_mov_b32_e32 v70, v18
	v_mov_b32_e32 v71, v33
	v_mov_b32_e32 v73, v31
	v_pk_add_f32 v[70:71], v[70:71], v[72:73] neg_lo:[0,1] neg_hi:[0,1]
	v_mov_b32_e32 v34, v32
	v_mov_b32_e32 v35, v31
	v_mov_b32_e32 v68, v30
	v_mov_b32_e32 v69, v29
	v_mov_b32_e32 v72, v30
	v_mov_b32_e32 v73, v33
	v_mov_b32_e32 v29, v71
	v_pk_add_f32 v[34:35], v[34:35], v[68:69] neg_lo:[0,1] neg_hi:[0,1]
	v_mov_b32_e32 v68, v18
	v_mov_b32_e32 v69, v23
	v_pk_add_f32 v[28:29], v[72:73], v[28:29] neg_lo:[0,1] neg_hi:[0,1]
	v_pk_add_f32 v[68:69], v[68:69], v[34:35] neg_lo:[0,1] neg_hi:[0,1]
	v_mov_b32_e32 v72, v28
	v_mov_b32_e32 v73, v35
	v_mov_b32_e32 v74, v32
	v_mov_b32_e32 v75, v19
	v_mov_b32_e32 v35, v25
	v_pk_add_f32 v[72:73], v[22:23], v[72:73] neg_lo:[0,1] neg_hi:[0,1]
	v_pk_add_f32 v[34:35], v[74:75], v[34:35] neg_lo:[0,1] neg_hi:[0,1]
	v_mov_b32_e32 v23, v31
	v_pk_add_f32 v[20:21], v[20:21], v[34:35] neg_lo:[0,1] neg_hi:[0,1]
	v_pk_add_f32 v[22:23], v[22:23], v[28:29] neg_lo:[0,1] neg_hi:[0,1]
	v_pk_add_f32 v[6:7], v[6:7], v[70:71] neg_lo:[0,1] neg_hi:[0,1]
	v_pk_add_f32 v[18:19], v[18:19], v[24:25] neg_lo:[0,1] neg_hi:[0,1]
	v_pk_add_f32 v[24:25], v[6:7], v[22:23]
	v_mov_b32_e32 v23, v69
	v_mov_b32_e32 v7, v21
	v_pk_add_f32 v[18:19], v[26:27], v[18:19] neg_lo:[0,1] neg_hi:[0,1]
	v_pk_add_f32 v[26:27], v[68:69], v[20:21]
	v_pk_add_f32 v[6:7], v[22:23], v[6:7]
	v_mov_b32_e32 v20, v24
	v_pk_add_f32 v[6:7], v[6:7], v[72:73] neg_lo:[0,1] neg_hi:[0,1]
	v_mov_b32_e32 v21, v27
	v_pk_add_f32 v[20:21], v[20:21], v[6:7] neg_lo:[0,1] neg_hi:[0,1]
	v_pk_add_f32 v[6:7], v[18:19], v[6:7] neg_lo:[0,1] neg_hi:[0,1]
	v_pk_add_f32 v[20:21], v[22:23], v[20:21] neg_lo:[0,1] neg_hi:[0,1]
	v_pk_add_f32 v[18:19], v[26:27], v[24:25]
	v_pk_add_f32 v[6:7], v[6:7], v[20:21]
	v_pk_add_f32 v[20:21], v[32:33], v[18:19]
	s_nop 0
	v_pk_add_f32 v[22:23], v[20:21], v[32:33] neg_lo:[0,1] neg_hi:[0,1]
	s_nop 0
	v_pk_add_f32 v[18:19], v[18:19], v[22:23] neg_lo:[0,1] neg_hi:[0,1]
	s_nop 0
	v_pk_add_f32 v[6:7], v[6:7], v[18:19]
	s_nop 0
	v_pk_add_f32 v[6:7], v[20:21], v[6:7]
	s_nop 0
	v_cndmask_b32_e32 v6, v214, v6, vcc
	v_cmp_neq_f32_e32 vcc, s21, v77
	s_nop 1
	v_cndmask_b32_e32 v7, v214, v7, vcc
	v_cmp_ngt_f32_e32 vcc, -1.0, v77
	s_nop 1
	v_cndmask_b32_e32 v7, v215, v7, vcc
	v_cmp_ngt_f32_e32 vcc, -1.0, v76
	s_nop 1
	v_cndmask_b32_e32 v6, v215, v6, vcc
	v_cmp_neq_f32_e32 vcc, -1.0, v76
	s_nop 1
	v_cndmask_b32_e32 v6, v216, v6, vcc
	v_cmp_neq_f32_e32 vcc, -1.0, v77
	s_nop 1
	v_cndmask_b32_e32 v7, v216, v7, vcc
	v_cmp_lt_f32_e64 vcc, |v76|, s23
	v_cndmask_b32_e64 v7, v7, v77, s[0:1]
	s_nop 0
	v_cndmask_b32_e32 v6, v6, v76, vcc
	v_pk_add_f32 v[6:7], v[16:17], v[6:7] neg_lo:[0,1] neg_hi:[0,1]
	global_store_dwordx4 v[14:15], v[8:11], off offset:1536
	global_store_dwordx4 v[14:15], v[4:7], off offset:1552
	s_nop 1
	v_mov_b32_e32 v4, v164
	v_mov_b32_e32 v5, v165
	v_mov_b32_e32 v6, v166
	v_mov_b32_e32 v7, v167
	v_fmamk_f32 v8, v60, 0x3c800000, v4
	v_min_f32_e32 v4, 0, v8
	v_mul_f32_e64 v8, |v8|, s6
	v_exp_f32_e32 v74, v8
	v_fmamk_f32 v17, v61, 0x3c800000, v5
	v_min_f32_e32 v5, 0, v17
	v_mul_f32_e64 v17, |v17|, s6
	v_exp_f32_e32 v75, v17
	v_add_f32_e32 v10, 1.0, v74
	v_add_f32_e32 v8, -1.0, v10
	v_sub_f32_e32 v9, v8, v10
	v_add_f32_e32 v9, 1.0, v9
	v_sub_f32_e32 v8, v74, v8
	v_add_f32_e32 v17, 1.0, v75
	v_add_f32_e32 v11, v8, v9
	v_frexp_mant_f32_e32 v8, v10
	v_add_f32_e32 v19, -1.0, v17
	v_cmp_gt_f32_e32 vcc, s7, v8
	v_cvt_f64_f32_e32 v[8:9], v10
	v_sub_f32_e32 v20, v19, v17
	v_frexp_exp_i32_f64_e32 v8, v[8:9]
	v_add_f32_e32 v20, 1.0, v20
	v_sub_f32_e32 v19, v75, v19
	v_subbrev_co_u32_e32 v60, vcc, 0, v8, vcc
	v_add_f32_e32 v19, v19, v20
	v_frexp_mant_f32_e32 v20, v17
	v_cmp_gt_f32_e32 vcc, s7, v20
	v_cvt_f64_f32_e32 v[20:21], v17
	v_frexp_exp_i32_f64_e32 v20, v[20:21]
	v_subbrev_co_u32_e32 v61, vcc, 0, v20, vcc
	v_sub_u32_e32 v8, 0, v60
	v_sub_u32_e32 v20, 0, v61
	v_ldexp_f32 v16, v10, v8
	v_ldexp_f32 v17, v17, v20
	v_ldexp_f32 v19, v19, v20
	v_pk_add_f32 v[20:21], v[16:17], 1.0 op_sel_hi:[1,0]
	v_ldexp_f32 v18, v11, v8
	v_pk_add_f32 v[22:23], v[20:21], -1.0 op_sel_hi:[1,0]
	v_pk_add_f32 v[28:29], v[16:17], -1.0 op_sel_hi:[1,0]
	v_pk_add_f32 v[22:23], v[16:17], v[22:23] neg_lo:[0,1] neg_hi:[0,1]
	v_pk_add_f32 v[30:31], v[28:29], 1.0 op_sel_hi:[1,0]
	v_pk_add_f32 v[22:23], v[18:19], v[22:23]
	v_pk_add_f32 v[16:17], v[16:17], v[30:31] neg_lo:[0,1] neg_hi:[0,1]
	v_pk_add_f32 v[24:25], v[20:21], v[22:23]
	v_pk_add_f32 v[16:17], v[18:19], v[16:17]
	v_rcp_f32_e32 v26, v24
	v_rcp_f32_e32 v27, v25
	v_pk_add_f32 v[18:19], v[28:29], v[16:17]
	v_pk_add_f32 v[20:21], v[24:25], v[20:21] neg_lo:[0,1] neg_hi:[0,1]
	v_pk_add_f32 v[28:29], v[18:19], v[28:29] neg_lo:[0,1] neg_hi:[0,1]
	v_pk_add_f32 v[20:21], v[22:23], v[20:21] neg_lo:[0,1] neg_hi:[0,1]
	v_pk_mul_f32 v[22:23], v[18:19], v[26:27]
	v_pk_add_f32 v[16:17], v[16:17], v[28:29] neg_lo:[0,1] neg_hi:[0,1]
	v_pk_mul_f32 v[28:29], v[24:25], v[22:23]
	v_cmp_neq_f32_e32 vcc, s21, v74
	v_pk_fma_f32 v[30:31], v[22:23], v[24:25], v[28:29] neg_lo:[0,0,1] neg_hi:[0,0,1]
	v_pk_fma_f32 v[30:31], v[22:23], v[20:21], v[30:31]
	v_cmp_lt_f32_e64 s[0:1], |v75|, s23
	v_pk_add_f32 v[32:33], v[28:29], v[30:31]
	v_fmamk_f32 v6, v62, 0x3c800000, v6
	v_pk_add_f32 v[34:35], v[18:19], v[32:33] neg_lo:[0,1] neg_hi:[0,1]
	v_pk_add_f32 v[28:29], v[32:33], v[28:29] neg_lo:[0,1] neg_hi:[0,1]
	v_pk_add_f32 v[18:19], v[18:19], v[34:35] neg_lo:[0,1] neg_hi:[0,1]
	v_fmac_f32_e32 v7, 0x3c800000, v63
	v_pk_add_f32 v[18:19], v[18:19], v[32:33] neg_lo:[0,1] neg_hi:[0,1]
	v_mov_b32_e32 v8, v244
	v_mov_b32_e32 v9, v245
	v_mov_b32_e32 v10, v246
	v_mov_b32_e32 v11, v247
	v_pk_fma_f32 v[8:9], v[64:65], s[28:29], v[8:9] op_sel_hi:[1,0,1]
	v_pk_add_f32 v[16:17], v[16:17], v[18:19]
	v_pk_add_f32 v[18:19], v[28:29], v[30:31] neg_lo:[0,1] neg_hi:[0,1]
	v_pk_fma_f32 v[10:11], v[66:67], s[28:29], v[10:11] op_sel_hi:[1,0,1]
	v_pk_add_f32 v[16:17], v[18:19], v[16:17]
	s_nop 0
	v_pk_add_f32 v[18:19], v[34:35], v[16:17]
	s_nop 0
	v_pk_mul_f32 v[28:29], v[26:27], v[18:19]
	s_nop 0
	v_pk_mul_f32 v[30:31], v[24:25], v[28:29]
	s_nop 0
	v_pk_fma_f32 v[24:25], v[28:29], v[24:25], v[30:31] neg_lo:[0,0,1] neg_hi:[0,0,1]
	s_nop 0
	v_pk_fma_f32 v[20:21], v[28:29], v[20:21], v[24:25]
	v_pk_add_f32 v[24:25], v[34:35], v[18:19] neg_lo:[0,1] neg_hi:[0,1]
	s_nop 0
	v_pk_add_f32 v[16:17], v[16:17], v[24:25]
	v_pk_add_f32 v[24:25], v[30:31], v[20:21]
	s_nop 0
	v_pk_add_f32 v[32:33], v[18:19], v[24:25] neg_lo:[0,1] neg_hi:[0,1]
	v_pk_add_f32 v[30:31], v[24:25], v[30:31] neg_lo:[0,1] neg_hi:[0,1]
	v_pk_add_f32 v[18:19], v[18:19], v[32:33] neg_lo:[0,1] neg_hi:[0,1]
	s_nop 0
	v_pk_add_f32 v[18:19], v[18:19], v[24:25] neg_lo:[0,1] neg_hi:[0,1]
	s_nop 0
	v_pk_add_f32 v[16:17], v[16:17], v[18:19]
	v_pk_add_f32 v[18:19], v[30:31], v[20:21] neg_lo:[0,1] neg_hi:[0,1]
	s_nop 0
	v_pk_add_f32 v[16:17], v[18:19], v[16:17]
	v_pk_add_f32 v[18:19], v[22:23], v[28:29]
	v_pk_add_f32 v[16:17], v[32:33], v[16:17]
	v_pk_add_f32 v[20:21], v[18:19], v[22:23] neg_lo:[0,1] neg_hi:[0,1]
	v_pk_mul_f32 v[16:17], v[26:27], v[16:17]
	v_pk_add_f32 v[20:21], v[28:29], v[20:21] neg_lo:[0,1] neg_hi:[0,1]
	s_nop 0
	v_pk_add_f32 v[16:17], v[20:21], v[16:17]
	s_nop 0
	v_pk_add_f32 v[20:21], v[18:19], v[16:17]
	s_nop 0
	v_pk_mul_f32 v[22:23], v[20:21], v[20:21]
	v_pk_add_f32 v[18:19], v[20:21], v[18:19] neg_lo:[0,1] neg_hi:[0,1]
	v_pk_fma_f32 v[24:25], v[22:23], s[48:49], v[12:13] op_sel_hi:[1,0,0]
	v_pk_add_f32 v[16:17], v[16:17], v[18:19] neg_lo:[0,1] neg_hi:[0,1]
	v_ldexp_f32 v18, v20, 1
	v_pk_fma_f32 v[24:25], v[22:23], v[24:25], s[50:51] op_sel_hi:[1,1,0]
	v_ldexp_f32 v19, v21, 1
	v_pk_mul_f32 v[20:21], v[20:21], v[22:23]
	v_cvt_f32_i32_e32 v23, v61
	v_cvt_f32_i32_e32 v22, v60
	v_pk_mul_f32 v[20:21], v[20:21], v[24:25]
	v_ldexp_f32 v27, v17, 1
	v_pk_add_f32 v[24:25], v[18:19], v[20:21]
	v_pk_mul_f32 v[28:29], v[22:23], s[52:53] op_sel_hi:[1,0]
	v_pk_add_f32 v[18:19], v[24:25], v[18:19] neg_lo:[0,1] neg_hi:[0,1]
	v_pk_fma_f32 v[30:31], v[22:23], s[52:53], v[28:29] op_sel_hi:[1,0,1] neg_lo:[0,0,1] neg_hi:[0,0,1]
	v_pk_add_f32 v[18:19], v[20:21], v[18:19] neg_lo:[0,1] neg_hi:[0,1]
	v_pk_fma_f32 v[22:23], v[22:23], s[54:55], v[30:31] op_sel_hi:[1,0,1]
	v_ldexp_f32 v16, v16, 1
	v_mov_b32_e32 v20, v28
	v_mov_b32_e32 v21, v19
	v_mov_b32_e32 v26, v22
	v_mov_b32_e32 v17, v27
	v_pk_add_f32 v[20:21], v[20:21], v[26:27]
	v_pk_add_f32 v[26:27], v[16:17], v[18:19]
	v_mov_b32_e32 v19, v25
	v_mov_b32_e32 v17, v27
	v_pk_add_f32 v[30:31], v[28:29], v[22:23]
	v_pk_add_f32 v[16:17], v[16:17], v[18:19]
	v_pk_add_f32 v[18:19], v[24:25], v[26:27]
	v_mov_b32_e32 v70, v24
	v_pk_add_f32 v[32:33], v[30:31], v[18:19]
	v_mov_b32_e32 v68, v18
	v_mov_b32_e32 v69, v33
	v_mov_b32_e32 v71, v31
	v_pk_add_f32 v[68:69], v[68:69], v[70:71] neg_lo:[0,1] neg_hi:[0,1]
	v_mov_b32_e32 v34, v32
	v_mov_b32_e32 v35, v31
	v_mov_b32_e32 v60, v30
	v_mov_b32_e32 v61, v29
	v_mov_b32_e32 v70, v30
	v_mov_b32_e32 v71, v33
	v_mov_b32_e32 v29, v69
	v_pk_add_f32 v[34:35], v[34:35], v[60:61] neg_lo:[0,1] neg_hi:[0,1]
	v_mov_b32_e32 v60, v18
	v_mov_b32_e32 v61, v23
	v_pk_add_f32 v[28:29], v[70:71], v[28:29] neg_lo:[0,1] neg_hi:[0,1]
	v_pk_add_f32 v[60:61], v[60:61], v[34:35] neg_lo:[0,1] neg_hi:[0,1]
	v_mov_b32_e32 v70, v28
	v_mov_b32_e32 v71, v35
	v_mov_b32_e32 v72, v32
	v_mov_b32_e32 v73, v19
	v_mov_b32_e32 v35, v25
	v_pk_add_f32 v[70:71], v[22:23], v[70:71] neg_lo:[0,1] neg_hi:[0,1]
	v_pk_add_f32 v[34:35], v[72:73], v[34:35] neg_lo:[0,1] neg_hi:[0,1]
	v_mov_b32_e32 v23, v31
	v_pk_add_f32 v[20:21], v[20:21], v[34:35] neg_lo:[0,1] neg_hi:[0,1]
	v_pk_add_f32 v[22:23], v[22:23], v[28:29] neg_lo:[0,1] neg_hi:[0,1]
	v_pk_add_f32 v[16:17], v[16:17], v[68:69] neg_lo:[0,1] neg_hi:[0,1]
	v_pk_add_f32 v[18:19], v[18:19], v[24:25] neg_lo:[0,1] neg_hi:[0,1]
	v_pk_add_f32 v[24:25], v[16:17], v[22:23]
	v_mov_b32_e32 v23, v61
	v_mov_b32_e32 v17, v21
	v_pk_add_f32 v[18:19], v[26:27], v[18:19] neg_lo:[0,1] neg_hi:[0,1]
	v_pk_add_f32 v[26:27], v[60:61], v[20:21]
	v_pk_add_f32 v[16:17], v[22:23], v[16:17]
	v_mov_b32_e32 v20, v24
	v_pk_add_f32 v[16:17], v[16:17], v[70:71] neg_lo:[0,1] neg_hi:[0,1]
	v_mov_b32_e32 v21, v27
	v_pk_add_f32 v[20:21], v[20:21], v[16:17] neg_lo:[0,1] neg_hi:[0,1]
	v_pk_add_f32 v[16:17], v[18:19], v[16:17] neg_lo:[0,1] neg_hi:[0,1]
	v_pk_add_f32 v[20:21], v[22:23], v[20:21] neg_lo:[0,1] neg_hi:[0,1]
	v_pk_add_f32 v[18:19], v[26:27], v[24:25]
	v_pk_add_f32 v[16:17], v[16:17], v[20:21]
	v_pk_add_f32 v[20:21], v[32:33], v[18:19]
	s_nop 0
	v_pk_add_f32 v[22:23], v[20:21], v[32:33] neg_lo:[0,1] neg_hi:[0,1]
	s_nop 0
	v_pk_add_f32 v[18:19], v[18:19], v[22:23] neg_lo:[0,1] neg_hi:[0,1]
	s_nop 0
	v_pk_add_f32 v[16:17], v[16:17], v[18:19]
	s_nop 0
	v_pk_add_f32 v[16:17], v[20:21], v[16:17]
	s_nop 0
	v_cndmask_b32_e32 v16, v214, v16, vcc
	v_cmp_neq_f32_e32 vcc, s21, v75
	s_nop 1
	v_cndmask_b32_e32 v17, v214, v17, vcc
	v_cmp_ngt_f32_e32 vcc, -1.0, v75
	s_nop 1
	v_cndmask_b32_e32 v17, v215, v17, vcc
	v_cmp_ngt_f32_e32 vcc, -1.0, v74
	s_nop 1
	v_cndmask_b32_e32 v16, v215, v16, vcc
	v_cmp_neq_f32_e32 vcc, -1.0, v74
	s_nop 1
	v_cndmask_b32_e32 v16, v216, v16, vcc
	v_cmp_neq_f32_e32 vcc, -1.0, v75
	s_nop 1
	v_cndmask_b32_e32 v17, v216, v17, vcc
	v_cmp_lt_f32_e64 vcc, |v74|, s23
	v_cndmask_b32_e64 v17, v17, v75, s[0:1]
	s_nop 0
	v_cndmask_b32_e32 v16, v16, v74, vcc
	v_pk_add_f32 v[4:5], v[4:5], v[16:17] neg_lo:[0,1] neg_hi:[0,1]
	v_min_f32_e32 v16, 0, v6
	v_mul_f32_e64 v6, |v6|, s6
	v_exp_f32_e32 v68, v6
	s_nop 0
	v_add_f32_e32 v6, 1.0, v68
	v_add_f32_e32 v17, -1.0, v6
	v_sub_f32_e32 v18, v17, v6
	v_add_f32_e32 v18, 1.0, v18
	v_sub_f32_e32 v17, v68, v17
	v_add_f32_e32 v17, v17, v18
	v_frexp_mant_f32_e32 v18, v6
	v_cmp_gt_f32_e32 vcc, s7, v18
	v_cvt_f64_f32_e32 v[18:19], v6
	v_frexp_exp_i32_f64_e32 v18, v[18:19]
	v_subbrev_co_u32_e32 v60, vcc, 0, v18, vcc
	v_sub_u32_e32 v18, 0, v60
	v_ldexp_f32 v6, v6, v18
	v_ldexp_f32 v18, v17, v18
	v_min_f32_e32 v17, 0, v7
	v_mul_f32_e64 v7, |v7|, s6
	v_exp_f32_e32 v69, v7
	s_nop 0
	v_add_f32_e32 v7, 1.0, v69
	v_add_f32_e32 v19, -1.0, v7
	v_sub_f32_e32 v20, v19, v7
	v_add_f32_e32 v20, 1.0, v20
	v_sub_f32_e32 v19, v69, v19
	v_add_f32_e32 v19, v19, v20
	v_frexp_mant_f32_e32 v20, v7
	v_cmp_gt_f32_e32 vcc, s7, v20
	v_cvt_f64_f32_e32 v[20:21], v7
	v_frexp_exp_i32_f64_e32 v20, v[20:21]
	v_subbrev_co_u32_e32 v61, vcc, 0, v20, vcc
	v_sub_u32_e32 v20, 0, v61
	v_ldexp_f32 v7, v7, v20
	v_ldexp_f32 v19, v19, v20
	v_pk_add_f32 v[20:21], v[6:7], 1.0 op_sel_hi:[1,0]
	v_pk_add_f32 v[28:29], v[6:7], -1.0 op_sel_hi:[1,0]
	v_pk_add_f32 v[22:23], v[20:21], -1.0 op_sel_hi:[1,0]
	v_pk_add_f32 v[30:31], v[28:29], 1.0 op_sel_hi:[1,0]
	v_pk_add_f32 v[22:23], v[6:7], v[22:23] neg_lo:[0,1] neg_hi:[0,1]
	v_pk_add_f32 v[6:7], v[6:7], v[30:31] neg_lo:[0,1] neg_hi:[0,1]
	v_pk_add_f32 v[22:23], v[18:19], v[22:23]
	v_pk_add_f32 v[6:7], v[18:19], v[6:7]
	v_pk_add_f32 v[24:25], v[20:21], v[22:23]
	v_pk_add_f32 v[18:19], v[28:29], v[6:7]
	v_rcp_f32_e32 v26, v24
	v_rcp_f32_e32 v27, v25
	v_pk_add_f32 v[20:21], v[24:25], v[20:21] neg_lo:[0,1] neg_hi:[0,1]
	v_pk_add_f32 v[28:29], v[18:19], v[28:29] neg_lo:[0,1] neg_hi:[0,1]
	v_pk_add_f32 v[20:21], v[22:23], v[20:21] neg_lo:[0,1] neg_hi:[0,1]
	v_pk_mul_f32 v[22:23], v[18:19], v[26:27]
	v_pk_add_f32 v[6:7], v[6:7], v[28:29] neg_lo:[0,1] neg_hi:[0,1]
	v_pk_mul_f32 v[28:29], v[24:25], v[22:23]
	v_cmp_neq_f32_e32 vcc, s21, v68
	v_pk_fma_f32 v[30:31], v[22:23], v[24:25], v[28:29] neg_lo:[0,0,1] neg_hi:[0,0,1]
	v_cmp_lt_f32_e64 s[0:1], |v69|, s23
	v_pk_fma_f32 v[30:31], v[22:23], v[20:21], v[30:31]
	s_nop 0
	v_pk_add_f32 v[32:33], v[28:29], v[30:31]
	s_nop 0
	v_pk_add_f32 v[34:35], v[18:19], v[32:33] neg_lo:[0,1] neg_hi:[0,1]
	v_pk_add_f32 v[28:29], v[32:33], v[28:29] neg_lo:[0,1] neg_hi:[0,1]
	v_pk_add_f32 v[18:19], v[18:19], v[34:35] neg_lo:[0,1] neg_hi:[0,1]
	s_nop 0
	v_pk_add_f32 v[18:19], v[18:19], v[32:33] neg_lo:[0,1] neg_hi:[0,1]
	s_nop 0
	v_pk_add_f32 v[6:7], v[6:7], v[18:19]
	v_pk_add_f32 v[18:19], v[28:29], v[30:31] neg_lo:[0,1] neg_hi:[0,1]
	s_nop 0
	v_pk_add_f32 v[6:7], v[18:19], v[6:7]
	s_nop 0
	v_pk_add_f32 v[18:19], v[34:35], v[6:7]
	s_nop 0
	v_pk_mul_f32 v[28:29], v[26:27], v[18:19]
	s_nop 0
	v_pk_mul_f32 v[30:31], v[24:25], v[28:29]
	s_nop 0
	v_pk_fma_f32 v[24:25], v[28:29], v[24:25], v[30:31] neg_lo:[0,0,1] neg_hi:[0,0,1]
	s_nop 0
	v_pk_fma_f32 v[20:21], v[28:29], v[20:21], v[24:25]
	v_pk_add_f32 v[24:25], v[34:35], v[18:19] neg_lo:[0,1] neg_hi:[0,1]
	s_nop 0
	v_pk_add_f32 v[6:7], v[6:7], v[24:25]
	v_pk_add_f32 v[24:25], v[30:31], v[20:21]
	s_nop 0
	v_pk_add_f32 v[32:33], v[18:19], v[24:25] neg_lo:[0,1] neg_hi:[0,1]
	v_pk_add_f32 v[30:31], v[24:25], v[30:31] neg_lo:[0,1] neg_hi:[0,1]
	v_pk_add_f32 v[18:19], v[18:19], v[32:33] neg_lo:[0,1] neg_hi:[0,1]
	s_nop 0
	v_pk_add_f32 v[18:19], v[18:19], v[24:25] neg_lo:[0,1] neg_hi:[0,1]
	s_nop 0
	v_pk_add_f32 v[6:7], v[6:7], v[18:19]
	v_pk_add_f32 v[18:19], v[30:31], v[20:21] neg_lo:[0,1] neg_hi:[0,1]
	s_nop 0
	v_pk_add_f32 v[6:7], v[18:19], v[6:7]
	v_pk_add_f32 v[18:19], v[22:23], v[28:29]
	v_pk_add_f32 v[6:7], v[32:33], v[6:7]
	v_pk_add_f32 v[20:21], v[18:19], v[22:23] neg_lo:[0,1] neg_hi:[0,1]
	v_pk_mul_f32 v[6:7], v[26:27], v[6:7]
	v_pk_add_f32 v[20:21], v[28:29], v[20:21] neg_lo:[0,1] neg_hi:[0,1]
	s_nop 0
	v_pk_add_f32 v[6:7], v[20:21], v[6:7]
	s_nop 0
	v_pk_add_f32 v[20:21], v[18:19], v[6:7]
	s_nop 0
	v_pk_mul_f32 v[22:23], v[20:21], v[20:21]
	v_pk_add_f32 v[18:19], v[20:21], v[18:19] neg_lo:[0,1] neg_hi:[0,1]
	v_pk_fma_f32 v[24:25], v[22:23], s[48:49], v[12:13] op_sel_hi:[1,0,0]
	v_pk_add_f32 v[6:7], v[6:7], v[18:19] neg_lo:[0,1] neg_hi:[0,1]
	v_ldexp_f32 v18, v20, 1
	v_pk_fma_f32 v[24:25], v[22:23], v[24:25], s[50:51] op_sel_hi:[1,1,0]
	v_ldexp_f32 v19, v21, 1
	v_pk_mul_f32 v[20:21], v[20:21], v[22:23]
	v_cvt_f32_i32_e32 v23, v61
	v_cvt_f32_i32_e32 v22, v60
	v_pk_mul_f32 v[20:21], v[20:21], v[24:25]
	v_ldexp_f32 v27, v7, 1
	v_pk_add_f32 v[24:25], v[18:19], v[20:21]
	v_pk_mul_f32 v[28:29], v[22:23], s[52:53] op_sel_hi:[1,0]
	v_pk_add_f32 v[18:19], v[24:25], v[18:19] neg_lo:[0,1] neg_hi:[0,1]
	v_pk_fma_f32 v[30:31], v[22:23], s[52:53], v[28:29] op_sel_hi:[1,0,1] neg_lo:[0,0,1] neg_hi:[0,0,1]
	v_pk_add_f32 v[18:19], v[20:21], v[18:19] neg_lo:[0,1] neg_hi:[0,1]
	v_pk_fma_f32 v[22:23], v[22:23], s[54:55], v[30:31] op_sel_hi:[1,0,1]
	v_ldexp_f32 v6, v6, 1
	v_mov_b32_e32 v20, v28
	v_mov_b32_e32 v21, v19
	v_mov_b32_e32 v26, v22
	v_mov_b32_e32 v7, v27
	v_pk_add_f32 v[20:21], v[20:21], v[26:27]
	v_pk_add_f32 v[26:27], v[6:7], v[18:19]
	v_mov_b32_e32 v19, v25
	v_mov_b32_e32 v7, v27
	v_pk_add_f32 v[30:31], v[28:29], v[22:23]
	v_pk_add_f32 v[6:7], v[6:7], v[18:19]
	v_pk_add_f32 v[18:19], v[24:25], v[26:27]
	v_mov_b32_e32 v64, v24
	v_pk_add_f32 v[32:33], v[30:31], v[18:19]
	v_mov_b32_e32 v62, v18
	v_mov_b32_e32 v63, v33
	v_mov_b32_e32 v65, v31
	v_pk_add_f32 v[62:63], v[62:63], v[64:65] neg_lo:[0,1] neg_hi:[0,1]
	v_mov_b32_e32 v34, v32
	v_mov_b32_e32 v35, v31
	v_mov_b32_e32 v60, v30
	v_mov_b32_e32 v61, v29
	v_mov_b32_e32 v64, v30
	v_mov_b32_e32 v65, v33
	v_mov_b32_e32 v29, v63
	v_pk_add_f32 v[34:35], v[34:35], v[60:61] neg_lo:[0,1] neg_hi:[0,1]
	v_mov_b32_e32 v60, v18
	v_mov_b32_e32 v61, v23
	v_pk_add_f32 v[28:29], v[64:65], v[28:29] neg_lo:[0,1] neg_hi:[0,1]
	v_pk_add_f32 v[60:61], v[60:61], v[34:35] neg_lo:[0,1] neg_hi:[0,1]
	v_mov_b32_e32 v64, v28
	v_mov_b32_e32 v65, v35
	v_mov_b32_e32 v66, v32
	v_mov_b32_e32 v67, v19
	v_mov_b32_e32 v35, v25
	v_pk_add_f32 v[64:65], v[22:23], v[64:65] neg_lo:[0,1] neg_hi:[0,1]
	v_pk_add_f32 v[34:35], v[66:67], v[34:35] neg_lo:[0,1] neg_hi:[0,1]
	v_mov_b32_e32 v23, v31
	v_pk_add_f32 v[20:21], v[20:21], v[34:35] neg_lo:[0,1] neg_hi:[0,1]
	v_pk_add_f32 v[22:23], v[22:23], v[28:29] neg_lo:[0,1] neg_hi:[0,1]
	v_pk_add_f32 v[6:7], v[6:7], v[62:63] neg_lo:[0,1] neg_hi:[0,1]
	v_pk_add_f32 v[18:19], v[18:19], v[24:25] neg_lo:[0,1] neg_hi:[0,1]
	v_pk_add_f32 v[24:25], v[6:7], v[22:23]
	v_mov_b32_e32 v23, v61
	v_mov_b32_e32 v7, v21
	v_pk_add_f32 v[18:19], v[26:27], v[18:19] neg_lo:[0,1] neg_hi:[0,1]
	v_pk_add_f32 v[26:27], v[60:61], v[20:21]
	v_pk_add_f32 v[6:7], v[22:23], v[6:7]
	v_mov_b32_e32 v20, v24
	v_pk_add_f32 v[6:7], v[6:7], v[64:65] neg_lo:[0,1] neg_hi:[0,1]
	v_mov_b32_e32 v21, v27
	v_pk_add_f32 v[20:21], v[20:21], v[6:7] neg_lo:[0,1] neg_hi:[0,1]
	v_pk_add_f32 v[6:7], v[18:19], v[6:7] neg_lo:[0,1] neg_hi:[0,1]
	v_pk_add_f32 v[20:21], v[22:23], v[20:21] neg_lo:[0,1] neg_hi:[0,1]
	v_pk_add_f32 v[18:19], v[26:27], v[24:25]
	v_pk_add_f32 v[6:7], v[6:7], v[20:21]
	v_pk_add_f32 v[20:21], v[32:33], v[18:19]
	s_nop 0
	v_pk_add_f32 v[22:23], v[20:21], v[32:33] neg_lo:[0,1] neg_hi:[0,1]
	s_nop 0
	v_pk_add_f32 v[18:19], v[18:19], v[22:23] neg_lo:[0,1] neg_hi:[0,1]
	s_nop 0
	v_pk_add_f32 v[6:7], v[6:7], v[18:19]
	s_nop 0
	v_pk_add_f32 v[6:7], v[20:21], v[6:7]
	s_nop 0
	v_cndmask_b32_e32 v6, v214, v6, vcc
	v_cmp_neq_f32_e32 vcc, s21, v69
	s_nop 1
	v_cndmask_b32_e32 v7, v214, v7, vcc
	v_cmp_ngt_f32_e32 vcc, -1.0, v69
	s_nop 1
	v_cndmask_b32_e32 v7, v215, v7, vcc
	v_cmp_ngt_f32_e32 vcc, -1.0, v68
	s_nop 1
	v_cndmask_b32_e32 v6, v215, v6, vcc
	v_cmp_neq_f32_e32 vcc, -1.0, v68
	s_nop 1
	v_cndmask_b32_e32 v6, v216, v6, vcc
	v_cmp_neq_f32_e32 vcc, -1.0, v69
	s_nop 1
	v_cndmask_b32_e32 v7, v216, v7, vcc
	v_cmp_lt_f32_e64 vcc, |v68|, s23
	v_cndmask_b32_e64 v7, v7, v69, s[0:1]
	s_mov_b64 s[0:1], 0x1000
	v_cndmask_b32_e32 v6, v6, v68, vcc
	v_lshl_add_u64 v[18:19], v[14:15], 0, s[0:1]
	s_movk_i32 s0, 0x1000
	v_pk_add_f32 v[6:7], v[16:17], v[6:7] neg_lo:[0,1] neg_hi:[0,1]
	v_add_co_u32_e32 v16, vcc, s0, v14
	s_nop 1
	v_addc_co_u32_e32 v17, vcc, 0, v15, vcc
	global_store_dwordx4 v[16:17], v[8:11], off
	global_store_dwordx4 v[18:19], v[4:7], off offset:16
	s_nop 1
	v_mov_b32_e32 v4, v164
	v_mov_b32_e32 v5, v165
	v_mov_b32_e32 v6, v166
	v_mov_b32_e32 v7, v167
	v_fmamk_f32 v8, v52, 0x3c800000, v4
	v_min_f32_e32 v4, 0, v8
	v_mul_f32_e64 v8, |v8|, s6
	v_exp_f32_e32 v68, v8
	v_fmamk_f32 v19, v53, 0x3c800000, v5
	v_min_f32_e32 v5, 0, v19
	v_mul_f32_e64 v19, |v19|, s6
	v_exp_f32_e32 v69, v19
	v_add_f32_e32 v10, 1.0, v68
	v_add_f32_e32 v8, -1.0, v10
	v_sub_f32_e32 v9, v8, v10
	v_add_f32_e32 v9, 1.0, v9
	v_sub_f32_e32 v8, v68, v8
	v_add_f32_e32 v19, 1.0, v69
	v_add_f32_e32 v11, v8, v9
	v_frexp_mant_f32_e32 v8, v10
	v_add_f32_e32 v21, -1.0, v19
	v_cmp_gt_f32_e32 vcc, s7, v8
	v_cvt_f64_f32_e32 v[8:9], v10
	v_sub_f32_e32 v22, v21, v19
	v_frexp_exp_i32_f64_e32 v8, v[8:9]
	v_add_f32_e32 v22, 1.0, v22
	v_sub_f32_e32 v21, v69, v21
	v_subbrev_co_u32_e32 v60, vcc, 0, v8, vcc
	v_add_f32_e32 v21, v21, v22
	v_frexp_mant_f32_e32 v22, v19
	v_cmp_gt_f32_e32 vcc, s7, v22
	v_cvt_f64_f32_e32 v[22:23], v19
	v_frexp_exp_i32_f64_e32 v22, v[22:23]
	v_subbrev_co_u32_e32 v61, vcc, 0, v22, vcc
	v_sub_u32_e32 v8, 0, v60
	v_sub_u32_e32 v22, 0, v61
	v_ldexp_f32 v18, v10, v8
	v_ldexp_f32 v19, v19, v22
	v_ldexp_f32 v21, v21, v22
	v_pk_add_f32 v[22:23], v[18:19], 1.0 op_sel_hi:[1,0]
	v_ldexp_f32 v20, v11, v8
	v_pk_add_f32 v[24:25], v[22:23], -1.0 op_sel_hi:[1,0]
	v_pk_add_f32 v[30:31], v[18:19], -1.0 op_sel_hi:[1,0]
	v_pk_add_f32 v[24:25], v[18:19], v[24:25] neg_lo:[0,1] neg_hi:[0,1]
	v_pk_add_f32 v[32:33], v[30:31], 1.0 op_sel_hi:[1,0]
	v_pk_add_f32 v[24:25], v[20:21], v[24:25]
	v_pk_add_f32 v[18:19], v[18:19], v[32:33] neg_lo:[0,1] neg_hi:[0,1]
	v_pk_add_f32 v[26:27], v[22:23], v[24:25]
	v_pk_add_f32 v[18:19], v[20:21], v[18:19]
	v_rcp_f32_e32 v28, v26
	v_rcp_f32_e32 v29, v27
	v_pk_add_f32 v[20:21], v[30:31], v[18:19]
	v_pk_add_f32 v[22:23], v[26:27], v[22:23] neg_lo:[0,1] neg_hi:[0,1]
	v_pk_add_f32 v[30:31], v[20:21], v[30:31] neg_lo:[0,1] neg_hi:[0,1]
	v_pk_add_f32 v[22:23], v[24:25], v[22:23] neg_lo:[0,1] neg_hi:[0,1]
	v_pk_mul_f32 v[24:25], v[20:21], v[28:29]
	v_pk_add_f32 v[18:19], v[18:19], v[30:31] neg_lo:[0,1] neg_hi:[0,1]
	v_pk_mul_f32 v[30:31], v[26:27], v[24:25]
	v_cmp_neq_f32_e32 vcc, s21, v68
	v_pk_fma_f32 v[32:33], v[24:25], v[26:27], v[30:31] neg_lo:[0,0,1] neg_hi:[0,0,1]
	v_pk_fma_f32 v[32:33], v[24:25], v[22:23], v[32:33]
	v_cmp_lt_f32_e64 s[0:1], |v69|, s23
	v_pk_add_f32 v[34:35], v[30:31], v[32:33]
	v_fmamk_f32 v6, v54, 0x3c800000, v6
	v_pk_add_f32 v[52:53], v[20:21], v[34:35] neg_lo:[0,1] neg_hi:[0,1]
	v_pk_add_f32 v[30:31], v[34:35], v[30:31] neg_lo:[0,1] neg_hi:[0,1]
	v_pk_add_f32 v[20:21], v[20:21], v[52:53] neg_lo:[0,1] neg_hi:[0,1]
	v_fmac_f32_e32 v7, 0x3c800000, v55
	v_pk_add_f32 v[20:21], v[20:21], v[34:35] neg_lo:[0,1] neg_hi:[0,1]
	v_mov_b32_e32 v8, v244
	v_mov_b32_e32 v9, v245
	v_mov_b32_e32 v10, v246
	v_mov_b32_e32 v11, v247
	v_pk_fma_f32 v[8:9], v[56:57], s[28:29], v[8:9] op_sel_hi:[1,0,1]
	v_pk_add_f32 v[18:19], v[18:19], v[20:21]
	v_pk_add_f32 v[20:21], v[30:31], v[32:33] neg_lo:[0,1] neg_hi:[0,1]
	v_pk_fma_f32 v[10:11], v[58:59], s[28:29], v[10:11] op_sel_hi:[1,0,1]
	v_pk_add_f32 v[18:19], v[20:21], v[18:19]
	s_nop 0
	v_pk_add_f32 v[20:21], v[52:53], v[18:19]
	s_nop 0
	v_pk_mul_f32 v[30:31], v[28:29], v[20:21]
	s_nop 0
	v_pk_mul_f32 v[32:33], v[26:27], v[30:31]
	s_nop 0
	v_pk_fma_f32 v[26:27], v[30:31], v[26:27], v[32:33] neg_lo:[0,0,1] neg_hi:[0,0,1]
	s_nop 0
	v_pk_fma_f32 v[22:23], v[30:31], v[22:23], v[26:27]
	v_pk_add_f32 v[26:27], v[52:53], v[20:21] neg_lo:[0,1] neg_hi:[0,1]
	s_nop 0
	v_pk_add_f32 v[18:19], v[18:19], v[26:27]
	v_pk_add_f32 v[26:27], v[32:33], v[22:23]
	s_nop 0
	v_pk_add_f32 v[34:35], v[20:21], v[26:27] neg_lo:[0,1] neg_hi:[0,1]
	v_pk_add_f32 v[32:33], v[26:27], v[32:33] neg_lo:[0,1] neg_hi:[0,1]
	v_pk_add_f32 v[20:21], v[20:21], v[34:35] neg_lo:[0,1] neg_hi:[0,1]
	s_nop 0
	v_pk_add_f32 v[20:21], v[20:21], v[26:27] neg_lo:[0,1] neg_hi:[0,1]
	s_nop 0
	v_pk_add_f32 v[18:19], v[18:19], v[20:21]
	v_pk_add_f32 v[20:21], v[32:33], v[22:23] neg_lo:[0,1] neg_hi:[0,1]
	s_nop 0
	v_pk_add_f32 v[18:19], v[20:21], v[18:19]
	v_pk_add_f32 v[20:21], v[24:25], v[30:31]
	v_pk_add_f32 v[18:19], v[34:35], v[18:19]
	v_pk_add_f32 v[22:23], v[20:21], v[24:25] neg_lo:[0,1] neg_hi:[0,1]
	v_pk_mul_f32 v[18:19], v[28:29], v[18:19]
	v_pk_add_f32 v[22:23], v[30:31], v[22:23] neg_lo:[0,1] neg_hi:[0,1]
	s_nop 0
	v_pk_add_f32 v[18:19], v[22:23], v[18:19]
	s_nop 0
	v_pk_add_f32 v[22:23], v[20:21], v[18:19]
	s_nop 0
	v_pk_mul_f32 v[24:25], v[22:23], v[22:23]
	v_pk_add_f32 v[20:21], v[22:23], v[20:21] neg_lo:[0,1] neg_hi:[0,1]
	v_pk_fma_f32 v[26:27], v[24:25], s[48:49], v[12:13] op_sel_hi:[1,0,0]
	v_pk_add_f32 v[18:19], v[18:19], v[20:21] neg_lo:[0,1] neg_hi:[0,1]
	v_ldexp_f32 v20, v22, 1
	v_pk_fma_f32 v[26:27], v[24:25], v[26:27], s[50:51] op_sel_hi:[1,1,0]
	v_ldexp_f32 v21, v23, 1
	v_pk_mul_f32 v[22:23], v[22:23], v[24:25]
	v_cvt_f32_i32_e32 v25, v61
	v_cvt_f32_i32_e32 v24, v60
	v_pk_mul_f32 v[22:23], v[22:23], v[26:27]
	v_ldexp_f32 v29, v19, 1
	v_pk_add_f32 v[26:27], v[20:21], v[22:23]
	v_pk_mul_f32 v[30:31], v[24:25], s[52:53] op_sel_hi:[1,0]
	v_pk_add_f32 v[20:21], v[26:27], v[20:21] neg_lo:[0,1] neg_hi:[0,1]
	v_pk_fma_f32 v[32:33], v[24:25], s[52:53], v[30:31] op_sel_hi:[1,0,1] neg_lo:[0,0,1] neg_hi:[0,0,1]
	v_pk_add_f32 v[20:21], v[22:23], v[20:21] neg_lo:[0,1] neg_hi:[0,1]
	v_pk_fma_f32 v[24:25], v[24:25], s[54:55], v[32:33] op_sel_hi:[1,0,1]
	v_ldexp_f32 v18, v18, 1
	v_mov_b32_e32 v22, v30
	v_mov_b32_e32 v23, v21
	v_mov_b32_e32 v28, v24
	v_mov_b32_e32 v19, v29
	v_pk_add_f32 v[22:23], v[22:23], v[28:29]
	v_pk_add_f32 v[28:29], v[18:19], v[20:21]
	v_mov_b32_e32 v21, v27
	v_mov_b32_e32 v19, v29
	v_pk_add_f32 v[32:33], v[30:31], v[24:25]
	v_pk_add_f32 v[18:19], v[18:19], v[20:21]
	v_pk_add_f32 v[20:21], v[26:27], v[28:29]
	v_mov_b32_e32 v64, v26
	v_pk_add_f32 v[34:35], v[32:33], v[20:21]
	v_mov_b32_e32 v62, v20
	v_mov_b32_e32 v63, v35
	v_mov_b32_e32 v65, v33
	v_pk_add_f32 v[62:63], v[62:63], v[64:65] neg_lo:[0,1] neg_hi:[0,1]
	v_mov_b32_e32 v52, v34
	v_mov_b32_e32 v53, v33
	v_mov_b32_e32 v60, v32
	v_mov_b32_e32 v61, v31
	v_mov_b32_e32 v64, v32
	v_mov_b32_e32 v65, v35
	v_mov_b32_e32 v31, v63
	v_pk_add_f32 v[52:53], v[52:53], v[60:61] neg_lo:[0,1] neg_hi:[0,1]
	v_mov_b32_e32 v60, v20
	v_mov_b32_e32 v61, v25
	v_pk_add_f32 v[30:31], v[64:65], v[30:31] neg_lo:[0,1] neg_hi:[0,1]
	v_pk_add_f32 v[60:61], v[60:61], v[52:53] neg_lo:[0,1] neg_hi:[0,1]
	v_mov_b32_e32 v64, v30
	v_mov_b32_e32 v65, v53
	v_mov_b32_e32 v66, v34
	v_mov_b32_e32 v67, v21
	v_mov_b32_e32 v53, v27
	v_pk_add_f32 v[64:65], v[24:25], v[64:65] neg_lo:[0,1] neg_hi:[0,1]
	v_pk_add_f32 v[52:53], v[66:67], v[52:53] neg_lo:[0,1] neg_hi:[0,1]
	v_mov_b32_e32 v25, v33
	v_pk_add_f32 v[22:23], v[22:23], v[52:53] neg_lo:[0,1] neg_hi:[0,1]
	v_pk_add_f32 v[24:25], v[24:25], v[30:31] neg_lo:[0,1] neg_hi:[0,1]
	v_pk_add_f32 v[18:19], v[18:19], v[62:63] neg_lo:[0,1] neg_hi:[0,1]
	v_pk_add_f32 v[20:21], v[20:21], v[26:27] neg_lo:[0,1] neg_hi:[0,1]
	v_pk_add_f32 v[26:27], v[18:19], v[24:25]
	v_mov_b32_e32 v25, v61
	v_mov_b32_e32 v19, v23
	v_pk_add_f32 v[20:21], v[28:29], v[20:21] neg_lo:[0,1] neg_hi:[0,1]
	v_pk_add_f32 v[28:29], v[60:61], v[22:23]
	v_pk_add_f32 v[18:19], v[24:25], v[18:19]
	v_mov_b32_e32 v22, v26
	v_pk_add_f32 v[18:19], v[18:19], v[64:65] neg_lo:[0,1] neg_hi:[0,1]
	v_mov_b32_e32 v23, v29
	v_pk_add_f32 v[22:23], v[22:23], v[18:19] neg_lo:[0,1] neg_hi:[0,1]
	v_pk_add_f32 v[18:19], v[20:21], v[18:19] neg_lo:[0,1] neg_hi:[0,1]
	v_pk_add_f32 v[22:23], v[24:25], v[22:23] neg_lo:[0,1] neg_hi:[0,1]
	v_pk_add_f32 v[20:21], v[28:29], v[26:27]
	v_pk_add_f32 v[18:19], v[18:19], v[22:23]
	v_pk_add_f32 v[22:23], v[34:35], v[20:21]
	s_nop 0
	v_pk_add_f32 v[24:25], v[22:23], v[34:35] neg_lo:[0,1] neg_hi:[0,1]
	s_nop 0
	v_pk_add_f32 v[20:21], v[20:21], v[24:25] neg_lo:[0,1] neg_hi:[0,1]
	s_nop 0
	v_pk_add_f32 v[18:19], v[18:19], v[20:21]
	s_nop 0
	v_pk_add_f32 v[18:19], v[22:23], v[18:19]
	s_nop 0
	v_cndmask_b32_e32 v18, v214, v18, vcc
	v_cmp_neq_f32_e32 vcc, s21, v69
	s_nop 1
	v_cndmask_b32_e32 v19, v214, v19, vcc
	v_cmp_ngt_f32_e32 vcc, -1.0, v69
	s_nop 1
	v_cndmask_b32_e32 v19, v215, v19, vcc
	v_cmp_ngt_f32_e32 vcc, -1.0, v68
	s_nop 1
	v_cndmask_b32_e32 v18, v215, v18, vcc
	v_cmp_neq_f32_e32 vcc, -1.0, v68
	s_nop 1
	v_cndmask_b32_e32 v18, v216, v18, vcc
	v_cmp_neq_f32_e32 vcc, -1.0, v69
	s_nop 1
	v_cndmask_b32_e32 v19, v216, v19, vcc
	v_cmp_lt_f32_e64 vcc, |v68|, s23
	v_cndmask_b32_e64 v19, v19, v69, s[0:1]
	s_nop 0
	v_cndmask_b32_e32 v18, v18, v68, vcc
	v_pk_add_f32 v[4:5], v[4:5], v[18:19] neg_lo:[0,1] neg_hi:[0,1]
	v_min_f32_e32 v18, 0, v6
	v_mul_f32_e64 v6, |v6|, s6
	v_exp_f32_e32 v62, v6
	s_nop 0
	v_add_f32_e32 v6, 1.0, v62
	v_add_f32_e32 v19, -1.0, v6
	v_sub_f32_e32 v20, v19, v6
	v_add_f32_e32 v20, 1.0, v20
	v_sub_f32_e32 v19, v62, v19
	v_add_f32_e32 v19, v19, v20
	v_frexp_mant_f32_e32 v20, v6
	v_cmp_gt_f32_e32 vcc, s7, v20
	v_cvt_f64_f32_e32 v[20:21], v6
	v_frexp_exp_i32_f64_e32 v20, v[20:21]
	v_subbrev_co_u32_e32 v54, vcc, 0, v20, vcc
	v_sub_u32_e32 v20, 0, v54
	v_ldexp_f32 v6, v6, v20
	v_ldexp_f32 v20, v19, v20
	v_min_f32_e32 v19, 0, v7
	v_mul_f32_e64 v7, |v7|, s6
	v_exp_f32_e32 v63, v7
	s_nop 0
	v_add_f32_e32 v7, 1.0, v63
	v_add_f32_e32 v21, -1.0, v7
	v_sub_f32_e32 v22, v21, v7
	v_add_f32_e32 v22, 1.0, v22
	v_sub_f32_e32 v21, v63, v21
	v_add_f32_e32 v21, v21, v22
	v_frexp_mant_f32_e32 v22, v7
	v_cmp_gt_f32_e32 vcc, s7, v22
	v_cvt_f64_f32_e32 v[22:23], v7
	v_frexp_exp_i32_f64_e32 v22, v[22:23]
	v_subbrev_co_u32_e32 v55, vcc, 0, v22, vcc
	v_sub_u32_e32 v22, 0, v55
	v_ldexp_f32 v7, v7, v22
	v_ldexp_f32 v21, v21, v22
	v_pk_add_f32 v[22:23], v[6:7], 1.0 op_sel_hi:[1,0]
	v_pk_add_f32 v[30:31], v[6:7], -1.0 op_sel_hi:[1,0]
	v_pk_add_f32 v[24:25], v[22:23], -1.0 op_sel_hi:[1,0]
	v_pk_add_f32 v[32:33], v[30:31], 1.0 op_sel_hi:[1,0]
	v_pk_add_f32 v[24:25], v[6:7], v[24:25] neg_lo:[0,1] neg_hi:[0,1]
	v_pk_add_f32 v[6:7], v[6:7], v[32:33] neg_lo:[0,1] neg_hi:[0,1]
	v_pk_add_f32 v[24:25], v[20:21], v[24:25]
	v_pk_add_f32 v[6:7], v[20:21], v[6:7]
	v_pk_add_f32 v[26:27], v[22:23], v[24:25]
	v_pk_add_f32 v[20:21], v[30:31], v[6:7]
	v_rcp_f32_e32 v28, v26
	v_rcp_f32_e32 v29, v27
	v_pk_add_f32 v[22:23], v[26:27], v[22:23] neg_lo:[0,1] neg_hi:[0,1]
	v_pk_add_f32 v[30:31], v[20:21], v[30:31] neg_lo:[0,1] neg_hi:[0,1]
	v_pk_add_f32 v[22:23], v[24:25], v[22:23] neg_lo:[0,1] neg_hi:[0,1]
	v_pk_mul_f32 v[24:25], v[20:21], v[28:29]
	v_pk_add_f32 v[6:7], v[6:7], v[30:31] neg_lo:[0,1] neg_hi:[0,1]
	v_pk_mul_f32 v[30:31], v[26:27], v[24:25]
	v_cmp_neq_f32_e32 vcc, s21, v62
	v_pk_fma_f32 v[32:33], v[24:25], v[26:27], v[30:31] neg_lo:[0,0,1] neg_hi:[0,0,1]
	v_cmp_lt_f32_e64 s[0:1], |v63|, s23
	v_pk_fma_f32 v[32:33], v[24:25], v[22:23], v[32:33]
	s_nop 0
	v_pk_add_f32 v[34:35], v[30:31], v[32:33]
	s_nop 0
	v_pk_add_f32 v[52:53], v[20:21], v[34:35] neg_lo:[0,1] neg_hi:[0,1]
	v_pk_add_f32 v[30:31], v[34:35], v[30:31] neg_lo:[0,1] neg_hi:[0,1]
	v_pk_add_f32 v[20:21], v[20:21], v[52:53] neg_lo:[0,1] neg_hi:[0,1]
	s_nop 0
	v_pk_add_f32 v[20:21], v[20:21], v[34:35] neg_lo:[0,1] neg_hi:[0,1]
	s_nop 0
	v_pk_add_f32 v[6:7], v[6:7], v[20:21]
	v_pk_add_f32 v[20:21], v[30:31], v[32:33] neg_lo:[0,1] neg_hi:[0,1]
	s_nop 0
	v_pk_add_f32 v[6:7], v[20:21], v[6:7]
	s_nop 0
	v_pk_add_f32 v[20:21], v[52:53], v[6:7]
	s_nop 0
	v_pk_mul_f32 v[30:31], v[28:29], v[20:21]
	s_nop 0
	v_pk_mul_f32 v[32:33], v[26:27], v[30:31]
	s_nop 0
	v_pk_fma_f32 v[26:27], v[30:31], v[26:27], v[32:33] neg_lo:[0,0,1] neg_hi:[0,0,1]
	s_nop 0
	v_pk_fma_f32 v[22:23], v[30:31], v[22:23], v[26:27]
	v_pk_add_f32 v[26:27], v[52:53], v[20:21] neg_lo:[0,1] neg_hi:[0,1]
	s_nop 0
	v_pk_add_f32 v[6:7], v[6:7], v[26:27]
	v_pk_add_f32 v[26:27], v[32:33], v[22:23]
	s_nop 0
	v_pk_add_f32 v[34:35], v[20:21], v[26:27] neg_lo:[0,1] neg_hi:[0,1]
	v_pk_add_f32 v[32:33], v[26:27], v[32:33] neg_lo:[0,1] neg_hi:[0,1]
	v_pk_add_f32 v[20:21], v[20:21], v[34:35] neg_lo:[0,1] neg_hi:[0,1]
	s_nop 0
	v_pk_add_f32 v[20:21], v[20:21], v[26:27] neg_lo:[0,1] neg_hi:[0,1]
	s_nop 0
	v_pk_add_f32 v[6:7], v[6:7], v[20:21]
	v_pk_add_f32 v[20:21], v[32:33], v[22:23] neg_lo:[0,1] neg_hi:[0,1]
	s_nop 0
	v_pk_add_f32 v[6:7], v[20:21], v[6:7]
	v_pk_add_f32 v[20:21], v[24:25], v[30:31]
	v_pk_add_f32 v[6:7], v[34:35], v[6:7]
	v_pk_add_f32 v[22:23], v[20:21], v[24:25] neg_lo:[0,1] neg_hi:[0,1]
	v_pk_mul_f32 v[6:7], v[28:29], v[6:7]
	v_pk_add_f32 v[22:23], v[30:31], v[22:23] neg_lo:[0,1] neg_hi:[0,1]
	s_nop 0
	v_pk_add_f32 v[6:7], v[22:23], v[6:7]
	s_nop 0
	v_pk_add_f32 v[22:23], v[20:21], v[6:7]
	s_nop 0
	v_pk_mul_f32 v[24:25], v[22:23], v[22:23]
	v_pk_add_f32 v[20:21], v[22:23], v[20:21] neg_lo:[0,1] neg_hi:[0,1]
	v_pk_fma_f32 v[26:27], v[24:25], s[48:49], v[12:13] op_sel_hi:[1,0,0]
	v_pk_add_f32 v[6:7], v[6:7], v[20:21] neg_lo:[0,1] neg_hi:[0,1]
	v_ldexp_f32 v20, v22, 1
	v_pk_fma_f32 v[26:27], v[24:25], v[26:27], s[50:51] op_sel_hi:[1,1,0]
	v_ldexp_f32 v21, v23, 1
	v_pk_mul_f32 v[22:23], v[22:23], v[24:25]
	v_cvt_f32_i32_e32 v25, v55
	v_cvt_f32_i32_e32 v24, v54
	v_pk_mul_f32 v[22:23], v[22:23], v[26:27]
	v_ldexp_f32 v29, v7, 1
	v_pk_add_f32 v[26:27], v[20:21], v[22:23]
	v_pk_mul_f32 v[30:31], v[24:25], s[52:53] op_sel_hi:[1,0]
	v_pk_add_f32 v[20:21], v[26:27], v[20:21] neg_lo:[0,1] neg_hi:[0,1]
	v_pk_fma_f32 v[32:33], v[24:25], s[52:53], v[30:31] op_sel_hi:[1,0,1] neg_lo:[0,0,1] neg_hi:[0,0,1]
	v_pk_add_f32 v[20:21], v[22:23], v[20:21] neg_lo:[0,1] neg_hi:[0,1]
	v_pk_fma_f32 v[24:25], v[24:25], s[54:55], v[32:33] op_sel_hi:[1,0,1]
	v_ldexp_f32 v6, v6, 1
	v_mov_b32_e32 v22, v30
	v_mov_b32_e32 v23, v21
	v_mov_b32_e32 v28, v24
	v_mov_b32_e32 v7, v29
	v_pk_add_f32 v[22:23], v[22:23], v[28:29]
	v_pk_add_f32 v[28:29], v[6:7], v[20:21]
	v_mov_b32_e32 v21, v27
	v_mov_b32_e32 v7, v29
	v_pk_add_f32 v[32:33], v[30:31], v[24:25]
	v_pk_add_f32 v[6:7], v[6:7], v[20:21]
	v_pk_add_f32 v[20:21], v[26:27], v[28:29]
	v_mov_b32_e32 v58, v26
	v_pk_add_f32 v[34:35], v[32:33], v[20:21]
	v_mov_b32_e32 v56, v20
	v_mov_b32_e32 v57, v35
	v_mov_b32_e32 v59, v33
	v_pk_add_f32 v[56:57], v[56:57], v[58:59] neg_lo:[0,1] neg_hi:[0,1]
	v_mov_b32_e32 v52, v34
	v_mov_b32_e32 v53, v33
	v_mov_b32_e32 v54, v32
	v_mov_b32_e32 v55, v31
	v_mov_b32_e32 v58, v32
	v_mov_b32_e32 v59, v35
	v_mov_b32_e32 v31, v57
	v_pk_add_f32 v[52:53], v[52:53], v[54:55] neg_lo:[0,1] neg_hi:[0,1]
	v_mov_b32_e32 v54, v20
	v_mov_b32_e32 v55, v25
	v_pk_add_f32 v[30:31], v[58:59], v[30:31] neg_lo:[0,1] neg_hi:[0,1]
	v_pk_add_f32 v[54:55], v[54:55], v[52:53] neg_lo:[0,1] neg_hi:[0,1]
	v_mov_b32_e32 v58, v30
	v_mov_b32_e32 v59, v53
	v_mov_b32_e32 v60, v34
	v_mov_b32_e32 v61, v21
	v_mov_b32_e32 v53, v27
	v_pk_add_f32 v[58:59], v[24:25], v[58:59] neg_lo:[0,1] neg_hi:[0,1]
	v_pk_add_f32 v[52:53], v[60:61], v[52:53] neg_lo:[0,1] neg_hi:[0,1]
	v_mov_b32_e32 v25, v33
	v_pk_add_f32 v[22:23], v[22:23], v[52:53] neg_lo:[0,1] neg_hi:[0,1]
	v_pk_add_f32 v[24:25], v[24:25], v[30:31] neg_lo:[0,1] neg_hi:[0,1]
	v_pk_add_f32 v[6:7], v[6:7], v[56:57] neg_lo:[0,1] neg_hi:[0,1]
	v_pk_add_f32 v[20:21], v[20:21], v[26:27] neg_lo:[0,1] neg_hi:[0,1]
	v_pk_add_f32 v[26:27], v[6:7], v[24:25]
	v_mov_b32_e32 v25, v55
	v_mov_b32_e32 v7, v23
	v_pk_add_f32 v[20:21], v[28:29], v[20:21] neg_lo:[0,1] neg_hi:[0,1]
	v_pk_add_f32 v[28:29], v[54:55], v[22:23]
	v_pk_add_f32 v[6:7], v[24:25], v[6:7]
	v_mov_b32_e32 v22, v26
	v_pk_add_f32 v[6:7], v[6:7], v[58:59] neg_lo:[0,1] neg_hi:[0,1]
	v_mov_b32_e32 v23, v29
	v_pk_add_f32 v[22:23], v[22:23], v[6:7] neg_lo:[0,1] neg_hi:[0,1]
	v_pk_add_f32 v[6:7], v[20:21], v[6:7] neg_lo:[0,1] neg_hi:[0,1]
	v_pk_add_f32 v[22:23], v[24:25], v[22:23] neg_lo:[0,1] neg_hi:[0,1]
	v_pk_add_f32 v[20:21], v[28:29], v[26:27]
	v_pk_add_f32 v[6:7], v[6:7], v[22:23]
	v_pk_add_f32 v[22:23], v[34:35], v[20:21]
	s_nop 0
	v_pk_add_f32 v[24:25], v[22:23], v[34:35] neg_lo:[0,1] neg_hi:[0,1]
	s_nop 0
	v_pk_add_f32 v[20:21], v[20:21], v[24:25] neg_lo:[0,1] neg_hi:[0,1]
	s_nop 0
	v_pk_add_f32 v[6:7], v[6:7], v[20:21]
	s_nop 0
	v_pk_add_f32 v[6:7], v[22:23], v[6:7]
	s_nop 0
	v_cndmask_b32_e32 v6, v214, v6, vcc
	v_cmp_neq_f32_e32 vcc, s21, v63
	s_nop 1
	v_cndmask_b32_e32 v7, v214, v7, vcc
	v_cmp_ngt_f32_e32 vcc, -1.0, v63
	s_nop 1
	v_cndmask_b32_e32 v7, v215, v7, vcc
	v_cmp_ngt_f32_e32 vcc, -1.0, v62
	s_nop 1
	v_cndmask_b32_e32 v6, v215, v6, vcc
	v_cmp_neq_f32_e32 vcc, -1.0, v62
	s_nop 1
	v_cndmask_b32_e32 v6, v216, v6, vcc
	v_cmp_neq_f32_e32 vcc, -1.0, v63
	s_nop 1
	v_cndmask_b32_e32 v7, v216, v7, vcc
	v_cmp_lt_f32_e64 vcc, |v62|, s23
	v_cndmask_b32_e64 v7, v7, v63, s[0:1]
	s_mov_b64 s[0:1], 0x1200
	v_cndmask_b32_e32 v6, v6, v62, vcc
	v_pk_add_f32 v[6:7], v[18:19], v[6:7] neg_lo:[0,1] neg_hi:[0,1]
	v_lshl_add_u64 v[18:19], v[14:15], 0, s[0:1]
	global_store_dwordx4 v[16:17], v[8:11], off offset:512
	global_store_dwordx4 v[18:19], v[4:7], off offset:16
	s_nop 1
	v_mov_b32_e32 v4, v164
	v_mov_b32_e32 v5, v165
	v_mov_b32_e32 v6, v166
	v_mov_b32_e32 v7, v167
	v_fmamk_f32 v8, v44, 0x3c800000, v4
	v_min_f32_e32 v4, 0, v8
	v_mul_f32_e64 v8, |v8|, s6
	v_exp_f32_e32 v60, v8
	v_fmamk_f32 v19, v45, 0x3c800000, v5
	v_min_f32_e32 v5, 0, v19
	v_mul_f32_e64 v19, |v19|, s6
	v_exp_f32_e32 v61, v19
	v_add_f32_e32 v10, 1.0, v60
	v_add_f32_e32 v8, -1.0, v10
	v_sub_f32_e32 v9, v8, v10
	v_add_f32_e32 v9, 1.0, v9
	v_sub_f32_e32 v8, v60, v8
	v_add_f32_e32 v19, 1.0, v61
	v_add_f32_e32 v11, v8, v9
	v_frexp_mant_f32_e32 v8, v10
	v_add_f32_e32 v21, -1.0, v19
	v_cmp_gt_f32_e32 vcc, s7, v8
	v_cvt_f64_f32_e32 v[8:9], v10
	v_sub_f32_e32 v22, v21, v19
	v_frexp_exp_i32_f64_e32 v8, v[8:9]
	v_add_f32_e32 v22, 1.0, v22
	v_sub_f32_e32 v21, v61, v21
	v_subbrev_co_u32_e32 v52, vcc, 0, v8, vcc
	v_add_f32_e32 v21, v21, v22
	v_frexp_mant_f32_e32 v22, v19
	v_cmp_gt_f32_e32 vcc, s7, v22
	v_cvt_f64_f32_e32 v[22:23], v19
	v_frexp_exp_i32_f64_e32 v22, v[22:23]
	v_subbrev_co_u32_e32 v53, vcc, 0, v22, vcc
	v_sub_u32_e32 v8, 0, v52
	v_sub_u32_e32 v22, 0, v53
	v_ldexp_f32 v18, v10, v8
	v_ldexp_f32 v19, v19, v22
	v_ldexp_f32 v21, v21, v22
	v_pk_add_f32 v[22:23], v[18:19], 1.0 op_sel_hi:[1,0]
	v_ldexp_f32 v20, v11, v8
	v_pk_add_f32 v[24:25], v[22:23], -1.0 op_sel_hi:[1,0]
	v_pk_add_f32 v[30:31], v[18:19], -1.0 op_sel_hi:[1,0]
	v_pk_add_f32 v[24:25], v[18:19], v[24:25] neg_lo:[0,1] neg_hi:[0,1]
	v_pk_add_f32 v[32:33], v[30:31], 1.0 op_sel_hi:[1,0]
	v_pk_add_f32 v[24:25], v[20:21], v[24:25]
	v_pk_add_f32 v[18:19], v[18:19], v[32:33] neg_lo:[0,1] neg_hi:[0,1]
	v_pk_add_f32 v[26:27], v[22:23], v[24:25]
	v_pk_add_f32 v[18:19], v[20:21], v[18:19]
	v_rcp_f32_e32 v28, v26
	v_rcp_f32_e32 v29, v27
	v_pk_add_f32 v[20:21], v[30:31], v[18:19]
	v_pk_add_f32 v[22:23], v[26:27], v[22:23] neg_lo:[0,1] neg_hi:[0,1]
	v_pk_add_f32 v[30:31], v[20:21], v[30:31] neg_lo:[0,1] neg_hi:[0,1]
	v_pk_add_f32 v[22:23], v[24:25], v[22:23] neg_lo:[0,1] neg_hi:[0,1]
	v_pk_mul_f32 v[24:25], v[20:21], v[28:29]
	v_pk_add_f32 v[18:19], v[18:19], v[30:31] neg_lo:[0,1] neg_hi:[0,1]
	v_pk_mul_f32 v[30:31], v[26:27], v[24:25]
	v_cmp_neq_f32_e32 vcc, s21, v60
	v_pk_fma_f32 v[32:33], v[24:25], v[26:27], v[30:31] neg_lo:[0,0,1] neg_hi:[0,0,1]
	v_pk_fma_f32 v[32:33], v[24:25], v[22:23], v[32:33]
	v_cmp_lt_f32_e64 s[0:1], |v61|, s23
	v_pk_add_f32 v[34:35], v[30:31], v[32:33]
	v_fmamk_f32 v6, v46, 0x3c800000, v6
	v_pk_add_f32 v[44:45], v[20:21], v[34:35] neg_lo:[0,1] neg_hi:[0,1]
	v_pk_add_f32 v[30:31], v[34:35], v[30:31] neg_lo:[0,1] neg_hi:[0,1]
	v_pk_add_f32 v[20:21], v[20:21], v[44:45] neg_lo:[0,1] neg_hi:[0,1]
	v_fmac_f32_e32 v7, 0x3c800000, v47
	v_pk_add_f32 v[20:21], v[20:21], v[34:35] neg_lo:[0,1] neg_hi:[0,1]
	v_mov_b32_e32 v8, v244
	v_mov_b32_e32 v9, v245
	v_mov_b32_e32 v10, v246
	v_mov_b32_e32 v11, v247
	v_pk_fma_f32 v[8:9], v[48:49], s[28:29], v[8:9] op_sel_hi:[1,0,1]
	v_pk_add_f32 v[18:19], v[18:19], v[20:21]
	v_pk_add_f32 v[20:21], v[30:31], v[32:33] neg_lo:[0,1] neg_hi:[0,1]
	v_pk_fma_f32 v[10:11], v[50:51], s[28:29], v[10:11] op_sel_hi:[1,0,1]
	v_pk_add_f32 v[18:19], v[20:21], v[18:19]
	s_nop 0
	v_pk_add_f32 v[20:21], v[44:45], v[18:19]
	s_nop 0
	v_pk_mul_f32 v[30:31], v[28:29], v[20:21]
	s_nop 0
	v_pk_mul_f32 v[32:33], v[26:27], v[30:31]
	s_nop 0
	v_pk_fma_f32 v[26:27], v[30:31], v[26:27], v[32:33] neg_lo:[0,0,1] neg_hi:[0,0,1]
	s_nop 0
	v_pk_fma_f32 v[22:23], v[30:31], v[22:23], v[26:27]
	v_pk_add_f32 v[26:27], v[44:45], v[20:21] neg_lo:[0,1] neg_hi:[0,1]
	s_nop 0
	v_pk_add_f32 v[18:19], v[18:19], v[26:27]
	v_pk_add_f32 v[26:27], v[32:33], v[22:23]
	s_nop 0
	v_pk_add_f32 v[34:35], v[20:21], v[26:27] neg_lo:[0,1] neg_hi:[0,1]
	v_pk_add_f32 v[32:33], v[26:27], v[32:33] neg_lo:[0,1] neg_hi:[0,1]
	v_pk_add_f32 v[20:21], v[20:21], v[34:35] neg_lo:[0,1] neg_hi:[0,1]
	s_nop 0
	v_pk_add_f32 v[20:21], v[20:21], v[26:27] neg_lo:[0,1] neg_hi:[0,1]
	s_nop 0
	v_pk_add_f32 v[18:19], v[18:19], v[20:21]
	v_pk_add_f32 v[20:21], v[32:33], v[22:23] neg_lo:[0,1] neg_hi:[0,1]
	s_nop 0
	v_pk_add_f32 v[18:19], v[20:21], v[18:19]
	v_pk_add_f32 v[20:21], v[24:25], v[30:31]
	v_pk_add_f32 v[18:19], v[34:35], v[18:19]
	v_pk_add_f32 v[22:23], v[20:21], v[24:25] neg_lo:[0,1] neg_hi:[0,1]
	v_pk_mul_f32 v[18:19], v[28:29], v[18:19]
	v_pk_add_f32 v[22:23], v[30:31], v[22:23] neg_lo:[0,1] neg_hi:[0,1]
	s_nop 0
	v_pk_add_f32 v[18:19], v[22:23], v[18:19]
	s_nop 0
	v_pk_add_f32 v[22:23], v[20:21], v[18:19]
	s_nop 0
	v_pk_mul_f32 v[24:25], v[22:23], v[22:23]
	v_pk_add_f32 v[20:21], v[22:23], v[20:21] neg_lo:[0,1] neg_hi:[0,1]
	v_pk_fma_f32 v[26:27], v[24:25], s[48:49], v[12:13] op_sel_hi:[1,0,0]
	v_pk_add_f32 v[18:19], v[18:19], v[20:21] neg_lo:[0,1] neg_hi:[0,1]
	v_ldexp_f32 v20, v22, 1
	v_pk_fma_f32 v[26:27], v[24:25], v[26:27], s[50:51] op_sel_hi:[1,1,0]
	v_ldexp_f32 v21, v23, 1
	v_pk_mul_f32 v[22:23], v[22:23], v[24:25]
	v_cvt_f32_i32_e32 v25, v53
	v_cvt_f32_i32_e32 v24, v52
	v_pk_mul_f32 v[22:23], v[22:23], v[26:27]
	v_ldexp_f32 v29, v19, 1
	v_pk_add_f32 v[26:27], v[20:21], v[22:23]
	v_pk_mul_f32 v[30:31], v[24:25], s[52:53] op_sel_hi:[1,0]
	v_pk_add_f32 v[20:21], v[26:27], v[20:21] neg_lo:[0,1] neg_hi:[0,1]
	v_pk_fma_f32 v[32:33], v[24:25], s[52:53], v[30:31] op_sel_hi:[1,0,1] neg_lo:[0,0,1] neg_hi:[0,0,1]
	v_pk_add_f32 v[20:21], v[22:23], v[20:21] neg_lo:[0,1] neg_hi:[0,1]
	v_pk_fma_f32 v[24:25], v[24:25], s[54:55], v[32:33] op_sel_hi:[1,0,1]
	v_ldexp_f32 v18, v18, 1
	v_mov_b32_e32 v22, v30
	v_mov_b32_e32 v23, v21
	v_mov_b32_e32 v28, v24
	v_mov_b32_e32 v19, v29
	v_pk_add_f32 v[22:23], v[22:23], v[28:29]
	v_pk_add_f32 v[28:29], v[18:19], v[20:21]
	v_mov_b32_e32 v21, v27
	v_mov_b32_e32 v19, v29
	v_pk_add_f32 v[32:33], v[30:31], v[24:25]
	v_pk_add_f32 v[18:19], v[18:19], v[20:21]
	v_pk_add_f32 v[20:21], v[26:27], v[28:29]
	v_mov_b32_e32 v56, v26
	v_pk_add_f32 v[34:35], v[32:33], v[20:21]
	v_mov_b32_e32 v54, v20
	v_mov_b32_e32 v55, v35
	v_mov_b32_e32 v57, v33
	v_pk_add_f32 v[54:55], v[54:55], v[56:57] neg_lo:[0,1] neg_hi:[0,1]
	v_mov_b32_e32 v44, v34
	v_mov_b32_e32 v45, v33
	v_mov_b32_e32 v52, v32
	v_mov_b32_e32 v53, v31
	v_mov_b32_e32 v56, v32
	v_mov_b32_e32 v57, v35
	v_mov_b32_e32 v31, v55
	v_pk_add_f32 v[44:45], v[44:45], v[52:53] neg_lo:[0,1] neg_hi:[0,1]
	v_mov_b32_e32 v52, v20
	v_mov_b32_e32 v53, v25
	v_pk_add_f32 v[30:31], v[56:57], v[30:31] neg_lo:[0,1] neg_hi:[0,1]
	v_pk_add_f32 v[52:53], v[52:53], v[44:45] neg_lo:[0,1] neg_hi:[0,1]
	v_mov_b32_e32 v56, v30
	v_mov_b32_e32 v57, v45
	v_mov_b32_e32 v58, v34
	v_mov_b32_e32 v59, v21
	v_mov_b32_e32 v45, v27
	v_pk_add_f32 v[56:57], v[24:25], v[56:57] neg_lo:[0,1] neg_hi:[0,1]
	v_pk_add_f32 v[44:45], v[58:59], v[44:45] neg_lo:[0,1] neg_hi:[0,1]
	v_mov_b32_e32 v25, v33
	v_pk_add_f32 v[22:23], v[22:23], v[44:45] neg_lo:[0,1] neg_hi:[0,1]
	v_pk_add_f32 v[24:25], v[24:25], v[30:31] neg_lo:[0,1] neg_hi:[0,1]
	v_pk_add_f32 v[18:19], v[18:19], v[54:55] neg_lo:[0,1] neg_hi:[0,1]
	v_pk_add_f32 v[20:21], v[20:21], v[26:27] neg_lo:[0,1] neg_hi:[0,1]
	v_pk_add_f32 v[26:27], v[18:19], v[24:25]
	v_mov_b32_e32 v25, v53
	v_mov_b32_e32 v19, v23
	v_pk_add_f32 v[20:21], v[28:29], v[20:21] neg_lo:[0,1] neg_hi:[0,1]
	v_pk_add_f32 v[28:29], v[52:53], v[22:23]
	v_pk_add_f32 v[18:19], v[24:25], v[18:19]
	v_mov_b32_e32 v22, v26
	v_pk_add_f32 v[18:19], v[18:19], v[56:57] neg_lo:[0,1] neg_hi:[0,1]
	v_mov_b32_e32 v23, v29
	v_pk_add_f32 v[22:23], v[22:23], v[18:19] neg_lo:[0,1] neg_hi:[0,1]
	v_pk_add_f32 v[18:19], v[20:21], v[18:19] neg_lo:[0,1] neg_hi:[0,1]
	v_pk_add_f32 v[22:23], v[24:25], v[22:23] neg_lo:[0,1] neg_hi:[0,1]
	v_pk_add_f32 v[20:21], v[28:29], v[26:27]
	v_pk_add_f32 v[18:19], v[18:19], v[22:23]
	v_pk_add_f32 v[22:23], v[34:35], v[20:21]
	s_nop 0
	v_pk_add_f32 v[24:25], v[22:23], v[34:35] neg_lo:[0,1] neg_hi:[0,1]
	s_nop 0
	v_pk_add_f32 v[20:21], v[20:21], v[24:25] neg_lo:[0,1] neg_hi:[0,1]
	s_nop 0
	v_pk_add_f32 v[18:19], v[18:19], v[20:21]
	s_nop 0
	v_pk_add_f32 v[18:19], v[22:23], v[18:19]
	s_nop 0
	v_cndmask_b32_e32 v18, v214, v18, vcc
	v_cmp_neq_f32_e32 vcc, s21, v61
	s_nop 1
	v_cndmask_b32_e32 v19, v214, v19, vcc
	v_cmp_ngt_f32_e32 vcc, -1.0, v61
	s_nop 1
	v_cndmask_b32_e32 v19, v215, v19, vcc
	v_cmp_ngt_f32_e32 vcc, -1.0, v60
	s_nop 1
	v_cndmask_b32_e32 v18, v215, v18, vcc
	v_cmp_neq_f32_e32 vcc, -1.0, v60
	s_nop 1
	v_cndmask_b32_e32 v18, v216, v18, vcc
	v_cmp_neq_f32_e32 vcc, -1.0, v61
	s_nop 1
	v_cndmask_b32_e32 v19, v216, v19, vcc
	v_cmp_lt_f32_e64 vcc, |v60|, s23
	v_cndmask_b32_e64 v19, v19, v61, s[0:1]
	s_nop 0
	v_cndmask_b32_e32 v18, v18, v60, vcc
	v_pk_add_f32 v[4:5], v[4:5], v[18:19] neg_lo:[0,1] neg_hi:[0,1]
	v_min_f32_e32 v18, 0, v6
	v_mul_f32_e64 v6, |v6|, s6
	v_exp_f32_e32 v54, v6
	s_nop 0
	v_add_f32_e32 v6, 1.0, v54
	v_add_f32_e32 v19, -1.0, v6
	v_sub_f32_e32 v20, v19, v6
	v_add_f32_e32 v20, 1.0, v20
	v_sub_f32_e32 v19, v54, v19
	v_add_f32_e32 v19, v19, v20
	v_frexp_mant_f32_e32 v20, v6
	v_cmp_gt_f32_e32 vcc, s7, v20
	v_cvt_f64_f32_e32 v[20:21], v6
	v_frexp_exp_i32_f64_e32 v20, v[20:21]
	v_subbrev_co_u32_e32 v46, vcc, 0, v20, vcc
	v_sub_u32_e32 v20, 0, v46
	v_ldexp_f32 v6, v6, v20
	v_ldexp_f32 v20, v19, v20
	v_min_f32_e32 v19, 0, v7
	v_mul_f32_e64 v7, |v7|, s6
	v_exp_f32_e32 v55, v7
	s_nop 0
	v_add_f32_e32 v7, 1.0, v55
	v_add_f32_e32 v21, -1.0, v7
	v_sub_f32_e32 v22, v21, v7
	v_add_f32_e32 v22, 1.0, v22
	v_sub_f32_e32 v21, v55, v21
	v_add_f32_e32 v21, v21, v22
	v_frexp_mant_f32_e32 v22, v7
	v_cmp_gt_f32_e32 vcc, s7, v22
	v_cvt_f64_f32_e32 v[22:23], v7
	v_frexp_exp_i32_f64_e32 v22, v[22:23]
	v_subbrev_co_u32_e32 v47, vcc, 0, v22, vcc
	v_sub_u32_e32 v22, 0, v47
	v_ldexp_f32 v7, v7, v22
	v_ldexp_f32 v21, v21, v22
	v_pk_add_f32 v[22:23], v[6:7], 1.0 op_sel_hi:[1,0]
	v_pk_add_f32 v[30:31], v[6:7], -1.0 op_sel_hi:[1,0]
	v_pk_add_f32 v[24:25], v[22:23], -1.0 op_sel_hi:[1,0]
	v_pk_add_f32 v[32:33], v[30:31], 1.0 op_sel_hi:[1,0]
	v_pk_add_f32 v[24:25], v[6:7], v[24:25] neg_lo:[0,1] neg_hi:[0,1]
	v_pk_add_f32 v[6:7], v[6:7], v[32:33] neg_lo:[0,1] neg_hi:[0,1]
	v_pk_add_f32 v[24:25], v[20:21], v[24:25]
	v_pk_add_f32 v[6:7], v[20:21], v[6:7]
	v_pk_add_f32 v[26:27], v[22:23], v[24:25]
	v_pk_add_f32 v[20:21], v[30:31], v[6:7]
	v_rcp_f32_e32 v28, v26
	v_rcp_f32_e32 v29, v27
	v_pk_add_f32 v[22:23], v[26:27], v[22:23] neg_lo:[0,1] neg_hi:[0,1]
	v_pk_add_f32 v[30:31], v[20:21], v[30:31] neg_lo:[0,1] neg_hi:[0,1]
	v_pk_add_f32 v[22:23], v[24:25], v[22:23] neg_lo:[0,1] neg_hi:[0,1]
	v_pk_mul_f32 v[24:25], v[20:21], v[28:29]
	v_pk_add_f32 v[6:7], v[6:7], v[30:31] neg_lo:[0,1] neg_hi:[0,1]
	v_pk_mul_f32 v[30:31], v[26:27], v[24:25]
	v_cmp_neq_f32_e32 vcc, s21, v54
	v_pk_fma_f32 v[32:33], v[24:25], v[26:27], v[30:31] neg_lo:[0,0,1] neg_hi:[0,0,1]
	v_cmp_lt_f32_e64 s[0:1], |v55|, s23
	v_pk_fma_f32 v[32:33], v[24:25], v[22:23], v[32:33]
	s_nop 0
	v_pk_add_f32 v[34:35], v[30:31], v[32:33]
	s_nop 0
	v_pk_add_f32 v[44:45], v[20:21], v[34:35] neg_lo:[0,1] neg_hi:[0,1]
	v_pk_add_f32 v[30:31], v[34:35], v[30:31] neg_lo:[0,1] neg_hi:[0,1]
	v_pk_add_f32 v[20:21], v[20:21], v[44:45] neg_lo:[0,1] neg_hi:[0,1]
	s_nop 0
	v_pk_add_f32 v[20:21], v[20:21], v[34:35] neg_lo:[0,1] neg_hi:[0,1]
	s_nop 0
	v_pk_add_f32 v[6:7], v[6:7], v[20:21]
	v_pk_add_f32 v[20:21], v[30:31], v[32:33] neg_lo:[0,1] neg_hi:[0,1]
	s_nop 0
	v_pk_add_f32 v[6:7], v[20:21], v[6:7]
	s_nop 0
	v_pk_add_f32 v[20:21], v[44:45], v[6:7]
	s_nop 0
	v_pk_mul_f32 v[30:31], v[28:29], v[20:21]
	s_nop 0
	v_pk_mul_f32 v[32:33], v[26:27], v[30:31]
	s_nop 0
	v_pk_fma_f32 v[26:27], v[30:31], v[26:27], v[32:33] neg_lo:[0,0,1] neg_hi:[0,0,1]
	s_nop 0
	v_pk_fma_f32 v[22:23], v[30:31], v[22:23], v[26:27]
	v_pk_add_f32 v[26:27], v[44:45], v[20:21] neg_lo:[0,1] neg_hi:[0,1]
	s_nop 0
	v_pk_add_f32 v[6:7], v[6:7], v[26:27]
	v_pk_add_f32 v[26:27], v[32:33], v[22:23]
	s_nop 0
	v_pk_add_f32 v[34:35], v[20:21], v[26:27] neg_lo:[0,1] neg_hi:[0,1]
	v_pk_add_f32 v[32:33], v[26:27], v[32:33] neg_lo:[0,1] neg_hi:[0,1]
	v_pk_add_f32 v[20:21], v[20:21], v[34:35] neg_lo:[0,1] neg_hi:[0,1]
	s_nop 0
	v_pk_add_f32 v[20:21], v[20:21], v[26:27] neg_lo:[0,1] neg_hi:[0,1]
	s_nop 0
	v_pk_add_f32 v[6:7], v[6:7], v[20:21]
	v_pk_add_f32 v[20:21], v[32:33], v[22:23] neg_lo:[0,1] neg_hi:[0,1]
	s_nop 0
	v_pk_add_f32 v[6:7], v[20:21], v[6:7]
	v_pk_add_f32 v[20:21], v[24:25], v[30:31]
	v_pk_add_f32 v[6:7], v[34:35], v[6:7]
	v_pk_add_f32 v[22:23], v[20:21], v[24:25] neg_lo:[0,1] neg_hi:[0,1]
	v_pk_mul_f32 v[6:7], v[28:29], v[6:7]
	v_pk_add_f32 v[22:23], v[30:31], v[22:23] neg_lo:[0,1] neg_hi:[0,1]
	s_nop 0
	v_pk_add_f32 v[6:7], v[22:23], v[6:7]
	s_nop 0
	v_pk_add_f32 v[22:23], v[20:21], v[6:7]
	s_nop 0
	v_pk_mul_f32 v[24:25], v[22:23], v[22:23]
	v_pk_add_f32 v[20:21], v[22:23], v[20:21] neg_lo:[0,1] neg_hi:[0,1]
	v_pk_fma_f32 v[26:27], v[24:25], s[48:49], v[12:13] op_sel_hi:[1,0,0]
	v_pk_add_f32 v[6:7], v[6:7], v[20:21] neg_lo:[0,1] neg_hi:[0,1]
	v_ldexp_f32 v20, v22, 1
	v_pk_fma_f32 v[26:27], v[24:25], v[26:27], s[50:51] op_sel_hi:[1,1,0]
	v_ldexp_f32 v21, v23, 1
	v_pk_mul_f32 v[22:23], v[22:23], v[24:25]
	v_cvt_f32_i32_e32 v25, v47
	v_cvt_f32_i32_e32 v24, v46
	v_pk_mul_f32 v[22:23], v[22:23], v[26:27]
	v_ldexp_f32 v29, v7, 1
	v_pk_add_f32 v[26:27], v[20:21], v[22:23]
	v_pk_mul_f32 v[30:31], v[24:25], s[52:53] op_sel_hi:[1,0]
	v_pk_add_f32 v[20:21], v[26:27], v[20:21] neg_lo:[0,1] neg_hi:[0,1]
	v_pk_fma_f32 v[32:33], v[24:25], s[52:53], v[30:31] op_sel_hi:[1,0,1] neg_lo:[0,0,1] neg_hi:[0,0,1]
	v_pk_add_f32 v[20:21], v[22:23], v[20:21] neg_lo:[0,1] neg_hi:[0,1]
	v_pk_fma_f32 v[24:25], v[24:25], s[54:55], v[32:33] op_sel_hi:[1,0,1]
	v_ldexp_f32 v6, v6, 1
	v_mov_b32_e32 v22, v30
	v_mov_b32_e32 v23, v21
	v_mov_b32_e32 v28, v24
	v_mov_b32_e32 v7, v29
	v_pk_add_f32 v[22:23], v[22:23], v[28:29]
	v_pk_add_f32 v[28:29], v[6:7], v[20:21]
	v_mov_b32_e32 v21, v27
	v_mov_b32_e32 v7, v29
	v_pk_add_f32 v[32:33], v[30:31], v[24:25]
	v_pk_add_f32 v[6:7], v[6:7], v[20:21]
	v_pk_add_f32 v[20:21], v[26:27], v[28:29]
	v_mov_b32_e32 v50, v26
	v_pk_add_f32 v[34:35], v[32:33], v[20:21]
	v_mov_b32_e32 v48, v20
	v_mov_b32_e32 v49, v35
	v_mov_b32_e32 v51, v33
	v_pk_add_f32 v[48:49], v[48:49], v[50:51] neg_lo:[0,1] neg_hi:[0,1]
	v_mov_b32_e32 v44, v34
	v_mov_b32_e32 v45, v33
	v_mov_b32_e32 v46, v32
	v_mov_b32_e32 v47, v31
	v_mov_b32_e32 v50, v32
	v_mov_b32_e32 v51, v35
	v_mov_b32_e32 v31, v49
	v_pk_add_f32 v[44:45], v[44:45], v[46:47] neg_lo:[0,1] neg_hi:[0,1]
	v_mov_b32_e32 v46, v20
	v_mov_b32_e32 v47, v25
	v_pk_add_f32 v[30:31], v[50:51], v[30:31] neg_lo:[0,1] neg_hi:[0,1]
	v_pk_add_f32 v[46:47], v[46:47], v[44:45] neg_lo:[0,1] neg_hi:[0,1]
	v_mov_b32_e32 v50, v30
	v_mov_b32_e32 v51, v45
	v_mov_b32_e32 v52, v34
	v_mov_b32_e32 v53, v21
	v_mov_b32_e32 v45, v27
	v_pk_add_f32 v[50:51], v[24:25], v[50:51] neg_lo:[0,1] neg_hi:[0,1]
	v_pk_add_f32 v[44:45], v[52:53], v[44:45] neg_lo:[0,1] neg_hi:[0,1]
	v_mov_b32_e32 v25, v33
	v_pk_add_f32 v[22:23], v[22:23], v[44:45] neg_lo:[0,1] neg_hi:[0,1]
	v_pk_add_f32 v[24:25], v[24:25], v[30:31] neg_lo:[0,1] neg_hi:[0,1]
	v_pk_add_f32 v[6:7], v[6:7], v[48:49] neg_lo:[0,1] neg_hi:[0,1]
	v_pk_add_f32 v[20:21], v[20:21], v[26:27] neg_lo:[0,1] neg_hi:[0,1]
	v_pk_add_f32 v[26:27], v[6:7], v[24:25]
	v_mov_b32_e32 v25, v47
	v_mov_b32_e32 v7, v23
	v_pk_add_f32 v[20:21], v[28:29], v[20:21] neg_lo:[0,1] neg_hi:[0,1]
	v_pk_add_f32 v[28:29], v[46:47], v[22:23]
	v_pk_add_f32 v[6:7], v[24:25], v[6:7]
	v_mov_b32_e32 v22, v26
	v_pk_add_f32 v[6:7], v[6:7], v[50:51] neg_lo:[0,1] neg_hi:[0,1]
	v_mov_b32_e32 v23, v29
	v_pk_add_f32 v[22:23], v[22:23], v[6:7] neg_lo:[0,1] neg_hi:[0,1]
	v_pk_add_f32 v[6:7], v[20:21], v[6:7] neg_lo:[0,1] neg_hi:[0,1]
	v_pk_add_f32 v[22:23], v[24:25], v[22:23] neg_lo:[0,1] neg_hi:[0,1]
	v_pk_add_f32 v[20:21], v[28:29], v[26:27]
	v_pk_add_f32 v[6:7], v[6:7], v[22:23]
	v_pk_add_f32 v[22:23], v[34:35], v[20:21]
	s_nop 0
	v_pk_add_f32 v[24:25], v[22:23], v[34:35] neg_lo:[0,1] neg_hi:[0,1]
	s_nop 0
	v_pk_add_f32 v[20:21], v[20:21], v[24:25] neg_lo:[0,1] neg_hi:[0,1]
	s_nop 0
	v_pk_add_f32 v[6:7], v[6:7], v[20:21]
	s_nop 0
	v_pk_add_f32 v[6:7], v[22:23], v[6:7]
	s_nop 0
	v_cndmask_b32_e32 v6, v214, v6, vcc
	v_cmp_neq_f32_e32 vcc, s21, v55
	s_nop 1
	v_cndmask_b32_e32 v7, v214, v7, vcc
	v_cmp_ngt_f32_e32 vcc, -1.0, v55
	s_nop 1
	v_cndmask_b32_e32 v7, v215, v7, vcc
	v_cmp_ngt_f32_e32 vcc, -1.0, v54
	s_nop 1
	v_cndmask_b32_e32 v6, v215, v6, vcc
	v_cmp_neq_f32_e32 vcc, -1.0, v54
	s_nop 1
	v_cndmask_b32_e32 v6, v216, v6, vcc
	v_cmp_neq_f32_e32 vcc, -1.0, v55
	s_nop 1
	v_cndmask_b32_e32 v7, v216, v7, vcc
	v_cmp_lt_f32_e64 vcc, |v54|, s23
	v_cndmask_b32_e64 v7, v7, v55, s[0:1]
	s_mov_b64 s[0:1], 0x1400
	v_cndmask_b32_e32 v6, v6, v54, vcc
	v_pk_add_f32 v[6:7], v[18:19], v[6:7] neg_lo:[0,1] neg_hi:[0,1]
	v_lshl_add_u64 v[18:19], v[14:15], 0, s[0:1]
	global_store_dwordx4 v[16:17], v[8:11], off offset:1024
	global_store_dwordx4 v[18:19], v[4:7], off offset:16
	s_nop 1
	v_mov_b32_e32 v4, v164
	v_mov_b32_e32 v5, v165
	v_mov_b32_e32 v6, v166
	v_mov_b32_e32 v7, v167
	v_fmamk_f32 v8, v36, 0x3c800000, v4
	v_min_f32_e32 v4, 0, v8
	v_mul_f32_e64 v8, |v8|, s6
	v_exp_f32_e32 v52, v8
	v_fmamk_f32 v19, v37, 0x3c800000, v5
	v_min_f32_e32 v5, 0, v19
	v_mul_f32_e64 v19, |v19|, s6
	v_exp_f32_e32 v53, v19
	v_add_f32_e32 v10, 1.0, v52
	v_add_f32_e32 v8, -1.0, v10
	v_sub_f32_e32 v9, v8, v10
	v_add_f32_e32 v9, 1.0, v9
	v_sub_f32_e32 v8, v52, v8
	v_add_f32_e32 v19, 1.0, v53
	v_add_f32_e32 v11, v8, v9
	v_frexp_mant_f32_e32 v8, v10
	v_add_f32_e32 v21, -1.0, v19
	v_cmp_gt_f32_e32 vcc, s7, v8
	v_cvt_f64_f32_e32 v[8:9], v10
	v_sub_f32_e32 v22, v21, v19
	v_frexp_exp_i32_f64_e32 v8, v[8:9]
	v_add_f32_e32 v22, 1.0, v22
	v_sub_f32_e32 v21, v53, v21
	v_subbrev_co_u32_e32 v44, vcc, 0, v8, vcc
	v_add_f32_e32 v21, v21, v22
	v_frexp_mant_f32_e32 v22, v19
	v_cmp_gt_f32_e32 vcc, s7, v22
	v_cvt_f64_f32_e32 v[22:23], v19
	v_frexp_exp_i32_f64_e32 v22, v[22:23]
	v_subbrev_co_u32_e32 v45, vcc, 0, v22, vcc
	v_sub_u32_e32 v8, 0, v44
	v_sub_u32_e32 v22, 0, v45
	v_ldexp_f32 v18, v10, v8
	v_ldexp_f32 v19, v19, v22
	v_ldexp_f32 v21, v21, v22
	v_pk_add_f32 v[22:23], v[18:19], 1.0 op_sel_hi:[1,0]
	v_ldexp_f32 v20, v11, v8
	v_pk_add_f32 v[24:25], v[22:23], -1.0 op_sel_hi:[1,0]
	v_pk_add_f32 v[30:31], v[18:19], -1.0 op_sel_hi:[1,0]
	v_pk_add_f32 v[24:25], v[18:19], v[24:25] neg_lo:[0,1] neg_hi:[0,1]
	v_pk_add_f32 v[32:33], v[30:31], 1.0 op_sel_hi:[1,0]
	v_pk_add_f32 v[24:25], v[20:21], v[24:25]
	v_pk_add_f32 v[18:19], v[18:19], v[32:33] neg_lo:[0,1] neg_hi:[0,1]
	v_pk_add_f32 v[26:27], v[22:23], v[24:25]
	v_pk_add_f32 v[18:19], v[20:21], v[18:19]
	v_rcp_f32_e32 v28, v26
	v_rcp_f32_e32 v29, v27
	v_pk_add_f32 v[20:21], v[30:31], v[18:19]
	v_pk_add_f32 v[22:23], v[26:27], v[22:23] neg_lo:[0,1] neg_hi:[0,1]
	v_pk_add_f32 v[30:31], v[20:21], v[30:31] neg_lo:[0,1] neg_hi:[0,1]
	v_pk_add_f32 v[22:23], v[24:25], v[22:23] neg_lo:[0,1] neg_hi:[0,1]
	v_pk_mul_f32 v[24:25], v[20:21], v[28:29]
	v_pk_add_f32 v[18:19], v[18:19], v[30:31] neg_lo:[0,1] neg_hi:[0,1]
	v_pk_mul_f32 v[30:31], v[26:27], v[24:25]
	v_cmp_neq_f32_e32 vcc, s21, v52
	v_pk_fma_f32 v[32:33], v[24:25], v[26:27], v[30:31] neg_lo:[0,0,1] neg_hi:[0,0,1]
	v_pk_fma_f32 v[32:33], v[24:25], v[22:23], v[32:33]
	v_cmp_lt_f32_e64 s[0:1], |v53|, s23
	v_pk_add_f32 v[34:35], v[30:31], v[32:33]
	v_fmamk_f32 v6, v38, 0x3c800000, v6
	v_pk_add_f32 v[36:37], v[20:21], v[34:35] neg_lo:[0,1] neg_hi:[0,1]
	v_pk_add_f32 v[30:31], v[34:35], v[30:31] neg_lo:[0,1] neg_hi:[0,1]
	v_pk_add_f32 v[20:21], v[20:21], v[36:37] neg_lo:[0,1] neg_hi:[0,1]
	v_fmac_f32_e32 v7, 0x3c800000, v39
	v_pk_add_f32 v[20:21], v[20:21], v[34:35] neg_lo:[0,1] neg_hi:[0,1]
	v_mov_b32_e32 v8, v244
	v_mov_b32_e32 v9, v245
	v_mov_b32_e32 v10, v246
	v_mov_b32_e32 v11, v247
	v_pk_fma_f32 v[8:9], v[40:41], s[28:29], v[8:9] op_sel_hi:[1,0,1]
	v_pk_add_f32 v[18:19], v[18:19], v[20:21]
	v_pk_add_f32 v[20:21], v[30:31], v[32:33] neg_lo:[0,1] neg_hi:[0,1]
	v_pk_fma_f32 v[10:11], v[42:43], s[28:29], v[10:11] op_sel_hi:[1,0,1]
	v_pk_add_f32 v[18:19], v[20:21], v[18:19]
	s_nop 0
	v_pk_add_f32 v[20:21], v[36:37], v[18:19]
	s_nop 0
	v_pk_mul_f32 v[30:31], v[28:29], v[20:21]
	s_nop 0
	v_pk_mul_f32 v[32:33], v[26:27], v[30:31]
	s_nop 0
	v_pk_fma_f32 v[26:27], v[30:31], v[26:27], v[32:33] neg_lo:[0,0,1] neg_hi:[0,0,1]
	s_nop 0
	v_pk_fma_f32 v[22:23], v[30:31], v[22:23], v[26:27]
	v_pk_add_f32 v[26:27], v[36:37], v[20:21] neg_lo:[0,1] neg_hi:[0,1]
	s_nop 0
	v_pk_add_f32 v[18:19], v[18:19], v[26:27]
	v_pk_add_f32 v[26:27], v[32:33], v[22:23]
	s_nop 0
	v_pk_add_f32 v[34:35], v[20:21], v[26:27] neg_lo:[0,1] neg_hi:[0,1]
	v_pk_add_f32 v[32:33], v[26:27], v[32:33] neg_lo:[0,1] neg_hi:[0,1]
	v_pk_add_f32 v[20:21], v[20:21], v[34:35] neg_lo:[0,1] neg_hi:[0,1]
	s_nop 0
	v_pk_add_f32 v[20:21], v[20:21], v[26:27] neg_lo:[0,1] neg_hi:[0,1]
	s_nop 0
	v_pk_add_f32 v[18:19], v[18:19], v[20:21]
	v_pk_add_f32 v[20:21], v[32:33], v[22:23] neg_lo:[0,1] neg_hi:[0,1]
	s_nop 0
	v_pk_add_f32 v[18:19], v[20:21], v[18:19]
	v_pk_add_f32 v[20:21], v[24:25], v[30:31]
	v_pk_add_f32 v[18:19], v[34:35], v[18:19]
	v_pk_add_f32 v[22:23], v[20:21], v[24:25] neg_lo:[0,1] neg_hi:[0,1]
	v_pk_mul_f32 v[18:19], v[28:29], v[18:19]
	v_pk_add_f32 v[22:23], v[30:31], v[22:23] neg_lo:[0,1] neg_hi:[0,1]
	s_nop 0
	v_pk_add_f32 v[18:19], v[22:23], v[18:19]
	s_nop 0
	v_pk_add_f32 v[22:23], v[20:21], v[18:19]
	s_nop 0
	v_pk_mul_f32 v[24:25], v[22:23], v[22:23]
	v_pk_add_f32 v[20:21], v[22:23], v[20:21] neg_lo:[0,1] neg_hi:[0,1]
	v_pk_fma_f32 v[26:27], v[24:25], s[48:49], v[12:13] op_sel_hi:[1,0,0]
	v_pk_add_f32 v[18:19], v[18:19], v[20:21] neg_lo:[0,1] neg_hi:[0,1]
	v_ldexp_f32 v20, v22, 1
	v_pk_fma_f32 v[26:27], v[24:25], v[26:27], s[50:51] op_sel_hi:[1,1,0]
	v_ldexp_f32 v21, v23, 1
	v_pk_mul_f32 v[22:23], v[22:23], v[24:25]
	v_cvt_f32_i32_e32 v25, v45
	v_cvt_f32_i32_e32 v24, v44
	v_pk_mul_f32 v[22:23], v[22:23], v[26:27]
	v_ldexp_f32 v29, v19, 1
	v_pk_add_f32 v[26:27], v[20:21], v[22:23]
	v_pk_mul_f32 v[30:31], v[24:25], s[52:53] op_sel_hi:[1,0]
	v_pk_add_f32 v[20:21], v[26:27], v[20:21] neg_lo:[0,1] neg_hi:[0,1]
	v_pk_fma_f32 v[32:33], v[24:25], s[52:53], v[30:31] op_sel_hi:[1,0,1] neg_lo:[0,0,1] neg_hi:[0,0,1]
	v_pk_add_f32 v[20:21], v[22:23], v[20:21] neg_lo:[0,1] neg_hi:[0,1]
	v_pk_fma_f32 v[24:25], v[24:25], s[54:55], v[32:33] op_sel_hi:[1,0,1]
	v_ldexp_f32 v18, v18, 1
	v_mov_b32_e32 v22, v30
	v_mov_b32_e32 v23, v21
	v_mov_b32_e32 v28, v24
	v_mov_b32_e32 v19, v29
	v_pk_add_f32 v[22:23], v[22:23], v[28:29]
	v_pk_add_f32 v[28:29], v[18:19], v[20:21]
	v_mov_b32_e32 v21, v27
	v_mov_b32_e32 v19, v29
	v_pk_add_f32 v[32:33], v[30:31], v[24:25]
	v_pk_add_f32 v[18:19], v[18:19], v[20:21]
	v_pk_add_f32 v[20:21], v[26:27], v[28:29]
	v_mov_b32_e32 v48, v26
	v_pk_add_f32 v[34:35], v[32:33], v[20:21]
	v_mov_b32_e32 v46, v20
	v_mov_b32_e32 v47, v35
	v_mov_b32_e32 v49, v33
	v_pk_add_f32 v[46:47], v[46:47], v[48:49] neg_lo:[0,1] neg_hi:[0,1]
	v_mov_b32_e32 v36, v34
	v_mov_b32_e32 v37, v33
	v_mov_b32_e32 v44, v32
	v_mov_b32_e32 v45, v31
	v_mov_b32_e32 v48, v32
	v_mov_b32_e32 v49, v35
	v_mov_b32_e32 v31, v47
	v_pk_add_f32 v[36:37], v[36:37], v[44:45] neg_lo:[0,1] neg_hi:[0,1]
	v_mov_b32_e32 v44, v20
	v_mov_b32_e32 v45, v25
	v_pk_add_f32 v[30:31], v[48:49], v[30:31] neg_lo:[0,1] neg_hi:[0,1]
	v_pk_add_f32 v[44:45], v[44:45], v[36:37] neg_lo:[0,1] neg_hi:[0,1]
	v_mov_b32_e32 v48, v30
	v_mov_b32_e32 v49, v37
	v_mov_b32_e32 v50, v34
	v_mov_b32_e32 v51, v21
	v_mov_b32_e32 v37, v27
	v_pk_add_f32 v[48:49], v[24:25], v[48:49] neg_lo:[0,1] neg_hi:[0,1]
	v_pk_add_f32 v[36:37], v[50:51], v[36:37] neg_lo:[0,1] neg_hi:[0,1]
	v_mov_b32_e32 v25, v33
	v_pk_add_f32 v[22:23], v[22:23], v[36:37] neg_lo:[0,1] neg_hi:[0,1]
	v_pk_add_f32 v[24:25], v[24:25], v[30:31] neg_lo:[0,1] neg_hi:[0,1]
	v_pk_add_f32 v[18:19], v[18:19], v[46:47] neg_lo:[0,1] neg_hi:[0,1]
	v_pk_add_f32 v[20:21], v[20:21], v[26:27] neg_lo:[0,1] neg_hi:[0,1]
	v_pk_add_f32 v[26:27], v[18:19], v[24:25]
	v_mov_b32_e32 v25, v45
	v_mov_b32_e32 v19, v23
	v_pk_add_f32 v[20:21], v[28:29], v[20:21] neg_lo:[0,1] neg_hi:[0,1]
	v_pk_add_f32 v[28:29], v[44:45], v[22:23]
	v_pk_add_f32 v[18:19], v[24:25], v[18:19]
	v_mov_b32_e32 v22, v26
	v_pk_add_f32 v[18:19], v[18:19], v[48:49] neg_lo:[0,1] neg_hi:[0,1]
	v_mov_b32_e32 v23, v29
	v_pk_add_f32 v[22:23], v[22:23], v[18:19] neg_lo:[0,1] neg_hi:[0,1]
	v_pk_add_f32 v[18:19], v[20:21], v[18:19] neg_lo:[0,1] neg_hi:[0,1]
	v_pk_add_f32 v[22:23], v[24:25], v[22:23] neg_lo:[0,1] neg_hi:[0,1]
	v_pk_add_f32 v[20:21], v[28:29], v[26:27]
	v_pk_add_f32 v[18:19], v[18:19], v[22:23]
	v_pk_add_f32 v[22:23], v[34:35], v[20:21]
	s_nop 0
	v_pk_add_f32 v[24:25], v[22:23], v[34:35] neg_lo:[0,1] neg_hi:[0,1]
	s_nop 0
	v_pk_add_f32 v[20:21], v[20:21], v[24:25] neg_lo:[0,1] neg_hi:[0,1]
	s_nop 0
	v_pk_add_f32 v[18:19], v[18:19], v[20:21]
	s_nop 0
	v_pk_add_f32 v[18:19], v[22:23], v[18:19]
	s_nop 0
	v_cndmask_b32_e32 v18, v214, v18, vcc
	v_cmp_neq_f32_e32 vcc, s21, v53
	s_nop 1
	v_cndmask_b32_e32 v19, v214, v19, vcc
	v_cmp_ngt_f32_e32 vcc, -1.0, v53
	s_nop 1
	v_cndmask_b32_e32 v19, v215, v19, vcc
	v_cmp_ngt_f32_e32 vcc, -1.0, v52
	s_nop 1
	v_cndmask_b32_e32 v18, v215, v18, vcc
	v_cmp_neq_f32_e32 vcc, -1.0, v52
	s_nop 1
	v_cndmask_b32_e32 v18, v216, v18, vcc
	v_cmp_neq_f32_e32 vcc, -1.0, v53
	s_nop 1
	v_cndmask_b32_e32 v19, v216, v19, vcc
	v_cmp_lt_f32_e64 vcc, |v52|, s23
	v_cndmask_b32_e64 v19, v19, v53, s[0:1]
	s_nop 0
	v_cndmask_b32_e32 v18, v18, v52, vcc
	v_pk_add_f32 v[4:5], v[4:5], v[18:19] neg_lo:[0,1] neg_hi:[0,1]
	v_min_f32_e32 v18, 0, v6
	v_mul_f32_e64 v6, |v6|, s6
	v_exp_f32_e32 v44, v6
	s_nop 0
	v_add_f32_e32 v6, 1.0, v44
	v_add_f32_e32 v19, -1.0, v6
	v_sub_f32_e32 v20, v19, v6
	v_add_f32_e32 v20, 1.0, v20
	v_sub_f32_e32 v19, v44, v19
	v_add_f32_e32 v19, v19, v20
	v_frexp_mant_f32_e32 v20, v6
	v_cmp_gt_f32_e32 vcc, s7, v20
	v_cvt_f64_f32_e32 v[20:21], v6
	v_frexp_exp_i32_f64_e32 v20, v[20:21]
	v_subbrev_co_u32_e32 v38, vcc, 0, v20, vcc
	v_sub_u32_e32 v20, 0, v38
	v_ldexp_f32 v6, v6, v20
	v_ldexp_f32 v20, v19, v20
	v_min_f32_e32 v19, 0, v7
	v_mul_f32_e64 v7, |v7|, s6
	v_exp_f32_e32 v45, v7
	s_nop 0
	v_add_f32_e32 v7, 1.0, v45
	v_add_f32_e32 v21, -1.0, v7
	v_sub_f32_e32 v22, v21, v7
	v_add_f32_e32 v22, 1.0, v22
	v_sub_f32_e32 v21, v45, v21
	v_add_f32_e32 v21, v21, v22
	v_frexp_mant_f32_e32 v22, v7
	v_cmp_gt_f32_e32 vcc, s7, v22
	v_cvt_f64_f32_e32 v[22:23], v7
	v_frexp_exp_i32_f64_e32 v22, v[22:23]
	v_subbrev_co_u32_e32 v39, vcc, 0, v22, vcc
	v_sub_u32_e32 v22, 0, v39
	v_ldexp_f32 v7, v7, v22
	v_ldexp_f32 v21, v21, v22
	v_pk_add_f32 v[22:23], v[6:7], 1.0 op_sel_hi:[1,0]
	v_pk_add_f32 v[30:31], v[6:7], -1.0 op_sel_hi:[1,0]
	v_pk_add_f32 v[24:25], v[22:23], -1.0 op_sel_hi:[1,0]
	v_pk_add_f32 v[32:33], v[30:31], 1.0 op_sel_hi:[1,0]
	v_pk_add_f32 v[24:25], v[6:7], v[24:25] neg_lo:[0,1] neg_hi:[0,1]
	v_pk_add_f32 v[6:7], v[6:7], v[32:33] neg_lo:[0,1] neg_hi:[0,1]
	v_pk_add_f32 v[24:25], v[20:21], v[24:25]
	v_pk_add_f32 v[6:7], v[20:21], v[6:7]
	v_pk_add_f32 v[26:27], v[22:23], v[24:25]
	v_pk_add_f32 v[20:21], v[30:31], v[6:7]
	v_rcp_f32_e32 v28, v26
	v_rcp_f32_e32 v29, v27
	v_pk_add_f32 v[22:23], v[26:27], v[22:23] neg_lo:[0,1] neg_hi:[0,1]
	v_pk_add_f32 v[30:31], v[20:21], v[30:31] neg_lo:[0,1] neg_hi:[0,1]
	v_pk_add_f32 v[22:23], v[24:25], v[22:23] neg_lo:[0,1] neg_hi:[0,1]
	v_pk_mul_f32 v[24:25], v[20:21], v[28:29]
	v_pk_add_f32 v[6:7], v[6:7], v[30:31] neg_lo:[0,1] neg_hi:[0,1]
	v_pk_mul_f32 v[30:31], v[26:27], v[24:25]
	v_cmp_neq_f32_e32 vcc, s21, v44
	v_pk_fma_f32 v[32:33], v[24:25], v[26:27], v[30:31] neg_lo:[0,0,1] neg_hi:[0,0,1]
	v_cmp_lt_f32_e64 s[0:1], |v45|, s23
	v_pk_fma_f32 v[32:33], v[24:25], v[22:23], v[32:33]
	s_nop 0
	v_pk_add_f32 v[34:35], v[30:31], v[32:33]
	s_nop 0
	v_pk_add_f32 v[36:37], v[20:21], v[34:35] neg_lo:[0,1] neg_hi:[0,1]
	v_pk_add_f32 v[30:31], v[34:35], v[30:31] neg_lo:[0,1] neg_hi:[0,1]
	v_pk_add_f32 v[20:21], v[20:21], v[36:37] neg_lo:[0,1] neg_hi:[0,1]
	s_nop 0
	v_pk_add_f32 v[20:21], v[20:21], v[34:35] neg_lo:[0,1] neg_hi:[0,1]
	s_nop 0
	v_pk_add_f32 v[6:7], v[6:7], v[20:21]
	v_pk_add_f32 v[20:21], v[30:31], v[32:33] neg_lo:[0,1] neg_hi:[0,1]
	s_nop 0
	v_pk_add_f32 v[6:7], v[20:21], v[6:7]
	s_nop 0
	v_pk_add_f32 v[20:21], v[36:37], v[6:7]
	s_nop 0
	v_pk_mul_f32 v[30:31], v[28:29], v[20:21]
	s_nop 0
	v_pk_mul_f32 v[32:33], v[26:27], v[30:31]
	s_nop 0
	v_pk_fma_f32 v[26:27], v[30:31], v[26:27], v[32:33] neg_lo:[0,0,1] neg_hi:[0,0,1]
	s_nop 0
	v_pk_fma_f32 v[22:23], v[30:31], v[22:23], v[26:27]
	v_pk_add_f32 v[26:27], v[36:37], v[20:21] neg_lo:[0,1] neg_hi:[0,1]
	s_nop 0
	v_pk_add_f32 v[6:7], v[6:7], v[26:27]
	v_pk_add_f32 v[26:27], v[32:33], v[22:23]
	s_nop 0
	v_pk_add_f32 v[34:35], v[20:21], v[26:27] neg_lo:[0,1] neg_hi:[0,1]
	v_pk_add_f32 v[32:33], v[26:27], v[32:33] neg_lo:[0,1] neg_hi:[0,1]
	v_pk_add_f32 v[20:21], v[20:21], v[34:35] neg_lo:[0,1] neg_hi:[0,1]
	s_nop 0
	v_pk_add_f32 v[20:21], v[20:21], v[26:27] neg_lo:[0,1] neg_hi:[0,1]
	s_nop 0
	v_pk_add_f32 v[6:7], v[6:7], v[20:21]
	v_pk_add_f32 v[20:21], v[32:33], v[22:23] neg_lo:[0,1] neg_hi:[0,1]
	s_nop 0
	v_pk_add_f32 v[6:7], v[20:21], v[6:7]
	v_pk_add_f32 v[20:21], v[24:25], v[30:31]
	v_pk_add_f32 v[6:7], v[34:35], v[6:7]
	v_pk_add_f32 v[22:23], v[20:21], v[24:25] neg_lo:[0,1] neg_hi:[0,1]
	v_pk_mul_f32 v[6:7], v[28:29], v[6:7]
	v_pk_add_f32 v[22:23], v[30:31], v[22:23] neg_lo:[0,1] neg_hi:[0,1]
	s_nop 0
	v_pk_add_f32 v[6:7], v[22:23], v[6:7]
	s_nop 0
	v_pk_add_f32 v[22:23], v[20:21], v[6:7]
	s_nop 0
	v_pk_mul_f32 v[24:25], v[22:23], v[22:23]
	v_pk_add_f32 v[20:21], v[22:23], v[20:21] neg_lo:[0,1] neg_hi:[0,1]
	v_pk_fma_f32 v[12:13], v[24:25], s[48:49], v[12:13] op_sel_hi:[1,0,0]
	v_pk_add_f32 v[6:7], v[6:7], v[20:21] neg_lo:[0,1] neg_hi:[0,1]
	v_ldexp_f32 v20, v22, 1
	v_pk_fma_f32 v[12:13], v[24:25], v[12:13], s[50:51] op_sel_hi:[1,1,0]
	v_ldexp_f32 v21, v23, 1
	v_pk_mul_f32 v[22:23], v[22:23], v[24:25]
	v_cvt_f32_i32_e32 v25, v39
	v_cvt_f32_i32_e32 v24, v38
	v_pk_mul_f32 v[12:13], v[22:23], v[12:13]
	v_ldexp_f32 v27, v7, 1
	v_pk_add_f32 v[22:23], v[20:21], v[12:13]
	v_pk_mul_f32 v[28:29], v[24:25], s[52:53] op_sel_hi:[1,0]
	v_pk_add_f32 v[20:21], v[22:23], v[20:21] neg_lo:[0,1] neg_hi:[0,1]
	v_pk_fma_f32 v[30:31], v[24:25], s[52:53], v[28:29] op_sel_hi:[1,0,1] neg_lo:[0,0,1] neg_hi:[0,0,1]
	v_pk_add_f32 v[12:13], v[12:13], v[20:21] neg_lo:[0,1] neg_hi:[0,1]
	v_pk_fma_f32 v[24:25], v[24:25], s[54:55], v[30:31] op_sel_hi:[1,0,1]
	v_ldexp_f32 v6, v6, 1
	v_mov_b32_e32 v20, v28
	v_mov_b32_e32 v21, v13
	v_mov_b32_e32 v26, v24
	v_mov_b32_e32 v7, v27
	v_pk_add_f32 v[20:21], v[20:21], v[26:27]
	v_pk_add_f32 v[26:27], v[6:7], v[12:13]
	v_mov_b32_e32 v13, v23
	v_mov_b32_e32 v7, v27
	v_pk_add_f32 v[30:31], v[28:29], v[24:25]
	v_pk_add_f32 v[6:7], v[6:7], v[12:13]
	v_pk_add_f32 v[12:13], v[22:23], v[26:27]
	v_mov_b32_e32 v40, v22
	v_pk_add_f32 v[32:33], v[30:31], v[12:13]
	v_mov_b32_e32 v38, v12
	v_mov_b32_e32 v39, v33
	v_mov_b32_e32 v41, v31
	v_pk_add_f32 v[38:39], v[38:39], v[40:41] neg_lo:[0,1] neg_hi:[0,1]
	v_mov_b32_e32 v34, v32
	v_mov_b32_e32 v35, v31
	v_mov_b32_e32 v36, v30
	v_mov_b32_e32 v37, v29
	v_mov_b32_e32 v40, v30
	v_mov_b32_e32 v41, v33
	v_mov_b32_e32 v29, v39
	v_pk_add_f32 v[34:35], v[34:35], v[36:37] neg_lo:[0,1] neg_hi:[0,1]
	v_mov_b32_e32 v36, v12
	v_mov_b32_e32 v37, v25
	v_pk_add_f32 v[28:29], v[40:41], v[28:29] neg_lo:[0,1] neg_hi:[0,1]
	v_pk_add_f32 v[36:37], v[36:37], v[34:35] neg_lo:[0,1] neg_hi:[0,1]
	v_mov_b32_e32 v40, v28
	v_mov_b32_e32 v41, v35
	v_mov_b32_e32 v42, v32
	v_mov_b32_e32 v43, v13
	v_mov_b32_e32 v35, v23
	v_pk_add_f32 v[40:41], v[24:25], v[40:41] neg_lo:[0,1] neg_hi:[0,1]
	v_pk_add_f32 v[34:35], v[42:43], v[34:35] neg_lo:[0,1] neg_hi:[0,1]
	v_mov_b32_e32 v25, v31
	v_pk_add_f32 v[12:13], v[12:13], v[22:23] neg_lo:[0,1] neg_hi:[0,1]
	v_pk_add_f32 v[20:21], v[20:21], v[34:35] neg_lo:[0,1] neg_hi:[0,1]
	v_pk_add_f32 v[22:23], v[24:25], v[28:29] neg_lo:[0,1] neg_hi:[0,1]
	v_pk_add_f32 v[6:7], v[6:7], v[38:39] neg_lo:[0,1] neg_hi:[0,1]
	v_pk_add_f32 v[12:13], v[26:27], v[12:13] neg_lo:[0,1] neg_hi:[0,1]
	v_pk_add_f32 v[24:25], v[6:7], v[22:23]
	v_mov_b32_e32 v23, v37
	v_mov_b32_e32 v7, v21
	v_pk_add_f32 v[26:27], v[36:37], v[20:21]
	v_pk_add_f32 v[6:7], v[22:23], v[6:7]
	v_mov_b32_e32 v20, v24
	v_pk_add_f32 v[6:7], v[6:7], v[40:41] neg_lo:[0,1] neg_hi:[0,1]
	v_mov_b32_e32 v21, v27
	v_pk_add_f32 v[20:21], v[20:21], v[6:7] neg_lo:[0,1] neg_hi:[0,1]
	v_pk_add_f32 v[6:7], v[12:13], v[6:7] neg_lo:[0,1] neg_hi:[0,1]
	v_pk_add_f32 v[20:21], v[22:23], v[20:21] neg_lo:[0,1] neg_hi:[0,1]
	v_pk_add_f32 v[12:13], v[26:27], v[24:25]
	v_pk_add_f32 v[6:7], v[6:7], v[20:21]
	v_pk_add_f32 v[20:21], v[32:33], v[12:13]
	s_nop 0
	v_pk_add_f32 v[22:23], v[20:21], v[32:33] neg_lo:[0,1] neg_hi:[0,1]
	s_nop 0
	v_pk_add_f32 v[12:13], v[12:13], v[22:23] neg_lo:[0,1] neg_hi:[0,1]
	s_nop 0
	v_pk_add_f32 v[6:7], v[6:7], v[12:13]
	s_nop 0
	v_pk_add_f32 v[6:7], v[20:21], v[6:7]
	s_nop 0
	v_cndmask_b32_e32 v6, v214, v6, vcc
	v_cmp_neq_f32_e32 vcc, s21, v45
	s_nop 1
	v_cndmask_b32_e32 v7, v214, v7, vcc
	v_cmp_ngt_f32_e32 vcc, -1.0, v45
	s_nop 1
	v_cndmask_b32_e32 v7, v215, v7, vcc
	v_cmp_ngt_f32_e32 vcc, -1.0, v44
	s_nop 1
	v_cndmask_b32_e32 v6, v215, v6, vcc
	v_cmp_neq_f32_e32 vcc, -1.0, v44
	s_nop 1
	v_cndmask_b32_e32 v6, v216, v6, vcc
	v_cmp_neq_f32_e32 vcc, -1.0, v45
	s_nop 1
	v_cndmask_b32_e32 v7, v216, v7, vcc
	v_cmp_lt_f32_e64 vcc, |v44|, s23
	v_cndmask_b32_e64 v7, v7, v45, s[0:1]
	s_mov_b64 s[0:1], 0x1600
	v_cndmask_b32_e32 v6, v6, v44, vcc
	v_pk_add_f32 v[6:7], v[18:19], v[6:7] neg_lo:[0,1] neg_hi:[0,1]
	v_lshl_add_u64 v[12:13], v[14:15], 0, s[0:1]
	global_store_dwordx4 v[16:17], v[8:11], off offset:1536
	global_store_dwordx4 v[12:13], v[4:7], off offset:16

.LBB0_864:
	s_cmp_lt_i32 s23, s33
	s_cselect_b64 s[0:1], -1, 0
	s_and_b64 s[0:1], vcc, s[0:1]
	s_and_saveexec_b64 s[20:21], s[0:1]
	s_cbranch_execz .LBB0_863
	s_and_b32 s0, s23, 7
	s_mul_i32 s0, s0, s43
	s_ashr_i32 s1, s23, 3
	s_add_i32 s0, s0, s1
	s_ashr_i32 s0, s0, 3
	s_lshl_b32 s0, s0, 2
	s_add_i32 s0, s0, 0
	s_add_i32 s1, s0, 0x20100
	v_mov_b32_e32 v3, s1
	ds_read_b32 v3, v3
	s_add_i32 s0, s0, 0x20380
	v_mov_b32_e32 v4, s0
	ds_read_b32 v4, v4
	s_waitcnt lgkmcnt(1)
	v_lshlrev_b32_e32 v5, 2, v3
	v_add_u32_e32 v5, 0, v5
	v_add_u32_e32 v5, 0x20600, v5
	ds_read_b32 v5, v5
	s_waitcnt lgkmcnt(1)
	v_add_u32_e32 v4, v4, v172
	s_waitcnt lgkmcnt(0)
	v_cmp_lt_i32_e64 s[0:1], v4, v5
	s_nop 1
	v_cndmask_b32_e64 v4, 0, v4, s[0:1]
	v_lshl_add_u32 v4, v3, 15, v4
	v_ashrrev_i32_e32 v5, 31, v4
	v_lshl_add_u64 v[4:5], v[4:5], 2, s[4:5]
	v_add_u32_e32 v3, s22, v1
	s_nop 0
	v_readfirstlane_b32 s0, v3
	s_mov_b32 m0, s0
	s_nop 0
	global_load_lds_dword v[4:5], off
	s_branch .LBB0_863
.LBB0_866:
	s_add_u32 s40, s18, 0x5400000
	s_addc_u32 s41, s19, 0
	v_mov_b32_e32 v12, v0
	v_readlane_b32 s0, v251, 0
	s_waitcnt vmcnt(0) lgkmcnt(0)
	s_barrier
	s_cmp_ge_i32 s0, s33
	v_readfirstlane_b32 s4, v12
	v_readlane_b32 s1, v251, 1
	s_cbranch_scc1 .LBB0_886
	v_ashrrev_i32_e32 v1, 31, v12
	v_lshrrev_b32_e32 v1, 26, v1
	v_add_u32_e32 v1, v12, v1
	v_ashrrev_i32_e32 v4, 6, v1
	v_bfe_i32 v1, v12, 27, 1
	v_lshlrev_b32_e32 v3, 4, v12
	v_lshrrev_b32_e32 v1, 22, v1
	v_add_u32_e32 v1, v3, v1
	v_and_b32_e32 v1, 0xfffffc00, v1
	v_sub_u32_e32 v1, v3, v1
	v_lshrrev_b32_e32 v5, 4, v1
	v_bitop3_b32 v1, v5, v1, 32 bitop3:0x6c
	v_ashrrev_i32_e32 v6, 31, v1
	v_lshrrev_b32_e32 v6, 26, v6
	v_add_u32_e32 v6, v1, v6
	v_ashrrev_i32_e32 v7, 6, v6
	v_and_b32_e32 v6, 0xc0, v6
	v_sub_u32_e32 v1, v1, v6
	v_lshlrev_b32_e32 v5, 5, v4
	v_ashrrev_i16_sdwa v1, v211, sext(v1) dst_sel:DWORD dst_unused:UNUSED_PAD src0_sel:DWORD src1_sel:BYTE_0
	v_and_b32_e32 v5, 32, v5
	v_bfe_i32 v1, v1, 0, 16
	v_add_u32_e32 v3, 0x2000, v3
	v_add_lshl_u32 v1, v5, v1, 1
	v_ashrrev_i32_e32 v5, 31, v3
	v_lshrrev_b32_e32 v5, 22, v5
	v_add_u32_e32 v5, v3, v5
	v_ashrrev_i32_e32 v5, 10, v5
	v_mul_i32_i24_e32 v6, 0x400, v5
	v_sub_u32_e32 v3, v3, v6
	v_lshrrev_b32_e32 v6, 4, v3
	v_bitop3_b32 v3, v6, v3, 32 bitop3:0x6c
	v_ashrrev_i32_e32 v6, 31, v3
	v_lshrrev_b32_e32 v6, 26, v6
	v_add_u32_e32 v6, v3, v6
	v_lshlrev_b32_e32 v9, 3, v5
	v_ashrrev_i32_e32 v8, 6, v6
	v_and_b32_e32 v9, -16, v9
	v_and_b32_e32 v6, 0xc0, v6
	v_add_u32_e32 v9, v8, v9
	v_and_b32_e32 v8, 3, v8
	s_mov_b32 s20, 0x3fffe0
	v_sub_u32_e32 v3, v3, v6
	v_and_or_b32 v8, v9, s20, v8
	v_lshrrev_b32_e32 v10, 2, v9
	v_lshlrev_b32_e32 v9, 1, v9
	v_lshlrev_b32_e32 v5, 5, v5
	v_ashrrev_i16_sdwa v3, v211, sext(v3) dst_sel:DWORD dst_unused:UNUSED_PAD src0_sel:DWORD src1_sel:BYTE_0
	v_lshlrev_b32_e32 v4, 3, v4
	v_and_b32_e32 v10, 4, v10
	v_and_b32_e32 v9, 24, v9
	v_and_b32_e32 v5, 32, v5
	v_bfe_i32 v3, v3, 0, 16
	s_lshl_b32 s5, s46, 24
	v_and_b32_e32 v4, -16, v4
	v_or3_b32 v8, v8, v10, v9
	v_add_lshl_u32 v3, v5, v3, 1
	s_add_u32 s0, s18, 0xd400000
	v_add_u32_e32 v4, v7, v4
	v_lshl_add_u32 v174, v8, 10, v3
	v_and_b32_e32 v3, 3, v7
	s_addc_u32 s1, s19, 0
	v_and_or_b32 v3, v4, s20, v3
	v_readlane_b32 s20, v251, 59
	s_add_u32 s44, s40, s5
	s_mul_i32 s20, s43, s20
	v_readlane_b32 s21, v251, 60
	s_addc_u32 s45, s41, 0
	s_add_i32 s22, s20, s21
	s_ashr_i32 s30, s22, 3
	s_lshl_b32 s20, s30, 2
	s_add_i32 s20, s20, 0
	s_add_i32 s20, s20, 0x20100
	v_mov_b32_e32 v7, s20
	ds_read_b32 v7, v7
	s_ashr_i32 s5, s4, 6
	s_ashr_i32 s24, s4, 8
	s_lshl_b32 s46, s5, 10
	s_and_b32 s31, s22, 7
	s_waitcnt lgkmcnt(0)
	v_readfirstlane_b32 s20, v7
	s_mul_hi_i32 s21, s20, 0x2aaaaaab
	s_lshr_b32 s23, s21, 31
	s_add_i32 s21, s21, s23
	s_mul_i32 s23, s21, -6
	s_add_i32 s20, s23, s20
	s_cmp_lt_u32 s20, 5
	s_cselect_b32 s23, 1, 2
	s_min_u32 s26, s20, 4
	s_add_i32 s25, s20, 1
	s_add_i32 s26, s26, -1
	s_cmp_lt_i32 s20, 3
	s_cselect_b32 s20, 0, s23
	s_cselect_b32 s23, s25, s26
	s_lshl_b32 s21, s21, 2
	s_or_b32 s20, s20, s21
	s_add_i32 s23, s23, s21
	s_cmp_lt_u32 s31, 4
	s_cselect_b32 s20, s20, s23
	s_ashr_i32 s21, s20, 31
	s_lshl_b32 s22, s22, 18
	v_lshrrev_b32_e32 v5, 2, v4
	v_lshlrev_b32_e32 v6, 1, v4
	s_and_b32 s22, s22, 0xc0000
	s_lshl_b64 s[20:21], s[20:21], 20
	v_and_b32_e32 v5, 4, v5
	v_and_b32_e32 v6, 24, v6
	s_add_u32 s20, s44, s20
	v_or3_b32 v3, v3, v5, v6
	v_lshl_add_u32 v4, v4, 2, 0
	s_addc_u32 s21, s45, s21
	v_lshl_add_u32 v176, v3, 10, v1
	v_mov_b32_e32 v3, 0x7f7f7f7f
	v_add_u32_e32 v173, 0x20800, v4
	s_add_u32 s34, s20, s22
	ds_read2st64_b32 v[4:5], v173 offset1:1
	ds_read2st64_b32 v[8:9], v173 offset0:2 offset1:3
	s_addc_u32 s35, s21, 0
	s_add_i32 s47, s46, 0
	s_add_i32 m0, s47, 0x10000
	s_waitcnt lgkmcnt(1)
	v_lshl_or_b32 v196, v5, 16, v4
	global_load_lds_dwordx4 v176, s[34:35]
	s_add_i32 m0, s47, 0x12000
	s_add_u32 s20, s34, 0x20000
	global_load_lds_dwordx4 v174, s[34:35]
	s_addc_u32 s21, s35, 0
	s_add_i32 m0, s47, 0x14000
	v_lshlrev_b32_e32 v4, 10, v4
	global_load_lds_dwordx4 v176, s[20:21]
	s_add_i32 m0, s47, 0x16000
	v_and_b32_e32 v4, 0x3fffc00, v4
	global_load_lds_dwordx4 v174, s[20:21]
	v_add_u32_e32 v6, v4, v1
	s_mov_b32 m0, s47
	v_bfe_u32 v4, v196, 16, 16
	s_add_i32 s48, s47, 0x2000
	s_waitcnt lgkmcnt(0)
	v_lshlrev_b32_e32 v5, 10, v8
	global_load_lds_dwordx4 v6, s[0:1]
	v_lshl_add_u32 v4, v4, 10, v1
	s_mov_b32 m0, s48
	v_and_b32_e32 v5, 0x3fffc00, v5
	s_add_i32 s49, s47, 0x4000
	v_lshl_or_b32 v170, v9, 16, v8
	global_load_lds_dwordx4 v4, s[0:1]
	v_add_u32_e32 v5, v5, v1
	s_mov_b32 m0, s49
	s_add_i32 s50, s47, 0x6000
	global_load_lds_dwordx4 v5, s[0:1]
	v_bfe_u32 v5, v170, 16, 16
	v_lshl_add_u32 v5, v5, 10, v1
	s_mov_b32 m0, s50
	v_mov_b32_e32 v177, v2
	global_load_lds_dwordx4 v5, s[0:1]
	v_mov_b32_e32 v175, v2
	s_cmp_eq_u32 s24, 1
	s_mov_b32 s73, s53
	v_lshl_add_u64 v[8:9], s[34:35], 0, v[176:177]
	s_cselect_b64 s[20:21], -1, 0
	s_cmp_lg_u32 s24, 1
	v_lshl_add_u64 v[10:11], s[34:35], 0, v[174:175]
	s_cbranch_scc1 .LBB0_869
	s_barrier
